# wave reductions via DPP/permlane swaps instead of ds_bpermute in peer_gather and the conv branch
# speedup vs baseline: 1.0344x; 1.0074x over previous
.LBB0_266:
	s_andn2_saveexec_b64 s[6:7], s[6:7]
	s_or_b64 exec, exec, s[6:7]
	v_mad_i64_i32 v[72:73], s[6:7], v80, s27, v[78:79]
	global_load_dwordx2 v[94:95], v[72:73], off
	global_load_dwordx2 v[96:97], v[72:73], off offset:512
	v_add_u32_e32 v92, 31, v144
	v_mad_i64_i32 v[72:73], s[6:7], v92, s27, v[78:79]
	v_add_u32_e32 v90, 32, v144
	global_load_dwordx2 v[98:99], v[72:73], off
	global_load_dwordx2 v[102:103], v[72:73], off offset:512
	v_mad_i64_i32 v[72:73], s[6:7], v90, s27, v[78:79]
	global_load_dwordx2 v[100:101], v[72:73], off
	global_load_dwordx2 v[104:105], v[72:73], off offset:512
	v_add_u32_e32 v88, 33, v144
	v_add_u32_e32 v86, 34, v144
	v_mad_i64_i32 v[106:107], s[6:7], v88, s27, v[78:79]
	ds_read_b128 v[72:75], v161 offset:34816
	v_mad_i64_i32 v[108:109], s[6:7], v86, s27, v[78:79]
	global_load_dwordx2 v[112:113], v[106:107], off
	global_load_dwordx2 v[114:115], v[106:107], off offset:512
	s_nop 0
	global_load_dwordx2 v[106:107], v[108:109], off
	global_load_dwordx2 v[110:111], v[108:109], off offset:512
	s_mov_b32 s24, 0x3b800000
	v_ashrrev_i32_e32 v81, 31, v80
	v_lshlrev_b64 v[80:81], 11, v[80:81]
	v_ashrrev_i32_e32 v93, 31, v92
	v_lshlrev_b64 v[92:93], 11, v[92:93]
	v_ashrrev_i32_e32 v91, 31, v90
	v_lshlrev_b64 v[90:91], 11, v[90:91]
	v_lshl_add_u64 v[90:91], v[76:77], 0, v[90:91]
	v_add_u32_e32 v160, s86, v160
	s_waitcnt vmcnt(9)
	v_lshlrev_b32_e32 v116, 16, v94
	s_waitcnt vmcnt(8)
	v_lshlrev_b32_e32 v87, 16, v96
	v_and_b32_e32 v89, 0xffff0000, v96
	v_lshlrev_b32_e32 v96, 16, v97
	v_and_b32_e32 v97, 0xffff0000, v97
	v_mul_f32_e32 v118, 0xbfb8aa3b, v96
	v_mul_f32_e32 v119, 0xbfb8aa3b, v97
	v_mul_f32_e32 v87, 0xbfb8aa3b, v87
	v_mul_f32_e32 v89, 0xbfb8aa3b, v89
	v_exp_f32_e32 v118, v118
	v_exp_f32_e32 v119, v119
	v_exp_f32_e32 v87, v87
	v_exp_f32_e32 v89, v89
	s_waitcnt vmcnt(4)
	v_lshlrev_b32_e32 v122, 16, v104
	v_lshlrev_b32_e32 v123, 16, v105
	v_lshlrev_b32_e32 v120, 16, v102
	v_lshlrev_b32_e32 v121, 16, v103
	v_mul_f32_e32 v122, 0xbfb8aa3b, v122
	v_mul_f32_e32 v123, 0xbfb8aa3b, v123
	v_add_f32_e32 v118, 1.0, v118
	v_add_f32_e32 v119, 1.0, v119
	v_mul_f32_e32 v120, 0xbfb8aa3b, v120
	v_mul_f32_e32 v121, 0xbfb8aa3b, v121
	v_exp_f32_e32 v126, v122
	v_exp_f32_e32 v127, v123
	v_add_f32_e32 v87, 1.0, v87
	v_add_f32_e32 v89, 1.0, v89
	v_rcp_f32_e32 v122, v118
	v_rcp_f32_e32 v123, v119
	v_and_b32_e32 v102, 0xffff0000, v102
	v_exp_f32_e32 v124, v120
	v_exp_f32_e32 v125, v121
	v_rcp_f32_e32 v120, v87
	v_rcp_f32_e32 v121, v89
	v_mul_f32_e32 v102, 0xbfb8aa3b, v102
	v_and_b32_e32 v117, 0xffff0000, v94
	v_lshlrev_b32_e32 v94, 16, v95
	v_and_b32_e32 v95, 0xffff0000, v95
	v_exp_f32_e32 v102, v102
	v_and_b32_e32 v103, 0xffff0000, v103
	v_pk_mul_f32 v[94:95], v[122:123], v[94:95]
	v_mul_f32_e32 v103, 0xbfb8aa3b, v103
	s_waitcnt lgkmcnt(0)
	v_pk_fma_f32 v[128:129], v[74:75], v[94:95], v[42:43]
	v_pk_mul_f32 v[42:43], v[120:121], v[116:117]
	v_exp_f32_e32 v103, v103
	v_add_f32_e32 v87, 1.0, v124
	v_pk_fma_f32 v[40:41], v[72:73], v[42:43], v[40:41]
	v_add_f32_e32 v89, 1.0, v102
	v_rcp_f32_e32 v102, v87
	v_add_f32_e32 v87, v40, v41
	v_add_f32_e32 v87, v87, v128
	v_add_f32_e32 v87, v129, v87
	v_add_f32_e32 v119, 1.0, v103
	v_rcp_f32_e32 v103, v89
	v_mov_b32_e32 v89, v87
	s_nop 1
	v_permlane32_swap_b32 v89, v87
	v_and_b32_e32 v104, 0xffff0000, v104
	v_mul_f32_e32 v104, 0xbfb8aa3b, v104
	v_exp_f32_e32 v104, v104
	v_and_b32_e32 v105, 0xffff0000, v105
	s_waitcnt lgkmcnt(0)
	v_add_f32_e32 v87, v87, v89
	v_mul_f32_e32 v105, 0xbfb8aa3b, v105
	v_mov_b32_e32 v89, v87
	s_nop 1
	v_permlane16_swap_b32 v89, v87
	v_exp_f32_e32 v105, v105
	v_add_f32_e32 v104, 1.0, v104
	v_rcp_f32_e32 v131, v119
	v_rcp_f32_e32 v119, v104
	v_add_f32_e32 v104, 1.0, v127
	v_rcp_f32_e32 v122, v104
	v_add_f32_e32 v104, 1.0, v105
	s_waitcnt lgkmcnt(0)
	v_add_f32_e32 v87, v87, v89
	v_rcp_f32_e32 v123, v104
	s_nop 0
	v_mov_b32_dpp v104, v87 row_ror:8 row_mask:0xf bank_mask:0xf
	s_waitcnt vmcnt(2)
	v_lshlrev_b32_e32 v105, 16, v114
	v_mul_f32_e32 v105, 0xbfb8aa3b, v105
	v_and_b32_e32 v114, 0xffff0000, v114
	v_exp_f32_e32 v105, v105
	s_waitcnt lgkmcnt(0)
	v_add_f32_e32 v87, v87, v104
	s_nop 1
	v_mov_b32_dpp v104, v87 row_half_mirror row_mask:0xf bank_mask:0xf
	s_nop 1
	v_mov_b32_dpp v104, v104 quad_perm:[3,2,1,0] row_mask:0xf bank_mask:0xf
	v_mul_f32_e32 v114, 0xbfb8aa3b, v114
	v_exp_f32_e32 v114, v114
	v_add_f32_e32 v105, 1.0, v105
	v_add_f32_e32 v124, 1.0, v126
	s_waitcnt lgkmcnt(0)
	v_add_f32_e32 v87, v87, v104
	s_nop 1
	v_mov_b32_dpp v104, v87 quad_perm:[2,3,0,1] row_mask:0xf bank_mask:0xf
	v_rcp_f32_e32 v126, v105
	v_add_f32_e32 v105, 1.0, v114
	v_rcp_f32_e32 v127, v105
	v_lshlrev_b32_e32 v105, 16, v115
	s_waitcnt lgkmcnt(0)
	v_add_f32_e32 v87, v87, v104
	s_nop 1
	v_mov_b32_dpp v104, v87 quad_perm:[1,0,3,2] row_mask:0xf bank_mask:0xf
	v_add_f32_e32 v118, 1.0, v125
	v_rcp_f32_e32 v130, v118
	v_rcp_f32_e32 v118, v124
	v_lshlrev_b32_e32 v124, 16, v112
	s_waitcnt lgkmcnt(0)
	v_add_f32_e32 v87, v87, v104
	v_mul_f32_e32 v104, 0x3b800000, v87
	v_pk_add_f32 v[132:133], v[40:41], v[104:105] op_sel_hi:[1,0] neg_lo:[0,1] neg_hi:[0,1]
	v_and_b32_e32 v125, 0xffff0000, v112
	v_mul_f32_e32 v112, 0xbfb8aa3b, v105
	v_pk_add_f32 v[104:105], v[128:129], v[104:105] op_sel_hi:[1,0] neg_lo:[0,1] neg_hi:[0,1]
	v_pk_mul_f32 v[40:41], v[132:133], v[132:133]
	v_pk_mul_f32 v[116:117], v[104:105], v[104:105]
	v_add_f32_e32 v40, v40, v41
	v_add_f32_e32 v40, v116, v40
	v_add_f32_e32 v40, v117, v40
	v_mov_b32_e32 v41, v40
	s_nop 1
	v_permlane32_swap_b32 v41, v40
	v_exp_f32_e32 v87, v112
	v_and_b32_e32 v112, 0xffff0000, v115
	v_mul_f32_e32 v112, 0xbfb8aa3b, v112
	v_exp_f32_e32 v112, v112
	s_waitcnt lgkmcnt(0)
	v_add_f32_e32 v40, v40, v41
	ds_bpermute_b32 v41, v185, v40
	v_add_f32_e32 v87, 1.0, v87
	v_rcp_f32_e32 v128, v87
	v_add_f32_e32 v87, 1.0, v112
	v_rcp_f32_e32 v129, v87
	s_waitcnt lgkmcnt(0)
	v_add_f32_e32 v41, v40, v41
	s_nop 1
	v_mov_b32_dpp v116, v41 row_ror:8 row_mask:0xf bank_mask:0xf
	v_add_u32_e32 v40, 35, v144
	v_lshlrev_b32_e32 v114, 16, v113
	v_and_b32_e32 v115, 0xffff0000, v113
	v_mad_i64_i32 v[112:113], s[6:7], v40, s27, v[78:79]
	s_waitcnt lgkmcnt(0)
	v_add_f32_e32 v41, v41, v116
	s_nop 1
	v_mov_b32_dpp v87, v41 row_half_mirror row_mask:0xf bank_mask:0xf
	s_nop 1
	v_mov_b32_dpp v87, v87 quad_perm:[3,2,1,0] row_mask:0xf bank_mask:0xf
	global_load_dwordx2 v[120:121], v[112:113], off
	global_load_dwordx2 v[134:135], v[112:113], off offset:512
	s_waitcnt vmcnt(2)
	v_lshlrev_b32_e32 v112, 16, v110
	v_mul_f32_e32 v112, 0xbfb8aa3b, v112
	v_exp_f32_e32 v113, v112
	s_waitcnt lgkmcnt(0)
	v_add_f32_e32 v41, v41, v87
	s_nop 1
	v_mov_b32_dpp v117, v41 quad_perm:[2,3,0,1] row_mask:0xf bank_mask:0xf
	v_lshlrev_b32_e32 v112, 16, v106
	v_add_f32_e32 v113, 1.0, v113
	v_rcp_f32_e32 v116, v113
	v_and_b32_e32 v113, 0xffff0000, v106
	s_waitcnt lgkmcnt(0)
	v_add_f32_e32 v41, v41, v117
	s_nop 1
	v_mov_b32_dpp v117, v41 quad_perm:[1,0,3,2] row_mask:0xf bank_mask:0xf
	v_and_b32_e32 v106, 0xffff0000, v110
	v_mul_f32_e32 v106, 0xbfb8aa3b, v106
	v_exp_f32_e32 v110, v106
	v_lshlrev_b32_e32 v96, 16, v98
	s_waitcnt lgkmcnt(0)
	v_add_f32_e32 v41, v41, v117
	v_fmamk_f32 v41, v41, 0x3b800000, v191
	v_mul_f32_e32 v106, 0x4b800000, v41
	v_cmp_gt_f32_e32 vcc, s29, v41
	v_and_b32_e32 v97, 0xffff0000, v98
	v_lshlrev_b32_e32 v98, 16, v99
	v_cndmask_b32_e32 v41, v41, v106, vcc
	v_rsq_f32_e32 v41, v41
	v_lshlrev_b32_e32 v106, 16, v111
	v_and_b32_e32 v99, 0xffff0000, v99
	v_mul_f32_e32 v106, 0xbfb8aa3b, v106
	v_pk_mul_f32 v[96:97], v[102:103], v[96:97]
	v_pk_fma_f32 v[36:37], v[68:69], v[42:43], v[36:37]
	v_exp_f32_e32 v138, v106
	v_mul_f32_e32 v106, 0x45800000, v41
	v_pk_mul_f32 v[98:99], v[130:131], v[98:99]
	v_pk_fma_f32 v[38:39], v[70:71], v[94:95], v[38:39]
	v_pk_fma_f32 v[36:37], v[72:73], v[96:97], v[36:37]
	v_cndmask_b32_e32 v106, v41, v106, vcc
	v_pk_fma_f32 v[38:39], v[74:75], v[98:99], v[38:39]
	v_add_f32_e32 v41, v36, v37
	v_add_f32_e32 v41, v41, v38
	v_add_f32_e32 v41, v39, v41
	v_mov_b32_e32 v117, v41
	s_nop 1
	v_permlane32_swap_b32 v117, v41
	v_pk_mul_f32 v[104:105], v[104:105], v[106:107] op_sel_hi:[1,0]
	v_pk_mul_f32 v[102:103], v[132:133], v[106:107] op_sel_hi:[1,0]
	v_pk_fma_f32 v[130:131], v[6:7], v[104:105], v[10:11]
	v_pk_fma_f32 v[102:103], v[4:5], v[102:103], v[8:9]
	s_waitcnt lgkmcnt(0)
	v_add_f32_e32 v41, v41, v117
	v_mov_b32_e32 v104, v41
	s_nop 1
	v_permlane16_swap_b32 v104, v41
	v_mul_f32_e32 v105, 0xbfb8aa3b, v102
	v_mul_f32_e32 v106, 0xbfb8aa3b, v103
	v_exp_f32_e32 v105, v105
	v_exp_f32_e32 v106, v106
	s_waitcnt lgkmcnt(0)
	v_add_f32_e32 v41, v41, v104
	s_nop 1
	v_mov_b32_dpp v117, v41 row_ror:8 row_mask:0xf bank_mask:0xf
	v_add_f32_e32 v104, 1.0, v105
	v_add_f32_e32 v105, 1.0, v106
	v_mul_f32_e32 v132, 0xbfb8aa3b, v131
	v_exp_f32_e32 v133, v132
	s_waitcnt lgkmcnt(0)
	v_add_f32_e32 v41, v41, v117
	s_nop 1
	v_mov_b32_dpp v106, v41 row_half_mirror row_mask:0xf bank_mask:0xf
	s_nop 1
	v_mov_b32_dpp v106, v106 quad_perm:[3,2,1,0] row_mask:0xf bank_mask:0xf
	v_mul_f32_e32 v117, 0xbfb8aa3b, v130
	v_exp_f32_e32 v117, v117
	v_rcp_f32_e32 v104, v104
	v_rcp_f32_e32 v105, v105
	s_waitcnt lgkmcnt(0)
	v_add_f32_e32 v41, v41, v106
	s_nop 1
	v_mov_b32_dpp v106, v41 quad_perm:[2,3,0,1] row_mask:0xf bank_mask:0xf
	v_add_f32_e32 v117, 1.0, v117
	v_rcp_f32_e32 v132, v117
	v_add_f32_e32 v117, 1.0, v133
	v_rcp_f32_e32 v133, v117
	s_waitcnt lgkmcnt(0)
	v_add_f32_e32 v41, v41, v106
	s_nop 1
	v_mov_b32_dpp v106, v41 quad_perm:[1,0,3,2] row_mask:0xf bank_mask:0xf
	v_pk_mul_f32 v[104:105], v[102:103], v[104:105]
	v_pk_mul_f32 v[102:103], v[130:131], v[132:133]
	v_pk_mul_f32 v[130:131], v[104:105], v[104:105]
	v_pk_mul_f32 v[132:133], v[102:103], v[102:103]
	s_waitcnt lgkmcnt(0)
	v_add_f32_e32 v41, v41, v106
	v_mul_f32_e32 v106, 0x3b800000, v41
	v_pk_add_f32 v[140:141], v[36:37], v[106:107] op_sel_hi:[1,0] neg_lo:[0,1] neg_hi:[0,1]
	v_pk_add_f32 v[142:143], v[38:39], v[106:107] op_sel_hi:[1,0] neg_lo:[0,1] neg_hi:[0,1]
	v_pk_mul_f32 v[36:37], v[140:141], v[140:141]
	v_pk_mul_f32 v[38:39], v[142:143], v[142:143]
	v_mov_b32_e32 v136, v36
	v_mov_b32_e32 v137, v130
	v_mov_b32_e32 v130, v37
	v_pk_add_f32 v[36:37], v[136:137], v[130:131]
	v_mov_b32_e32 v130, v38
	v_mov_b32_e32 v131, v132
	v_pk_add_f32 v[36:37], v[130:131], v[36:37]
	v_mov_b32_e32 v132, v39
	v_pk_add_f32 v[36:37], v[132:133], v[36:37]
	ds_bpermute_b32 v39, v184, v37
	ds_bpermute_b32 v38, v184, v36
	v_add_f32_e32 v41, 1.0, v110
	s_waitcnt vmcnt(0)
	v_and_b32_e32 v110, 0xffff0000, v134
	v_rcp_f32_e32 v117, v41
	v_add_f32_e32 v41, 1.0, v138
	s_waitcnt lgkmcnt(0)
	v_pk_add_f32 v[36:37], v[36:37], v[38:39]
	ds_bpermute_b32 v39, v185, v37
	ds_bpermute_b32 v38, v185, v36
	v_mul_f32_e32 v110, 0xbfb8aa3b, v110
	v_rcp_f32_e32 v138, v41
	v_and_b32_e32 v41, 0xffff0000, v111
	v_exp_f32_e32 v111, v110
	s_waitcnt lgkmcnt(0)
	v_pk_add_f32 v[36:37], v[36:37], v[38:39]
	s_nop 1
	v_mov_b32_dpp v39, v37 row_ror:8 row_mask:0xf bank_mask:0xf
	s_nop 0
	v_mov_b32_dpp v38, v36 row_ror:8 row_mask:0xf bank_mask:0xf
	s_mov_b32 s6, 0x358637bd
	v_lshlrev_b32_e32 v132, 16, v107
	v_and_b32_e32 v133, 0xffff0000, v107
	v_lshlrev_b32_e32 v107, 16, v134
	s_waitcnt lgkmcnt(0)
	v_pk_add_f32 v[36:37], v[36:37], v[38:39]
	s_nop 1
	v_mov_b32_dpp v39, v37 row_half_mirror row_mask:0xf bank_mask:0xf
	s_nop 1
	v_mov_b32_dpp v39, v39 quad_perm:[3,2,1,0] row_mask:0xf bank_mask:0xf
	v_mov_b32_dpp v38, v36 row_half_mirror row_mask:0xf bank_mask:0xf
	s_nop 1
	v_mov_b32_dpp v38, v38 quad_perm:[3,2,1,0] row_mask:0xf bank_mask:0xf
	v_mul_f32_e32 v107, 0xbfb8aa3b, v107
	v_lshlrev_b32_e32 v108, 16, v100
	v_and_b32_e32 v109, 0xffff0000, v100
	v_lshlrev_b32_e32 v100, 16, v101
	s_waitcnt lgkmcnt(0)
	v_pk_add_f32 v[36:37], v[36:37], v[38:39]
	s_nop 1
	v_mov_b32_dpp v39, v37 quad_perm:[2,3,0,1] row_mask:0xf bank_mask:0xf
	s_nop 0
	v_mov_b32_dpp v38, v36 quad_perm:[2,3,0,1] row_mask:0xf bank_mask:0xf
	v_and_b32_e32 v101, 0xffff0000, v101
	v_exp_f32_e32 v107, v107
	v_pk_fma_f32 v[34:35], v[66:67], v[94:95], v[34:35]
	v_pk_mul_f32 v[100:101], v[122:123], v[100:101]
	s_waitcnt lgkmcnt(0)
	v_pk_add_f32 v[38:39], v[36:37], v[38:39]
	s_nop 1
	v_mov_b32_dpp v131, v39 quad_perm:[1,0,3,2] row_mask:0xf bank_mask:0xf
	s_nop 0
	v_mov_b32_dpp v130, v38 quad_perm:[1,0,3,2] row_mask:0xf bank_mask:0xf
	v_add_u32_e32 v36, 36, v144
	v_add_f32_e32 v37, 1.0, v111
	v_pk_fma_f32 v[34:35], v[70:71], v[98:99], v[34:35]
	v_pk_fma_f32 v[32:33], v[64:65], v[42:43], v[32:33]
	s_waitcnt lgkmcnt(0)
	v_pk_add_f32 v[130:131], v[38:39], v[130:131]
	v_mov_b64_e32 v[38:39], s[6:7]
	v_pk_fma_f32 v[130:131], v[130:131], s[24:25], v[38:39] op_sel_hi:[1,0,0]
	v_mad_i64_i32 v[152:153], s[6:7], v36, s27, v[78:79]
	v_mul_f32_e32 v111, 0x4b800000, v130
	v_cmp_gt_f32_e32 vcc, s29, v130
	global_load_dwordx2 v[136:137], v[152:153], off
	s_nop 0
	global_load_dwordx2 v[152:153], v[152:153], off offset:512
	v_cndmask_b32_e32 v111, v130, v111, vcc
	v_rsq_f32_e32 v111, v111
	v_pk_fma_f32 v[154:155], v[74:75], v[100:101], v[34:35]
	v_pk_mul_f32 v[34:35], v[118:119], v[108:109]
	v_pk_fma_f32 v[32:33], v[68:69], v[96:97], v[32:33]
	v_add_f32_e32 v107, 1.0, v107
	v_pk_fma_f32 v[32:33], v[72:73], v[34:35], v[32:33]
	v_lshlrev_b32_e32 v106, 16, v120
	v_add_f32_e32 v108, v32, v33
	v_rcp_f32_e32 v110, v107
	v_and_b32_e32 v107, 0xffff0000, v120
	v_mul_f32_e32 v120, 0x45800000, v111
	v_add_f32_e32 v108, v108, v154
	v_cndmask_b32_e32 v120, v111, v120, vcc
	v_add_f32_e32 v111, v155, v108
	v_mov_b32_e32 v122, v111
	s_nop 1
	v_permlane32_swap_b32 v122, v111
	v_pk_mul_f32 v[108:109], v[140:141], v[120:121] op_sel_hi:[1,0]
	v_pk_mul_f32 v[118:119], v[142:143], v[120:121] op_sel_hi:[1,0]
	v_pk_fma_f32 v[108:109], v[4:5], v[108:109], v[8:9]
	v_pk_fma_f32 v[118:119], v[6:7], v[118:119], v[10:11]
	s_waitcnt lgkmcnt(0)
	v_add_f32_e32 v111, v111, v122
	v_mov_b32_e32 v120, v111
	s_nop 1
	v_permlane16_swap_b32 v120, v111
	v_mul_f32_e32 v122, 0xbfb8aa3b, v108
	v_mul_f32_e32 v123, 0xbfb8aa3b, v109
	v_mul_f32_e32 v130, 0xbfb8aa3b, v118
	v_exp_f32_e32 v122, v122
	s_waitcnt lgkmcnt(0)
	v_add_f32_e32 v111, v111, v120
	s_nop 1
	v_mov_b32_dpp v120, v111 row_ror:8 row_mask:0xf bank_mask:0xf
	v_exp_f32_e32 v123, v123
	v_exp_f32_e32 v130, v130
	v_mul_f32_e32 v134, 0xbfb8aa3b, v119
	v_exp_f32_e32 v134, v134
	s_waitcnt lgkmcnt(0)
	v_add_f32_e32 v111, v111, v120
	s_nop 1
	v_mov_b32_dpp v120, v111 row_half_mirror row_mask:0xf bank_mask:0xf
	s_nop 1
	v_mov_b32_dpp v120, v120 quad_perm:[3,2,1,0] row_mask:0xf bank_mask:0xf
	v_add_f32_e32 v122, 1.0, v122
	v_add_f32_e32 v123, 1.0, v123
	v_add_f32_e32 v130, 1.0, v130
	v_rcp_f32_e32 v122, v122
	s_waitcnt lgkmcnt(0)
	v_add_f32_e32 v111, v111, v120
	s_nop 1
	v_mov_b32_dpp v120, v111 quad_perm:[2,3,0,1] row_mask:0xf bank_mask:0xf
	v_rcp_f32_e32 v123, v123
	v_rcp_f32_e32 v140, v130
	v_add_f32_e32 v130, 1.0, v134
	v_rcp_f32_e32 v141, v130
	s_waitcnt lgkmcnt(0)
	v_add_f32_e32 v111, v111, v120
	s_nop 1
	v_mov_b32_dpp v120, v111 quad_perm:[1,0,3,2] row_mask:0xf bank_mask:0xf
	v_pk_mul_f32 v[122:123], v[108:109], v[122:123]
	v_pk_mul_f32 v[108:109], v[118:119], v[140:141]
	v_pk_mul_f32 v[118:119], v[122:123], v[122:123]
	v_pk_mul_f32 v[140:141], v[108:109], v[108:109]
	s_waitcnt lgkmcnt(0)
	v_add_f32_e32 v111, v111, v120
	v_mul_f32_e32 v120, 0x3b800000, v111
	v_pk_add_f32 v[162:163], v[32:33], v[120:121] op_sel_hi:[1,0] neg_lo:[0,1] neg_hi:[0,1]
	v_pk_add_f32 v[154:155], v[154:155], v[120:121] op_sel_hi:[1,0] neg_lo:[0,1] neg_hi:[0,1]
	v_pk_mul_f32 v[32:33], v[162:163], v[162:163]
	v_pk_mul_f32 v[142:143], v[154:155], v[154:155]
	v_mov_b32_e32 v156, v32
	v_mov_b32_e32 v157, v118
	v_mov_b32_e32 v118, v33
	v_pk_add_f32 v[32:33], v[156:157], v[118:119]
	v_mov_b32_e32 v118, v142
	v_mov_b32_e32 v119, v140
	v_pk_add_f32 v[32:33], v[118:119], v[32:33]
	v_mov_b32_e32 v140, v143
	v_pk_add_f32 v[32:33], v[140:141], v[32:33]
	ds_bpermute_b32 v119, v184, v33
	ds_bpermute_b32 v118, v184, v32
	v_rcp_f32_e32 v111, v37
	v_lshlrev_b32_e32 v37, 16, v135
	v_mul_f32_e32 v37, 0xbfb8aa3b, v37
	v_and_b32_e32 v120, 0xffff0000, v135
	s_waitcnt lgkmcnt(0)
	v_pk_add_f32 v[32:33], v[32:33], v[118:119]
	ds_bpermute_b32 v119, v185, v33
	ds_bpermute_b32 v118, v185, v32
	v_exp_f32_e32 v37, v37
	v_mul_f32_e32 v120, 0xbfb8aa3b, v120
	v_exp_f32_e32 v120, v120
	v_lshlrev_b32_e32 v140, 16, v121
	s_waitcnt lgkmcnt(0)
	v_pk_add_f32 v[32:33], v[32:33], v[118:119]
	s_nop 1
	v_mov_b32_dpp v119, v33 row_ror:8 row_mask:0xf bank_mask:0xf
	s_nop 0
	v_mov_b32_dpp v118, v32 row_ror:8 row_mask:0xf bank_mask:0xf
	v_add_f32_e32 v37, 1.0, v37
	v_rcp_f32_e32 v142, v37
	v_and_b32_e32 v141, 0xffff0000, v121
	v_add_f32_e32 v37, 1.0, v120
	s_waitcnt lgkmcnt(0)
	v_pk_add_f32 v[118:119], v[32:33], v[118:119]
	s_nop 1
	v_mov_b32_dpp v121, v119 row_half_mirror row_mask:0xf bank_mask:0xf
	s_nop 1
	v_mov_b32_dpp v121, v121 quad_perm:[3,2,1,0] row_mask:0xf bank_mask:0xf
	v_mov_b32_dpp v120, v118 row_half_mirror row_mask:0xf bank_mask:0xf
	s_nop 1
	v_mov_b32_dpp v120, v120 quad_perm:[3,2,1,0] row_mask:0xf bank_mask:0xf
	v_add_u32_e32 v32, 37, v144
	v_mad_i64_i32 v[134:135], s[6:7], v32, s27, v[78:79]
	global_load_dwordx2 v[156:157], v[134:135], off
	global_load_dwordx2 v[158:159], v[134:135], off offset:512
	s_waitcnt lgkmcnt(0)
	v_pk_add_f32 v[118:119], v[118:119], v[120:121]
	s_nop 1
	v_mov_b32_dpp v121, v119 quad_perm:[2,3,0,1] row_mask:0xf bank_mask:0xf
	s_nop 0
	v_mov_b32_dpp v120, v118 quad_perm:[2,3,0,1] row_mask:0xf bank_mask:0xf
	s_waitcnt vmcnt(2)
	v_lshlrev_b32_e32 v33, 16, v152
	v_mul_f32_e32 v33, 0xbfb8aa3b, v33
	v_exp_f32_e32 v33, v33
	v_pk_fma_f32 v[22:23], v[62:63], v[94:95], v[22:23]
	s_waitcnt lgkmcnt(0)
	v_pk_add_f32 v[134:135], v[118:119], v[120:121]
	s_nop 1
	v_mov_b32_dpp v165, v135 quad_perm:[1,0,3,2] row_mask:0xf bank_mask:0xf
	s_nop 0
	v_mov_b32_dpp v164, v134 quad_perm:[1,0,3,2] row_mask:0xf bank_mask:0xf
	v_add_f32_e32 v33, 1.0, v33
	v_rcp_f32_e32 v120, v33
	v_pk_fma_f32 v[22:23], v[66:67], v[98:99], v[22:23]
	v_pk_fma_f32 v[20:21], v[60:61], v[42:43], v[20:21]
	s_waitcnt lgkmcnt(0)
	v_pk_add_f32 v[134:135], v[134:135], v[164:165]
	v_pk_mul_f32 v[114:115], v[128:129], v[114:115]
	v_pk_fma_f32 v[134:135], v[134:135], s[24:25], v[38:39] op_sel_hi:[1,0,0]
	v_pk_fma_f32 v[22:23], v[70:71], v[100:101], v[22:23]
	v_mul_f32_e32 v33, 0x4b800000, v134
	v_cmp_gt_f32_e32 vcc, s29, v134
	v_pk_fma_f32 v[20:21], v[64:65], v[96:97], v[20:21]
	v_pk_fma_f32 v[164:165], v[74:75], v[114:115], v[22:23]
	v_cndmask_b32_e32 v33, v134, v33, vcc
	v_rsq_f32_e32 v33, v33
	v_pk_mul_f32 v[22:23], v[126:127], v[124:125]
	v_pk_fma_f32 v[20:21], v[68:69], v[34:35], v[20:21]
	v_lshlrev_b32_e32 v118, 16, v136
	v_mul_f32_e32 v130, 0x45800000, v33
	v_pk_fma_f32 v[20:21], v[72:73], v[22:23], v[20:21]
	v_cndmask_b32_e32 v130, v33, v130, vcc
	v_add_f32_e32 v33, v20, v21
	v_add_f32_e32 v33, v33, v164
	v_add_f32_e32 v33, v165, v33
	v_mov_b32_e32 v128, v33
	s_nop 1
	v_permlane32_swap_b32 v128, v33
	v_pk_mul_f32 v[124:125], v[162:163], v[130:131] op_sel_hi:[1,0]
	v_pk_mul_f32 v[126:127], v[154:155], v[130:131] op_sel_hi:[1,0]
	v_pk_fma_f32 v[124:125], v[4:5], v[124:125], v[8:9]
	v_pk_fma_f32 v[126:127], v[6:7], v[126:127], v[10:11]
	s_waitcnt lgkmcnt(0)
	v_add_f32_e32 v33, v33, v128
	v_mov_b32_e32 v128, v33
	s_nop 1
	v_permlane16_swap_b32 v128, v33
	v_mul_f32_e32 v129, 0xbfb8aa3b, v124
	v_mul_f32_e32 v130, 0xbfb8aa3b, v125
	v_exp_f32_e32 v129, v129
	v_exp_f32_e32 v130, v130
	s_waitcnt lgkmcnt(0)
	v_add_f32_e32 v33, v33, v128
	s_nop 1
	v_mov_b32_dpp v134, v33 row_ror:8 row_mask:0xf bank_mask:0xf
	v_add_f32_e32 v128, 1.0, v129
	v_add_f32_e32 v129, 1.0, v130
	v_and_b32_e32 v119, 0xffff0000, v136
	v_mul_f32_e32 v136, 0xbfb8aa3b, v127
	s_waitcnt lgkmcnt(0)
	v_add_f32_e32 v33, v33, v134
	s_nop 1
	v_mov_b32_dpp v130, v33 row_half_mirror row_mask:0xf bank_mask:0xf
	s_nop 1
	v_mov_b32_dpp v130, v130 quad_perm:[3,2,1,0] row_mask:0xf bank_mask:0xf
	v_mul_f32_e32 v134, 0xbfb8aa3b, v126
	v_exp_f32_e32 v134, v134
	v_exp_f32_e32 v136, v136
	v_rcp_f32_e32 v128, v128
	s_waitcnt lgkmcnt(0)
	v_add_f32_e32 v33, v33, v130
	s_nop 1
	v_mov_b32_dpp v130, v33 quad_perm:[2,3,0,1] row_mask:0xf bank_mask:0xf
	v_add_f32_e32 v134, 1.0, v134
	v_rcp_f32_e32 v129, v129
	v_rcp_f32_e32 v154, v134
	v_add_f32_e32 v134, 1.0, v136
	s_waitcnt lgkmcnt(0)
	v_add_f32_e32 v33, v33, v130
	s_nop 1
	v_mov_b32_dpp v130, v33 quad_perm:[1,0,3,2] row_mask:0xf bank_mask:0xf
	v_rcp_f32_e32 v155, v134
	v_pk_mul_f32 v[128:129], v[124:125], v[128:129]
	v_and_b32_e32 v121, 0xffff0000, v152
	v_pk_mul_f32 v[124:125], v[128:129], v[128:129]
	s_waitcnt lgkmcnt(0)
	v_add_f32_e32 v33, v33, v130
	v_mul_f32_e32 v130, 0x3b800000, v33
	v_pk_add_f32 v[162:163], v[20:21], v[130:131] op_sel_hi:[1,0] neg_lo:[0,1] neg_hi:[0,1]
	v_pk_mul_f32 v[126:127], v[126:127], v[154:155]
	v_pk_add_f32 v[164:165], v[164:165], v[130:131] op_sel_hi:[1,0] neg_lo:[0,1] neg_hi:[0,1]
	v_pk_mul_f32 v[20:21], v[162:163], v[162:163]
	v_pk_mul_f32 v[154:155], v[126:127], v[126:127]
	v_pk_mul_f32 v[166:167], v[164:165], v[164:165]
	v_mov_b32_e32 v168, v20
	v_mov_b32_e32 v169, v124
	v_mov_b32_e32 v124, v21
	v_pk_add_f32 v[20:21], v[168:169], v[124:125]
	v_mov_b32_e32 v124, v166
	v_mov_b32_e32 v125, v154
	v_pk_add_f32 v[20:21], v[124:125], v[20:21]
	v_mov_b32_e32 v154, v167
	v_pk_add_f32 v[20:21], v[154:155], v[20:21]
	ds_bpermute_b32 v125, v184, v21
	ds_bpermute_b32 v124, v184, v20
	v_mul_f32_e32 v121, 0xbfb8aa3b, v121
	v_exp_f32_e32 v33, v121
	v_lshlrev_b32_e32 v121, 16, v153
	v_mul_f32_e32 v121, 0xbfb8aa3b, v121
	s_waitcnt lgkmcnt(0)
	v_pk_add_f32 v[20:21], v[20:21], v[124:125]
	ds_bpermute_b32 v125, v185, v21
	ds_bpermute_b32 v124, v185, v20
	v_exp_f32_e32 v130, v121
	v_add_f32_e32 v33, 1.0, v33
	v_rcp_f32_e32 v121, v33
	v_lshlrev_b32_e32 v152, 16, v137
	s_waitcnt lgkmcnt(0)
	v_pk_add_f32 v[20:21], v[20:21], v[124:125]
	s_nop 1
	v_mov_b32_dpp v125, v21 row_ror:8 row_mask:0xf bank_mask:0xf
	s_nop 0
	v_mov_b32_dpp v124, v20 row_ror:8 row_mask:0xf bank_mask:0xf
	v_add_f32_e32 v33, 1.0, v130
	v_rcp_f32_e32 v154, v33
	v_and_b32_e32 v33, 0xffff0000, v153
	v_and_b32_e32 v153, 0xffff0000, v137
	s_waitcnt lgkmcnt(0)
	v_pk_add_f32 v[20:21], v[20:21], v[124:125]
	s_nop 1
	v_mov_b32_dpp v125, v21 row_half_mirror row_mask:0xf bank_mask:0xf
	s_nop 1
	v_mov_b32_dpp v125, v125 quad_perm:[3,2,1,0] row_mask:0xf bank_mask:0xf
	v_mov_b32_dpp v124, v20 row_half_mirror row_mask:0xf bank_mask:0xf
	s_nop 1
	v_mov_b32_dpp v124, v124 quad_perm:[3,2,1,0] row_mask:0xf bank_mask:0xf
	v_mul_f32_e32 v41, 0xbfb8aa3b, v41
	v_exp_f32_e32 v41, v41
	v_pk_fma_f32 v[82:83], v[42:43], v[56:57], v[82:83]
	v_pk_fma_f32 v[84:85], v[58:59], v[94:95], v[84:85]
	s_waitcnt lgkmcnt(0)
	v_pk_add_f32 v[124:125], v[20:21], v[124:125]
	s_nop 1
	v_mov_b32_dpp v137, v125 quad_perm:[2,3,0,1] row_mask:0xf bank_mask:0xf
	s_nop 0
	v_mov_b32_dpp v136, v124 quad_perm:[2,3,0,1] row_mask:0xf bank_mask:0xf
	v_add_f32_e32 v41, 1.0, v41
	v_rcp_f32_e32 v139, v41
	v_pk_fma_f32 v[82:83], v[60:61], v[96:97], v[82:83]
	v_pk_fma_f32 v[84:85], v[62:63], v[98:99], v[84:85]
	s_waitcnt lgkmcnt(0)
	v_pk_add_f32 v[136:137], v[124:125], v[136:137]
	s_nop 1
	v_mov_b32_dpp v167, v137 quad_perm:[1,0,3,2] row_mask:0xf bank_mask:0xf
	s_nop 0
	v_mov_b32_dpp v166, v136 quad_perm:[1,0,3,2] row_mask:0xf bank_mask:0xf
	v_pk_fma_f32 v[82:83], v[64:65], v[34:35], v[82:83]
	v_pk_fma_f32 v[84:85], v[66:67], v[100:101], v[84:85]
	v_pk_mul_f32 v[112:113], v[116:117], v[112:113]
	v_pk_fma_f32 v[82:83], v[68:69], v[22:23], v[82:83]
	s_waitcnt lgkmcnt(0)
	v_pk_add_f32 v[136:137], v[136:137], v[166:167]
	v_pk_mul_f32 v[132:133], v[138:139], v[132:133]
	v_pk_fma_f32 v[136:137], v[136:137], s[24:25], v[38:39] op_sel_hi:[1,0,0]
	v_pk_fma_f32 v[84:85], v[70:71], v[114:115], v[84:85]
	v_mul_f32_e32 v130, 0x4b800000, v136
	v_cmp_gt_f32_e32 vcc, s29, v136
	v_pk_fma_f32 v[116:117], v[72:73], v[112:113], v[82:83]
	v_pk_fma_f32 v[138:139], v[74:75], v[132:133], v[84:85]
	v_cndmask_b32_e32 v130, v136, v130, vcc
	v_rsq_f32_e32 v130, v130
	v_add_f32_e32 v82, v116, v117
	v_add_f32_e32 v82, v82, v138
	s_waitcnt vmcnt(0)
	v_lshlrev_b32_e32 v21, 16, v158
	v_mul_f32_e32 v134, 0x45800000, v130
	v_cndmask_b32_e32 v130, v130, v134, vcc
	v_add_f32_e32 v134, v139, v82
	ds_bpermute_b32 v136, v184, v134
	v_pk_mul_f32 v[84:85], v[164:165], v[130:131] op_sel_hi:[1,0]
	v_pk_mul_f32 v[82:83], v[162:163], v[130:131] op_sel_hi:[1,0]
	v_pk_fma_f32 v[162:163], v[6:7], v[84:85], v[10:11]
	v_mul_f32_e32 v21, 0xbfb8aa3b, v21
	s_waitcnt lgkmcnt(0)
	v_add_f32_e32 v84, v134, v136
	ds_bpermute_b32 v85, v185, v84
	v_exp_f32_e32 v21, v21
	v_pk_fma_f32 v[82:83], v[4:5], v[82:83], v[8:9]
	v_lshlrev_b32_e32 v20, 16, v156
	v_mul_f32_e32 v130, 0xbfb8aa3b, v82
	v_add_f32_e32 v21, 1.0, v21
	s_waitcnt lgkmcnt(0)
	v_add_f32_e32 v136, v84, v85
	v_rcp_f32_e32 v124, v21
	v_and_b32_e32 v21, 0xffff0000, v156
	v_mov_b32_dpp v156, v136 row_ror:8 row_mask:0xf bank_mask:0xf
	v_exp_f32_e32 v130, v130
	v_mul_f32_e32 v134, 0xbfb8aa3b, v83
	v_exp_f32_e32 v134, v134
	v_and_b32_e32 v125, 0xffff0000, v158
	v_add_f32_e32 v84, 1.0, v130
	s_waitcnt lgkmcnt(0)
	v_add_f32_e32 v130, v136, v156
	v_add_f32_e32 v85, 1.0, v134
	s_nop 0
	v_mov_b32_dpp v134, v130 row_half_mirror row_mask:0xf bank_mask:0xf
	s_nop 1
	v_mov_b32_dpp v134, v134 quad_perm:[3,2,1,0] row_mask:0xf bank_mask:0xf
	v_mul_f32_e32 v136, 0xbfb8aa3b, v162
	v_exp_f32_e32 v136, v136
	v_mul_f32_e32 v156, 0xbfb8aa3b, v163
	v_exp_f32_e32 v156, v156
	s_waitcnt lgkmcnt(0)
	v_add_f32_e32 v130, v130, v134
	s_nop 1
	v_mov_b32_dpp v134, v130 quad_perm:[2,3,0,1] row_mask:0xf bank_mask:0xf
	v_add_f32_e32 v136, 1.0, v136
	v_rcp_f32_e32 v84, v84
	v_rcp_f32_e32 v85, v85
	v_rcp_f32_e32 v164, v136
	s_waitcnt lgkmcnt(0)
	v_add_f32_e32 v130, v130, v134
	s_nop 1
	v_mov_b32_dpp v134, v130 quad_perm:[1,0,3,2] row_mask:0xf bank_mask:0xf
	v_add_f32_e32 v136, 1.0, v156
	v_rcp_f32_e32 v165, v136
	v_pk_mul_f32 v[84:85], v[82:83], v[84:85]
	v_mul_f32_e32 v125, 0xbfb8aa3b, v125
	s_waitcnt lgkmcnt(0)
	v_add_f32_e32 v130, v130, v134
	v_mul_f32_e32 v130, 0x3b800000, v130
	v_pk_add_f32 v[166:167], v[116:117], v[130:131] op_sel_hi:[1,0] neg_lo:[0,1] neg_hi:[0,1]
	v_pk_mul_f32 v[82:83], v[162:163], v[164:165]
	v_pk_mul_f32 v[162:163], v[84:85], v[84:85]
	v_pk_add_f32 v[168:169], v[138:139], v[130:131] op_sel_hi:[1,0] neg_lo:[0,1] neg_hi:[0,1]
	v_pk_mul_f32 v[116:117], v[166:167], v[166:167]
	v_pk_mul_f32 v[164:165], v[82:83], v[82:83]
	v_pk_mul_f32 v[138:139], v[168:169], v[168:169]
	v_mov_b32_e32 v170, v116
	v_mov_b32_e32 v171, v162
	v_mov_b32_e32 v162, v117
	v_pk_add_f32 v[116:117], v[170:171], v[162:163]
	v_mov_b32_e32 v162, v138
	v_mov_b32_e32 v163, v164
	v_pk_add_f32 v[116:117], v[162:163], v[116:117]
	v_mov_b32_e32 v164, v139
	v_pk_add_f32 v[116:117], v[164:165], v[116:117]
	ds_bpermute_b32 v139, v184, v117
	ds_bpermute_b32 v138, v184, v116
	v_lshlrev_b32_e32 v130, 16, v159
	v_mul_f32_e32 v130, 0xbfb8aa3b, v130
	v_exp_f32_e32 v130, v130
	v_exp_f32_e32 v125, v125
	s_waitcnt lgkmcnt(0)
	v_pk_add_f32 v[138:139], v[116:117], v[138:139]
	ds_bpermute_b32 v163, v185, v139
	ds_bpermute_b32 v162, v185, v138
	v_add_f32_e32 v117, 1.0, v130
	v_add_f32_e32 v116, 1.0, v125
	v_rcp_f32_e32 v125, v116
	v_lshlrev_b32_e32 v116, 16, v157
	s_waitcnt lgkmcnt(0)
	v_pk_add_f32 v[162:163], v[138:139], v[162:163]
	s_nop 1
	v_mov_b32_dpp v165, v163 row_ror:8 row_mask:0xf bank_mask:0xf
	s_nop 0
	v_mov_b32_dpp v164, v162 row_ror:8 row_mask:0xf bank_mask:0xf
	v_rcp_f32_e32 v138, v117
	v_and_b32_e32 v117, 0xffff0000, v159
	v_mul_f32_e32 v117, 0xbfb8aa3b, v117
	v_exp_f32_e32 v130, v117
	s_waitcnt lgkmcnt(0)
	v_pk_add_f32 v[158:159], v[162:163], v[164:165]
	s_nop 1
	v_mov_b32_dpp v163, v159 row_half_mirror row_mask:0xf bank_mask:0xf
	s_nop 1
	v_mov_b32_dpp v163, v163 quad_perm:[3,2,1,0] row_mask:0xf bank_mask:0xf
	v_mov_b32_dpp v162, v158 row_half_mirror row_mask:0xf bank_mask:0xf
	s_nop 1
	v_mov_b32_dpp v162, v162 quad_perm:[3,2,1,0] row_mask:0xf bank_mask:0xf
	v_and_b32_e32 v117, 0xffff0000, v157
	v_add_f32_e32 v130, 1.0, v130
	v_rcp_f32_e32 v139, v130
	v_mul_f32_e32 v130, 0x4b800000, v131
	s_waitcnt lgkmcnt(0)
	v_pk_add_f32 v[156:157], v[158:159], v[162:163]
	s_nop 1
	v_mov_b32_dpp v159, v157 quad_perm:[2,3,0,1] row_mask:0xf bank_mask:0xf
	s_nop 0
	v_mov_b32_dpp v158, v156 quad_perm:[2,3,0,1] row_mask:0xf bank_mask:0xf
	v_lshl_add_u64 v[162:163], v[76:77], 0, v[80:81]
	v_cmp_gt_f32_e32 vcc, s29, v131
	v_pk_fma_f32 v[24:25], v[42:43], v[52:53], v[24:25]
	v_rcp_f32_e32 v143, v37
	s_waitcnt lgkmcnt(0)
	v_pk_add_f32 v[80:81], v[156:157], v[158:159]
	s_nop 1
	v_mov_b32_dpp v157, v81 quad_perm:[1,0,3,2] row_mask:0xf bank_mask:0xf
	s_nop 0
	v_mov_b32_dpp v156, v80 quad_perm:[1,0,3,2] row_mask:0xf bank_mask:0xf
	v_cndmask_b32_e32 v130, v131, v130, vcc
	v_rsq_f32_e32 v130, v130
	v_pk_fma_f32 v[26:27], v[94:95], v[54:55], v[26:27]
	v_pk_fma_f32 v[24:25], v[56:57], v[96:97], v[24:25]
	s_waitcnt lgkmcnt(0)
	v_pk_add_f32 v[80:81], v[80:81], v[156:157]
	v_pk_fma_f32 v[26:27], v[58:59], v[98:99], v[26:27]
	v_pk_fma_f32 v[80:81], v[80:81], s[24:25], v[38:39] op_sel_hi:[1,0,0]
	v_pk_fma_f32 v[24:25], v[60:61], v[34:35], v[24:25]
	v_mul_f32_e32 v131, 0x4b800000, v80
	v_cmp_gt_f32_e64 s[6:7], s29, v80
	v_pk_fma_f32 v[26:27], v[62:63], v[100:101], v[26:27]
	v_pk_fma_f32 v[24:25], v[64:65], v[22:23], v[24:25]
	v_cndmask_b32_e64 v80, v80, v131, s[6:7]
	v_rsq_f32_e32 v131, v80
	v_mul_f32_e32 v80, 0x45800000, v130
	v_cndmask_b32_e32 v80, v130, v80, vcc
	v_pk_fma_f32 v[26:27], v[66:67], v[114:115], v[26:27]
	v_mul_f32_e32 v130, 0x45800000, v131
	v_pk_mul_f32 v[106:107], v[110:111], v[106:107]
	v_pk_fma_f32 v[24:25], v[68:69], v[112:113], v[24:25]
	v_cndmask_b32_e64 v134, v131, v130, s[6:7]
	v_pk_mul_f32 v[130:131], v[142:143], v[140:141]
	v_pk_fma_f32 v[26:27], v[70:71], v[132:133], v[26:27]
	v_pk_fma_f32 v[110:111], v[72:73], v[106:107], v[24:25]
	v_pk_fma_f32 v[140:141], v[74:75], v[130:131], v[26:27]
	v_add_f32_e32 v24, v110, v111
	v_add_f32_e32 v24, v24, v140
	v_add_f32_e32 v136, v141, v24
	ds_bpermute_b32 v156, v184, v136
	v_pk_mul_f32 v[26:27], v[168:169], v[134:135] op_sel_hi:[1,0]
	v_pk_mul_f32 v[24:25], v[166:167], v[134:135] op_sel_hi:[1,0]
	v_pk_fma_f32 v[142:143], v[6:7], v[26:27], v[10:11]
	v_pk_fma_f32 v[24:25], v[4:5], v[24:25], v[8:9]
	s_waitcnt lgkmcnt(0)
	v_add_f32_e32 v26, v136, v156
	ds_bpermute_b32 v27, v185, v26
	v_mul_f32_e32 v134, 0xbfb8aa3b, v24
	v_exp_f32_e32 v134, v134
	v_mul_f32_e32 v136, 0xbfb8aa3b, v25
	v_exp_f32_e32 v136, v136
	s_waitcnt lgkmcnt(0)
	v_add_f32_e32 v156, v26, v27
	s_nop 1
	v_mov_b32_dpp v157, v156 row_ror:8 row_mask:0xf bank_mask:0xf
	v_add_f32_e32 v26, 1.0, v134
	v_add_f32_e32 v27, 1.0, v136
	v_rcp_f32_e32 v26, v26
	v_rcp_f32_e32 v27, v27
	s_waitcnt lgkmcnt(0)
	v_add_f32_e32 v134, v156, v157
	s_nop 1
	v_mov_b32_dpp v136, v134 row_half_mirror row_mask:0xf bank_mask:0xf
	s_nop 1
	v_mov_b32_dpp v136, v136 quad_perm:[3,2,1,0] row_mask:0xf bank_mask:0xf
	v_mul_f32_e32 v156, 0xbfb8aa3b, v142
	v_mul_f32_e32 v157, 0xbfb8aa3b, v143
	v_exp_f32_e32 v156, v156
	v_exp_f32_e32 v157, v157
	s_waitcnt lgkmcnt(0)
	v_add_f32_e32 v134, v134, v136
	s_nop 1
	v_mov_b32_dpp v136, v134 quad_perm:[2,3,0,1] row_mask:0xf bank_mask:0xf
	v_add_f32_e32 v156, 1.0, v156
	v_add_f32_e32 v157, 1.0, v157
	v_rcp_f32_e32 v156, v156
	v_rcp_f32_e32 v157, v157
	s_waitcnt lgkmcnt(0)
	v_add_f32_e32 v134, v134, v136
	s_nop 1
	v_mov_b32_dpp v136, v134 quad_perm:[1,0,3,2] row_mask:0xf bank_mask:0xf
	v_pk_mul_f32 v[26:27], v[24:25], v[26:27]
	v_pk_mul_f32 v[24:25], v[142:143], v[156:157]
	v_pk_mul_f32 v[142:143], v[26:27], v[26:27]
	v_pk_mul_f32 v[156:157], v[24:25], v[24:25]
	s_waitcnt lgkmcnt(0)
	v_add_f32_e32 v134, v134, v136
	v_mul_f32_e32 v134, 0x3b800000, v134
	v_pk_add_f32 v[110:111], v[110:111], v[134:135] op_sel_hi:[1,0] neg_lo:[0,1] neg_hi:[0,1]
	v_pk_add_f32 v[140:141], v[140:141], v[134:135] op_sel_hi:[1,0] neg_lo:[0,1] neg_hi:[0,1]
	v_pk_mul_f32 v[158:159], v[110:111], v[110:111]
	v_pk_mul_f32 v[164:165], v[140:141], v[140:141]
	v_mov_b32_e32 v166, v158
	v_mov_b32_e32 v167, v142
	v_mov_b32_e32 v142, v159
	v_pk_add_f32 v[142:143], v[166:167], v[142:143]
	v_mov_b32_e32 v158, v164
	v_mov_b32_e32 v159, v156
	v_pk_add_f32 v[142:143], v[158:159], v[142:143]
	v_mov_b32_e32 v156, v165
	v_pk_add_f32 v[142:143], v[156:157], v[142:143]
	ds_bpermute_b32 v157, v184, v143
	ds_bpermute_b32 v156, v184, v142
	v_pk_mul_f32 v[104:105], v[104:105], v[80:81] op_sel_hi:[1,0]
	v_pk_mul_f32 v[102:103], v[102:103], v[80:81] op_sel_hi:[1,0]
	v_pk_mul_f32 v[104:105], v[12:13], v[104:105]
	v_pk_mul_f32 v[102:103], v[14:15], v[102:103]
	s_waitcnt lgkmcnt(0)
	v_pk_add_f32 v[142:143], v[142:143], v[156:157]
	ds_bpermute_b32 v157, v185, v143
	ds_bpermute_b32 v156, v185, v142
	v_cvt_pk_bf16_f32 v104, v104, v105
	v_cvt_pk_bf16_f32 v105, v102, v103
	global_store_dwordx2 v[162:163], v[104:105], off
	v_pk_fma_f32 v[16:17], v[42:43], v[48:49], v[16:17]
	s_waitcnt lgkmcnt(0)
	v_pk_add_f32 v[102:103], v[142:143], v[156:157]
	s_nop 1
	v_mov_b32_dpp v105, v103 row_ror:8 row_mask:0xf bank_mask:0xf
	s_nop 0
	v_mov_b32_dpp v104, v102 row_ror:8 row_mask:0xf bank_mask:0xf
	v_lshl_add_u64 v[142:143], v[76:77], 0, v[92:93]
	v_mul_f32_e32 v33, 0xbfb8aa3b, v33
	v_pk_fma_f32 v[16:17], v[52:53], v[96:97], v[16:17]
	v_exp_f32_e32 v33, v33
	s_waitcnt lgkmcnt(0)
	v_pk_add_f32 v[92:93], v[102:103], v[104:105]
	s_nop 1
	v_mov_b32_dpp v103, v93 row_half_mirror row_mask:0xf bank_mask:0xf
	s_nop 1
	v_mov_b32_dpp v103, v103 quad_perm:[3,2,1,0] row_mask:0xf bank_mask:0xf
	v_mov_b32_dpp v102, v92 row_half_mirror row_mask:0xf bank_mask:0xf
	s_nop 1
	v_mov_b32_dpp v102, v102 quad_perm:[3,2,1,0] row_mask:0xf bank_mask:0xf
	v_pk_fma_f32 v[104:105], v[56:57], v[34:35], v[16:17]
	v_mul_f32_e32 v80, 0x4b800000, v135
	v_cmp_gt_f32_e32 vcc, s29, v135
	v_add_f32_e32 v33, 1.0, v33
	s_waitcnt lgkmcnt(0)
	v_pk_add_f32 v[92:93], v[92:93], v[102:103]
	s_nop 1
	v_mov_b32_dpp v103, v93 quad_perm:[2,3,0,1] row_mask:0xf bank_mask:0xf
	s_nop 0
	v_mov_b32_dpp v102, v92 quad_perm:[2,3,0,1] row_mask:0xf bank_mask:0xf
	v_cndmask_b32_e32 v80, v135, v80, vcc
	v_rsq_f32_e32 v80, v80
	v_pk_fma_f32 v[18:19], v[94:95], v[50:51], v[18:19]
	v_rcp_f32_e32 v155, v33
	s_waitcnt lgkmcnt(0)
	v_pk_add_f32 v[16:17], v[92:93], v[102:103]
	s_nop 1
	v_mov_b32_dpp v93, v17 quad_perm:[1,0,3,2] row_mask:0xf bank_mask:0xf
	s_nop 0
	v_mov_b32_dpp v92, v16 quad_perm:[1,0,3,2] row_mask:0xf bank_mask:0xf
	v_pk_fma_f32 v[18:19], v[54:55], v[98:99], v[18:19]
	v_mul_f32_e32 v134, 0x45800000, v80
	v_pk_fma_f32 v[18:19], v[58:59], v[100:101], v[18:19]
	v_cndmask_b32_e32 v80, v80, v134, vcc
	s_waitcnt lgkmcnt(0)
	v_pk_add_f32 v[16:17], v[16:17], v[92:93]
	v_pk_fma_f32 v[18:19], v[62:63], v[114:115], v[18:19]
	v_pk_fma_f32 v[16:17], v[16:17], s[24:25], v[38:39] op_sel_hi:[1,0,0]
	v_pk_fma_f32 v[18:19], v[66:67], v[132:133], v[18:19]
	v_mul_f32_e32 v92, 0x4b800000, v16
	v_cmp_gt_f32_e32 vcc, s29, v16
	v_pk_fma_f32 v[18:19], v[70:71], v[130:131], v[18:19]
	v_pk_mul_f32 v[102:103], v[122:123], v[80:81] op_sel_hi:[1,0]
	v_cndmask_b32_e32 v16, v16, v92, vcc
	v_pk_mul_f32 v[92:93], v[108:109], v[80:81] op_sel_hi:[1,0]
	v_pk_mul_f32 v[108:109], v[154:155], v[152:153]
	v_rsq_f32_e32 v16, v16
	v_pk_fma_f32 v[122:123], v[74:75], v[108:109], v[18:19]
	v_pk_fma_f32 v[18:19], v[60:61], v[22:23], v[104:105]
	v_pk_mul_f32 v[118:119], v[120:121], v[118:119]
	v_pk_fma_f32 v[18:19], v[64:65], v[112:113], v[18:19]
	v_mul_f32_e32 v80, 0x45800000, v16
	v_pk_fma_f32 v[18:19], v[68:69], v[106:107], v[18:19]
	v_cndmask_b32_e32 v16, v16, v80, vcc
	v_pk_fma_f32 v[104:105], v[72:73], v[118:119], v[18:19]
	v_pk_mul_f32 v[102:103], v[12:13], v[102:103]
	v_add_f32_e32 v18, v104, v105
	v_add_f32_e32 v18, v18, v122
	v_add_f32_e32 v80, v123, v18
	ds_bpermute_b32 v120, v184, v80
	v_pk_mul_f32 v[92:93], v[14:15], v[92:93]
	v_cvt_pk_bf16_f32 v102, v102, v103
	v_cvt_pk_bf16_f32 v103, v92, v93
	v_pk_mul_f32 v[18:19], v[110:111], v[16:17] op_sel_hi:[1,0]
	v_pk_mul_f32 v[92:93], v[140:141], v[16:17] op_sel_hi:[1,0]
	s_waitcnt lgkmcnt(0)
	v_add_f32_e32 v16, v80, v120
	v_mov_b32_e32 v80, v16
	s_nop 1
	v_permlane16_swap_b32 v80, v16
	v_pk_fma_f32 v[18:19], v[4:5], v[18:19], v[8:9]
	v_pk_fma_f32 v[110:111], v[6:7], v[92:93], v[10:11]
	v_mul_f32_e32 v92, 0xbfb8aa3b, v18
	v_mul_f32_e32 v93, 0xbfb8aa3b, v19
	s_waitcnt lgkmcnt(0)
	v_add_f32_e32 v16, v16, v80
	s_nop 1
	v_mov_b32_dpp v80, v16 row_ror:8 row_mask:0xf bank_mask:0xf
	v_exp_f32_e32 v92, v92
	v_exp_f32_e32 v93, v93
	v_mul_f32_e32 v120, 0xbfb8aa3b, v110
	v_mul_f32_e32 v121, 0xbfb8aa3b, v111
	s_waitcnt lgkmcnt(0)
	v_add_f32_e32 v16, v16, v80
	s_nop 1
	v_mov_b32_dpp v80, v16 row_half_mirror row_mask:0xf bank_mask:0xf
	s_nop 1
	v_mov_b32_dpp v80, v80 quad_perm:[3,2,1,0] row_mask:0xf bank_mask:0xf
	v_exp_f32_e32 v120, v120
	v_exp_f32_e32 v121, v121
	v_add_f32_e32 v92, 1.0, v92
	v_add_f32_e32 v93, 1.0, v93
	s_waitcnt lgkmcnt(0)
	v_add_f32_e32 v16, v16, v80
	s_nop 1
	v_mov_b32_dpp v80, v16 quad_perm:[2,3,0,1] row_mask:0xf bank_mask:0xf
	v_rcp_f32_e32 v92, v92
	v_rcp_f32_e32 v93, v93
	v_add_f32_e32 v120, 1.0, v120
	v_add_f32_e32 v121, 1.0, v121
	s_waitcnt lgkmcnt(0)
	v_add_f32_e32 v16, v16, v80
	s_nop 1
	v_mov_b32_dpp v80, v16 quad_perm:[1,0,3,2] row_mask:0xf bank_mask:0xf
	v_rcp_f32_e32 v120, v120
	v_rcp_f32_e32 v121, v121
	v_pk_mul_f32 v[92:93], v[18:19], v[92:93]
	v_pk_fma_f32 v[30:31], v[94:95], v[46:47], v[30:31]
	s_waitcnt lgkmcnt(0)
	v_add_f32_e32 v16, v16, v80
	v_mul_f32_e32 v16, 0x3b800000, v16
	v_pk_add_f32 v[104:105], v[104:105], v[16:17] op_sel_hi:[1,0] neg_lo:[0,1] neg_hi:[0,1]
	v_pk_mul_f32 v[18:19], v[110:111], v[120:121]
	v_pk_mul_f32 v[110:111], v[92:93], v[92:93]
	v_pk_add_f32 v[122:123], v[122:123], v[16:17] op_sel_hi:[1,0] neg_lo:[0,1] neg_hi:[0,1]
	v_pk_mul_f32 v[134:135], v[104:105], v[104:105]
	v_pk_mul_f32 v[120:121], v[18:19], v[18:19]
	v_pk_mul_f32 v[140:141], v[122:123], v[122:123]
	v_mov_b32_e32 v152, v134
	v_mov_b32_e32 v153, v110
	v_mov_b32_e32 v110, v135
	v_pk_add_f32 v[110:111], v[152:153], v[110:111]
	v_mov_b32_e32 v134, v140
	v_mov_b32_e32 v135, v120
	v_pk_add_f32 v[110:111], v[134:135], v[110:111]
	v_mov_b32_e32 v120, v141
	v_pk_add_f32 v[110:111], v[120:121], v[110:111]
	ds_bpermute_b32 v121, v184, v111
	ds_bpermute_b32 v120, v184, v110
	v_pk_fma_f32 v[28:29], v[42:43], v[44:45], v[28:29]
	v_mul_f32_e32 v16, 0x4b800000, v137
	v_pk_fma_f32 v[28:29], v[48:49], v[96:97], v[28:29]
	v_cmp_gt_f32_e32 vcc, s29, v137
	s_waitcnt lgkmcnt(0)
	v_pk_add_f32 v[46:47], v[110:111], v[120:121]
	ds_bpermute_b32 v95, v185, v47
	ds_bpermute_b32 v94, v185, v46
	v_pk_fma_f32 v[28:29], v[52:53], v[34:35], v[28:29]
	v_cndmask_b32_e32 v16, v137, v16, vcc
	v_pk_fma_f32 v[22:23], v[56:57], v[22:23], v[28:29]
	v_rsq_f32_e32 v16, v16
	s_waitcnt lgkmcnt(0)
	v_pk_add_f32 v[42:43], v[46:47], v[94:95]
	s_nop 1
	v_mov_b32_dpp v45, v43 row_ror:8 row_mask:0xf bank_mask:0xf
	s_nop 0
	v_mov_b32_dpp v44, v42 row_ror:8 row_mask:0xf bank_mask:0xf
	v_pk_fma_f32 v[30:31], v[50:51], v[98:99], v[30:31]
	v_pk_fma_f32 v[22:23], v[60:61], v[112:113], v[22:23]
	v_pk_fma_f32 v[30:31], v[54:55], v[100:101], v[30:31]
	v_mul_f32_e32 v46, 0x45800000, v16
	s_waitcnt lgkmcnt(0)
	v_pk_add_f32 v[42:43], v[42:43], v[44:45]
	s_nop 1
	v_mov_b32_dpp v45, v43 row_half_mirror row_mask:0xf bank_mask:0xf
	s_nop 1
	v_mov_b32_dpp v45, v45 quad_perm:[3,2,1,0] row_mask:0xf bank_mask:0xf
	v_mov_b32_dpp v44, v42 row_half_mirror row_mask:0xf bank_mask:0xf
	s_nop 1
	v_mov_b32_dpp v44, v44 quad_perm:[3,2,1,0] row_mask:0xf bank_mask:0xf
	v_pk_fma_f32 v[30:31], v[58:59], v[114:115], v[30:31]
	v_pk_fma_f32 v[22:23], v[64:65], v[106:107], v[22:23]
	v_pk_fma_f32 v[30:31], v[62:63], v[132:133], v[30:31]
	v_cndmask_b32_e32 v16, v16, v46, vcc
	s_waitcnt lgkmcnt(0)
	v_pk_add_f32 v[28:29], v[42:43], v[44:45]
	s_nop 1
	v_mov_b32_dpp v35, v29 quad_perm:[2,3,0,1] row_mask:0xf bank_mask:0xf
	s_nop 0
	v_mov_b32_dpp v34, v28 quad_perm:[2,3,0,1] row_mask:0xf bank_mask:0xf
	v_pk_fma_f32 v[30:31], v[66:67], v[130:131], v[30:31]
	v_pk_mul_f32 v[20:21], v[124:125], v[20:21]
	v_pk_fma_f32 v[22:23], v[68:69], v[118:119], v[22:23]
	v_pk_mul_f32 v[42:43], v[128:129], v[16:17] op_sel_hi:[1,0]
	s_waitcnt lgkmcnt(0)
	v_pk_add_f32 v[28:29], v[28:29], v[34:35]
	s_nop 1
	v_mov_b32_dpp v35, v29 quad_perm:[1,0,3,2] row_mask:0xf bank_mask:0xf
	s_nop 0
	v_mov_b32_dpp v34, v28 quad_perm:[1,0,3,2] row_mask:0xf bank_mask:0xf
	v_pk_mul_f32 v[44:45], v[126:127], v[16:17] op_sel_hi:[1,0]
	v_mul_f32_e32 v16, 0x4b800000, v81
	v_cmp_gt_f32_e32 vcc, s29, v81
	v_pk_fma_f32 v[30:31], v[70:71], v[108:109], v[30:31]
	s_waitcnt lgkmcnt(0)
	v_pk_add_f32 v[28:29], v[28:29], v[34:35]
	v_pk_fma_f32 v[20:21], v[72:73], v[20:21], v[22:23]
	v_pk_fma_f32 v[28:29], v[28:29], s[24:25], v[38:39] op_sel_hi:[1,0,0]
	v_cndmask_b32_e32 v16, v81, v16, vcc
	v_mul_f32_e32 v34, 0x4b800000, v28
	v_cmp_gt_f32_e64 s[6:7], s29, v28
	v_add_f32_e32 v22, v20, v21
	v_rsq_f32_e32 v54, v16
	v_cndmask_b32_e64 v28, v28, v34, s[6:7]
	v_rsq_f32_e32 v28, v28
	v_pk_mul_f32 v[34:35], v[138:139], v[116:117]
	v_pk_mul_f32 v[42:43], v[12:13], v[42:43]
	v_pk_fma_f32 v[30:31], v[74:75], v[34:35], v[30:31]
	v_mul_f32_e32 v16, 0x45800000, v28
	v_add_f32_e32 v22, v22, v30
	v_pk_mul_f32 v[44:45], v[14:15], v[44:45]
	v_cndmask_b32_e64 v16, v28, v16, s[6:7]
	v_add_f32_e32 v28, v31, v22
	v_cvt_pk_bf16_f32 v42, v42, v43
	v_cvt_pk_bf16_f32 v43, v44, v45
	ds_bpermute_b32 v44, v184, v28
	v_pk_mul_f32 v[22:23], v[104:105], v[16:17] op_sel_hi:[1,0]
	v_pk_mul_f32 v[34:35], v[122:123], v[16:17] op_sel_hi:[1,0]
	v_pk_fma_f32 v[22:23], v[4:5], v[22:23], v[8:9]
	v_pk_fma_f32 v[34:35], v[6:7], v[34:35], v[10:11]
	s_waitcnt lgkmcnt(0)
	v_add_f32_e32 v16, v28, v44
	v_mov_b32_e32 v28, v16
	s_nop 1
	v_permlane16_swap_b32 v28, v16
	v_mul_f32_e32 v44, 0xbfb8aa3b, v22
	v_mul_f32_e32 v45, 0xbfb8aa3b, v23
	v_exp_f32_e32 v44, v44
	v_exp_f32_e32 v45, v45
	s_waitcnt lgkmcnt(0)
	v_add_f32_e32 v16, v16, v28
	s_nop 1
	v_mov_b32_dpp v28, v16 row_ror:8 row_mask:0xf bank_mask:0xf
	v_mul_f32_e32 v46, 0xbfb8aa3b, v34
	v_mul_f32_e32 v47, 0xbfb8aa3b, v35
	v_exp_f32_e32 v46, v46
	v_exp_f32_e32 v47, v47
	s_waitcnt lgkmcnt(0)
	v_add_f32_e32 v16, v16, v28
	s_nop 1
	v_mov_b32_dpp v28, v16 row_half_mirror row_mask:0xf bank_mask:0xf
	s_nop 1
	v_mov_b32_dpp v28, v28 quad_perm:[3,2,1,0] row_mask:0xf bank_mask:0xf
	v_add_f32_e32 v44, 1.0, v44
	v_add_f32_e32 v45, 1.0, v45
	v_rcp_f32_e32 v44, v44
	v_rcp_f32_e32 v45, v45
	s_waitcnt lgkmcnt(0)
	v_add_f32_e32 v16, v16, v28
	s_nop 1
	v_mov_b32_dpp v28, v16 quad_perm:[2,3,0,1] row_mask:0xf bank_mask:0xf
	v_add_f32_e32 v46, 1.0, v46
	v_add_f32_e32 v47, 1.0, v47
	v_rcp_f32_e32 v46, v46
	v_rcp_f32_e32 v47, v47
	s_waitcnt lgkmcnt(0)
	v_add_f32_e32 v16, v16, v28
	s_nop 1
	v_mov_b32_dpp v28, v16 quad_perm:[1,0,3,2] row_mask:0xf bank_mask:0xf
	v_pk_mul_f32 v[22:23], v[22:23], v[44:45]
	v_pk_mul_f32 v[34:35], v[34:35], v[46:47]
	v_pk_mul_f32 v[44:45], v[22:23], v[22:23]
	v_pk_mul_f32 v[46:47], v[34:35], v[34:35]
	s_waitcnt lgkmcnt(0)
	v_add_f32_e32 v16, v16, v28
	v_mul_f32_e32 v16, 0x3b800000, v16
	v_pk_add_f32 v[20:21], v[20:21], v[16:17] op_sel_hi:[1,0] neg_lo:[0,1] neg_hi:[0,1]
	v_pk_add_f32 v[30:31], v[30:31], v[16:17] op_sel_hi:[1,0] neg_lo:[0,1] neg_hi:[0,1]
	v_pk_mul_f32 v[48:49], v[20:21], v[20:21]
	v_pk_mul_f32 v[50:51], v[30:31], v[30:31]
	v_mov_b32_e32 v52, v48
	v_mov_b32_e32 v53, v44
	v_mov_b32_e32 v44, v49
	v_pk_add_f32 v[44:45], v[52:53], v[44:45]
	v_mov_b32_e32 v48, v50
	v_mov_b32_e32 v49, v46
	v_pk_add_f32 v[44:45], v[48:49], v[44:45]
	v_mov_b32_e32 v46, v51
	v_pk_add_f32 v[44:45], v[46:47], v[44:45]
	ds_bpermute_b32 v47, v184, v45
	ds_bpermute_b32 v46, v184, v44
	v_mul_f32_e32 v16, 0x45800000, v54
	v_cndmask_b32_e32 v16, v54, v16, vcc
	v_ashrrev_i32_e32 v89, 31, v88
	v_pk_mul_f32 v[48:49], v[84:85], v[16:17] op_sel_hi:[1,0]
	s_waitcnt lgkmcnt(0)
	v_pk_add_f32 v[44:45], v[44:45], v[46:47]
	ds_bpermute_b32 v47, v185, v45
	ds_bpermute_b32 v46, v185, v44
	v_pk_mul_f32 v[50:51], v[82:83], v[16:17] op_sel_hi:[1,0]
	global_store_dwordx2 v[90:91], v[42:43], off
	v_lshlrev_b64 v[42:43], 11, v[88:89]
	v_pk_mul_f32 v[48:49], v[12:13], v[48:49]
	s_waitcnt lgkmcnt(0)
	v_pk_add_f32 v[44:45], v[44:45], v[46:47]
	s_nop 1
	v_mov_b32_dpp v47, v45 row_ror:8 row_mask:0xf bank_mask:0xf
	s_nop 0
	v_mov_b32_dpp v46, v44 row_ror:8 row_mask:0xf bank_mask:0xf
	v_pk_mul_f32 v[50:51], v[14:15], v[50:51]
	v_lshl_add_u64 v[42:43], v[76:77], 0, v[42:43]
	v_cvt_pk_bf16_f32 v48, v48, v49
	v_cvt_pk_bf16_f32 v49, v50, v51
	global_store_dwordx2 v[42:43], v[48:49], off
	s_waitcnt lgkmcnt(0)
	v_pk_add_f32 v[42:43], v[44:45], v[46:47]
	s_nop 1
	v_mov_b32_dpp v45, v43 row_half_mirror row_mask:0xf bank_mask:0xf
	s_nop 1
	v_mov_b32_dpp v45, v45 quad_perm:[3,2,1,0] row_mask:0xf bank_mask:0xf
	v_mov_b32_dpp v44, v42 row_half_mirror row_mask:0xf bank_mask:0xf
	s_nop 1
	v_mov_b32_dpp v44, v44 quad_perm:[3,2,1,0] row_mask:0xf bank_mask:0xf
	v_mul_f32_e32 v16, 0x4b800000, v17
	v_cmp_gt_f32_e32 vcc, s29, v17
	v_ashrrev_i32_e32 v87, 31, v86
	v_ashrrev_i32_e32 v41, 31, v40
	v_cndmask_b32_e32 v16, v17, v16, vcc
	v_rsq_f32_e32 v28, v16
	s_waitcnt lgkmcnt(0)
	v_pk_add_f32 v[16:17], v[42:43], v[44:45]
	s_nop 1
	v_mov_b32_dpp v43, v17 quad_perm:[2,3,0,1] row_mask:0xf bank_mask:0xf
	s_nop 0
	v_mov_b32_dpp v42, v16 quad_perm:[2,3,0,1] row_mask:0xf bank_mask:0xf
	v_mul_f32_e32 v46, 0x45800000, v28
	v_cndmask_b32_e32 v28, v28, v46, vcc
	v_pk_mul_f32 v[26:27], v[26:27], v[28:29] op_sel_hi:[1,0]
	v_pk_mul_f32 v[24:25], v[24:25], v[28:29] op_sel_hi:[1,0]
	s_waitcnt lgkmcnt(0)
	v_pk_add_f32 v[16:17], v[16:17], v[42:43]
	s_nop 1
	v_mov_b32_dpp v43, v17 quad_perm:[1,0,3,2] row_mask:0xf bank_mask:0xf
	s_nop 0
	v_mov_b32_dpp v42, v16 quad_perm:[1,0,3,2] row_mask:0xf bank_mask:0xf
	v_pk_mul_f32 v[26:27], v[12:13], v[26:27]
	v_pk_mul_f32 v[24:25], v[14:15], v[24:25]
	v_cvt_pk_bf16_f32 v26, v26, v27
	v_mul_f32_e32 v28, 0x4b800000, v29
	s_waitcnt lgkmcnt(0)
	v_pk_add_f32 v[16:17], v[16:17], v[42:43]
	v_lshlrev_b64 v[44:45], 11, v[86:87]
	v_pk_fma_f32 v[16:17], v[16:17], s[24:25], v[38:39] op_sel_hi:[1,0,0]
	v_lshl_add_u64 v[44:45], v[76:77], 0, v[44:45]
	v_mul_f32_e32 v27, 0x4b800000, v16
	v_cmp_gt_f32_e32 vcc, s29, v16
	v_ashrrev_i32_e32 v37, 31, v36
	v_ashrrev_i32_e32 v33, 31, v32
	v_cndmask_b32_e32 v16, v16, v27, vcc
	v_rsq_f32_e32 v16, v16
	v_cvt_pk_bf16_f32 v27, v24, v25
	global_store_dwordx2 v[44:45], v[26:27], off
	v_lshlrev_b64 v[26:27], 11, v[40:41]
	v_mul_f32_e32 v24, 0x45800000, v16
	v_cndmask_b32_e32 v16, v16, v24, vcc
	v_pk_mul_f32 v[20:21], v[20:21], v[16:17] op_sel_hi:[1,0]
	v_pk_mul_f32 v[24:25], v[30:31], v[16:17] op_sel_hi:[1,0]
	v_pk_fma_f32 v[20:21], v[4:5], v[20:21], v[8:9]
	v_pk_fma_f32 v[24:25], v[6:7], v[24:25], v[10:11]
	v_mul_f32_e32 v16, 0xbfb8aa3b, v20
	v_exp_f32_e32 v16, v16
	v_mul_f32_e32 v30, 0xbfb8aa3b, v21
	v_exp_f32_e32 v31, v30
	v_cmp_gt_f32_e32 vcc, s29, v29
	v_add_f32_e32 v16, 1.0, v16
	v_rcp_f32_e32 v30, v16
	v_add_f32_e32 v16, 1.0, v31
	v_mul_f32_e32 v31, 0xbfb8aa3b, v24
	v_exp_f32_e32 v38, v31
	v_mul_f32_e32 v31, 0xbfb8aa3b, v25
	v_exp_f32_e32 v39, v31
	v_rcp_f32_e32 v31, v16
	v_add_f32_e32 v16, 1.0, v38
	v_rcp_f32_e32 v38, v16
	v_add_f32_e32 v16, 1.0, v39
	v_rcp_f32_e32 v39, v16
	v_pk_mul_f32 v[20:21], v[20:21], v[30:31]
	v_cndmask_b32_e32 v16, v29, v28, vcc
	v_pk_mul_f32 v[28:29], v[20:21], v[20:21]
	v_pk_mul_f32 v[24:25], v[24:25], v[38:39]
	v_add_f32_e32 v28, v28, v29
	v_pk_mul_f32 v[30:31], v[24:25], v[24:25]
	v_rsq_f32_e32 v16, v16
	v_add_f32_e32 v28, v30, v28
	v_add_f32_e32 v28, v31, v28
	ds_bpermute_b32 v29, v184, v28
	v_mul_f32_e32 v30, 0x45800000, v16
	v_cndmask_b32_e32 v16, v16, v30, vcc
	v_pk_mul_f32 v[18:19], v[18:19], v[16:17] op_sel_hi:[1,0]
	v_lshl_add_u64 v[26:27], v[76:77], 0, v[26:27]
	s_waitcnt lgkmcnt(0)
	v_add_f32_e32 v31, v28, v29
	ds_bpermute_b32 v38, v185, v31
	v_pk_mul_f32 v[28:29], v[92:93], v[16:17] op_sel_hi:[1,0]
	v_pk_mul_f32 v[18:19], v[14:15], v[18:19]
	v_pk_mul_f32 v[28:29], v[12:13], v[28:29]
	v_cmp_gt_f32_e32 vcc, s29, v17
	s_waitcnt lgkmcnt(0)
	v_add_f32_e32 v30, v31, v38
	s_nop 1
	v_mov_b32_dpp v31, v30 row_ror:8 row_mask:0xf bank_mask:0xf
	v_cvt_pk_bf16_f32 v28, v28, v29
	v_cvt_pk_bf16_f32 v29, v18, v19
	global_store_dwordx2 v[26:27], v[28:29], off
	v_mul_f32_e32 v19, 0x4b800000, v17
	s_waitcnt lgkmcnt(0)
	v_add_f32_e32 v16, v30, v31
	s_nop 1
	v_mov_b32_dpp v18, v16 row_half_mirror row_mask:0xf bank_mask:0xf
	s_nop 1
	v_mov_b32_dpp v18, v18 quad_perm:[3,2,1,0] row_mask:0xf bank_mask:0xf
	v_cndmask_b32_e32 v17, v17, v19, vcc
	v_rsq_f32_e32 v19, v17
	s_movk_i32 s6, 0x7ff
	v_add_u32_e32 v144, s85, v144
	s_waitcnt lgkmcnt(0)
	v_add_f32_e32 v26, v16, v18
	s_nop 1
	v_mov_b32_dpp v27, v26 quad_perm:[2,3,0,1] row_mask:0xf bank_mask:0xf
	v_mul_f32_e32 v18, 0x45800000, v19
	v_cndmask_b32_e32 v18, v19, v18, vcc
	v_pk_mul_f32 v[22:23], v[22:23], v[18:19] op_sel_hi:[1,0]
	v_pk_mul_f32 v[18:19], v[34:35], v[18:19] op_sel_hi:[1,0]
	s_waitcnt lgkmcnt(0)
	v_add_f32_e32 v26, v26, v27
	s_nop 1
	v_mov_b32_dpp v27, v26 quad_perm:[1,0,3,2] row_mask:0xf bank_mask:0xf
	v_pk_mul_f32 v[22:23], v[12:13], v[22:23]
	v_lshlrev_b64 v[16:17], 11, v[36:37]
	v_cvt_pk_bf16_f32 v22, v22, v23
	v_pk_mul_f32 v[18:19], v[14:15], v[18:19]
	s_waitcnt lgkmcnt(0)
	v_add_f32_e32 v23, v26, v27
	v_fmamk_f32 v23, v23, 0x3b800000, v191
	v_mul_f32_e32 v26, 0x4b800000, v23
	v_cmp_gt_f32_e32 vcc, s29, v23
	v_lshl_add_u64 v[16:17], v[76:77], 0, v[16:17]
	global_store_dwordx2 v[142:143], v[102:103], off
	v_cndmask_b32_e32 v23, v23, v26, vcc
	v_rsq_f32_e32 v26, v23
	v_cvt_pk_bf16_f32 v23, v18, v19
	global_store_dwordx2 v[16:17], v[22:23], off
	v_mul_f32_e32 v16, 0x45800000, v26
	v_cndmask_b32_e32 v16, v26, v16, vcc
	v_pk_mul_f32 v[18:19], v[20:21], v[16:17] op_sel_hi:[1,0]
	v_pk_mul_f32 v[16:17], v[24:25], v[16:17] op_sel_hi:[1,0]
	v_pk_mul_f32 v[18:19], v[12:13], v[18:19]
	v_pk_mul_f32 v[16:17], v[14:15], v[16:17]
	v_cvt_pk_bf16_f32 v18, v18, v19
	v_cvt_pk_bf16_f32 v19, v16, v17
	v_lshlrev_b64 v[16:17], 11, v[32:33]
	v_cmp_lt_i32_e32 vcc, s6, v160
	v_lshl_add_u64 v[16:17], v[76:77], 0, v[16:17]
	s_or_b64 s[22:23], vcc, s[22:23]
	global_store_dwordx2 v[16:17], v[18:19], off
	s_andn2_b64 exec, exec, s[22:23]
	s_cbranch_execz .LBB0_327

.LBB0_762:
	v_ashrrev_i32_e32 v1, 31, v0
	v_lshlrev_b64 v[2:3], 6, v[0:1]
	v_lshl_add_u64 v[2:3], s[96:97], 0, v[2:3]
	global_load_dwordx4 v[84:87], v[2:3], off
	global_load_dwordx4 v[88:91], v[2:3], off offset:16
	v_lshlrev_b64 v[72:73], 11, v[0:1]
	global_load_dwordx4 v[94:97], v[2:3], off offset:32
	v_lshl_add_u64 v[72:73], v[26:27], 0, v[72:73]
	global_load_dwordx4 v[98:101], v[72:73], off
	global_load_dwordx4 v[102:105], v[72:73], off offset:16
	global_load_dwordx4 v[106:109], v[2:3], off offset:48
	s_mov_b32 s14, 0x42ee0000
	s_mov_b32 s58, 16
	s_waitcnt vmcnt(5)
	v_mov_b32_e32 v2, v85
	v_mov_b32_e32 v3, v86
	s_waitcnt vmcnt(4)
	v_mov_b32_e32 v72, v89
	v_mov_b32_e32 v73, v90
	v_mov_b32_e32 v85, v87
	v_mov_b32_e32 v89, v91
	s_waitcnt vmcnt(3)
	v_mov_b32_e32 v86, v95
	v_mov_b32_e32 v90, v97
	s_waitcnt vmcnt(2)
	v_lshlrev_b32_e32 v91, 16, v98
	v_pk_add_f32 v[2:3], v[2:3], v[84:85]
	v_pk_add_f32 v[72:73], v[72:73], v[88:89]
	v_pk_add_f32 v[84:85], v[94:95], v[86:87]
	v_pk_add_f32 v[86:87], v[96:97], v[90:91]
	v_pk_add_f32 v[2:3], v[2:3], v[2:3] op_sel:[0,1] op_sel_hi:[1,0]
	v_pk_add_f32 v[72:73], v[72:73], v[72:73] op_sel:[0,1] op_sel_hi:[1,0]
	s_waitcnt vmcnt(0)
	v_mov_b32_e32 v85, v108
	v_mov_b32_e32 v87, v109
	v_mov_b32_e32 v3, v106
	v_mov_b32_e32 v73, v107
	v_pk_add_f32 v[84:85], v[84:85], v[86:87]
	v_pk_add_f32 v[2:3], v[2:3], v[72:73]
	v_and_b32_e32 v98, 0xffff0000, v98
	v_pk_add_f32 v[2:3], v[2:3], v[84:85]
	v_lshlrev_b32_e32 v110, 16, v99
	v_add_f32_e32 v2, v2, v3
	v_fmamk_f32 v2, v2, 0x3a800000, v191
	v_mul_f32_e32 v3, 0x4b800000, v2
	v_cmp_gt_f32_e32 vcc, s18, v2
	v_and_b32_e32 v99, 0xffff0000, v99
	v_lshlrev_b32_e32 v111, 16, v100
	v_cndmask_b32_e32 v2, v2, v3, vcc
	v_rsq_f32_e32 v2, v2
	v_and_b32_e32 v100, 0xffff0000, v100
	v_lshlrev_b32_e32 v112, 16, v101
	v_and_b32_e32 v101, 0xffff0000, v101
	v_mul_f32_e32 v84, 0x45800000, v2
	v_cndmask_b32_e32 v2, v2, v84, vcc
	v_lshlrev_b32_e32 v113, 16, v102
	v_and_b32_e32 v102, 0xffff0000, v102
	v_lshlrev_b32_e32 v114, 16, v103
	v_and_b32_e32 v103, 0xffff0000, v103
	v_lshlrev_b32_e32 v115, 16, v104
	v_and_b32_e32 v3, 0xffff0000, v104
	v_lshlrev_b32_e32 v72, 16, v105
	v_and_b32_e32 v73, 0xffff0000, v105
	v_mul_f32_e32 v84, v2, v91
	v_mul_f32_e32 v85, v2, v98
	v_mul_f32_e32 v86, v2, v110
	v_mul_f32_e32 v87, v2, v99
	v_mul_f32_e32 v88, v2, v111
	v_mul_f32_e32 v89, v2, v100
	v_mul_f32_e32 v90, v2, v112
	v_mul_f32_e32 v91, v2, v101
	v_mul_f32_e32 v95, v2, v113
	v_mul_f32_e32 v96, v2, v102
	v_mul_f32_e32 v97, v2, v114
	v_mul_f32_e32 v98, v2, v103
	v_mul_f32_e32 v99, v2, v115
	v_mul_f32_e32 v100, v2, v3
	v_mul_f32_e32 v72, v2, v72
	v_mul_f32_e32 v73, v2, v73
	v_max_f32_e64 v2, |v84|, |v85|
	v_max_f32_e64 v3, |v86|, |v87|
	v_max_f32_e64 v94, |v88|, |v89|
	v_max_f32_e64 v101, |v90|, |v91|
	v_max3_f32 v2, v2, 0, v3
	v_max_f32_e64 v102, |v95|, |v96|
	v_max_f32_e64 v103, |v97|, |v98|
	v_max3_f32 v2, v2, v94, v101
	v_max_f32_e64 v104, |v99|, |v100|
	v_max_f32_e64 v105, |v72|, |v73|
	v_max3_f32 v2, v2, v102, v103
	v_max3_f32 v2, v2, v104, v105
	v_mov_b32_e32 v3, v2
	s_nop 1
	v_permlane32_swap_b32 v3, v2
	v_add_u32_e32 v94, s86, v0
	v_cmp_gt_i32_e64 s[48:49], s87, v94
	s_waitcnt lgkmcnt(0)
	v_max_f32_e32 v3, v3, v3
	v_max_f32_e32 v2, v2, v3
	v_mov_b32_e32 v3, v2
	s_nop 1
	v_permlane16_swap_b32 v3, v2
	s_waitcnt lgkmcnt(0)
	v_max_f32_e32 v3, v3, v3
	v_max_f32_e32 v2, v2, v3
	s_nop 1
	v_mov_b32_dpp v3, v2 row_ror:8 row_mask:0xf bank_mask:0xf
	s_waitcnt lgkmcnt(0)
	v_max_f32_e32 v3, v3, v3
	v_max_f32_e32 v2, v2, v3
	s_nop 1
	v_mov_b32_dpp v3, v2 row_half_mirror row_mask:0xf bank_mask:0xf
	s_nop 1
	v_mov_b32_dpp v3, v3 quad_perm:[3,2,1,0] row_mask:0xf bank_mask:0xf
	s_waitcnt lgkmcnt(0)
	v_max_f32_e32 v3, v3, v3
	v_max_f32_e32 v2, v2, v3
	s_nop 1
	v_mov_b32_dpp v3, v2 quad_perm:[2,3,0,1] row_mask:0xf bank_mask:0xf
	s_waitcnt lgkmcnt(0)
	v_max_f32_e32 v3, v3, v3
	v_max_f32_e32 v101, v2, v3
	s_nop 1
	v_mov_b32_dpp v102, v101 quad_perm:[1,0,3,2] row_mask:0xf bank_mask:0xf
	v_lshlrev_b64 v[2:3], 10, v[0:1]
	v_lshlrev_b64 v[206:207], 2, v[2:3]
	v_lshl_add_u64 v[206:207], v[28:29], 0, v[206:207]
	global_load_dwordx4 v[208:211], v[206:207], off offset:48
	global_load_dwordx4 v[212:215], v[206:207], off offset:32
	global_load_dwordx4 v[216:219], v[206:207], off offset:16
	global_load_dwordx4 v[220:223], v[206:207], off
	s_waitcnt lgkmcnt(0)
	v_max_f32_e32 v1, v102, v102
	v_max_f32_e32 v101, v101, v1
	v_div_scale_f32 v1, s[12:13], v101, v101, s14
	v_rcp_f32_e32 v102, v1
	v_div_scale_f32 v103, vcc, s14, v101, s14
	s_movk_i32 s12, 0x3fff
	v_fma_f32 v104, -v1, v102, 1.0
	v_fmac_f32_e32 v102, v104, v102
	v_mul_f32_e32 v104, v103, v102
	v_fma_f32 v105, -v1, v104, v103
	v_fmac_f32_e32 v104, v105, v102
	v_fma_f32 v1, -v1, v104, v103
	v_div_fmas_f32 v1, v1, v102, v104
	v_div_fixup_f32 v1, v1, v101, s14
	v_cmp_lt_f32_e32 vcc, 0, v101
	v_cmp_lt_i32_e64 s[50:51], s12, v94
	s_or_b64 s[10:11], s[50:51], s[10:11]
	v_cndmask_b32_e32 v102, 0, v1, vcc
	v_mul_f32_e32 v1, v84, v102
	v_mul_f32_e32 v84, v85, v102
	v_mul_f32_e32 v85, v86, v102
	v_mul_f32_e32 v86, v87, v102
	v_rndne_f32_e32 v1, v1
	v_rndne_f32_e32 v84, v84
	v_mul_f32_e32 v87, v88, v102
	v_mul_f32_e32 v88, v89, v102
	v_rndne_f32_e32 v85, v85
	v_rndne_f32_e32 v86, v86
	v_cvt_i32_f32_e32 v1, v1
	v_cvt_i32_f32_e32 v84, v84
	v_rndne_f32_e32 v87, v87
	v_rndne_f32_e32 v88, v88
	v_cvt_i32_f32_e32 v85, v85
	v_cvt_i32_f32_e32 v86, v86
	v_cvt_i32_f32_e32 v87, v87
	v_cvt_i32_f32_e32 v88, v88
	v_mul_f32_e32 v89, v90, v102
	v_add_u32_e32 v90, 8, v1
	v_add_u32_e32 v104, 8, v84
	v_and_b32_e32 v103, 15, v1
	v_lshlrev_b32_e32 v105, 4, v84
	v_add_u32_e32 v1, v1, v84
	v_lshl_add_u32 v84, v85, 4, v196
	v_lshl_add_u32 v107, v86, 8, v200
	v_lshrrev_b32_e32 v90, 4, v90
	v_and_b32_e32 v104, 0xf0, v104
	v_lshl_add_u32 v109, v87, 12, v201
	v_lshl_add_u32 v111, v88, 16, v202
	v_and_b32_e32 v84, 0xf00, v84
	v_and_b32_e32 v107, 0xf000, v107
	v_and_or_b32 v90, v90, 15, v104
	v_lshlrev_b32_e32 v106, 8, v85
	v_add3_u32 v1, v1, v85, v86
	v_and_b32_e32 v85, 0xf0000, v109
	v_and_b32_e32 v109, 0xf00000, v111
	v_or3_b32 v84, v90, v84, v107
	v_lshlrev_b32_e32 v110, 16, v87
	v_or3_b32 v84, v84, v85, v109
	v_add3_u32 v85, v1, v87, v88
	v_mul_f32_e32 v87, v91, v102
	v_rndne_f32_e32 v89, v89
	v_rndne_f32_e32 v87, v87
	v_cvt_i32_f32_e32 v89, v89
	v_cvt_i32_f32_e32 v87, v87
	v_lshlrev_b32_e32 v108, 12, v86
	v_and_b32_e32 v105, 0xf0, v105
	v_lshl_add_u32 v1, v89, 20, v203
	v_lshl_add_u32 v90, v87, 24, v204
	v_and_b32_e32 v1, 0xf000000, v1
	v_and_b32_e32 v90, 0xf0000000, v90
	v_and_b32_e32 v106, 0xf00, v106
	v_or3_b32 v1, v84, v1, v90
	v_lshl_or_b32 v84, v87, 28, v103
	v_lshlrev_b32_e32 v112, 20, v88
	v_and_b32_e32 v108, 0xf000, v108
	v_and_b32_e32 v86, 0xf0000, v110
	v_lshlrev_b32_e32 v88, 24, v89
	v_or3_b32 v84, v84, v105, v106
	v_and_b32_e32 v110, 0xf00000, v112
	v_and_b32_e32 v88, 0xf000000, v88
	v_or3_b32 v84, v84, v108, v86
	v_or3_b32 v88, v84, v110, v88
	v_add3_u32 v84, v85, v89, v87
	v_mul_f32_e32 v85, v95, v102
	v_mul_f32_e32 v86, v96, v102
	v_rndne_f32_e32 v85, v85
	v_rndne_f32_e32 v86, v86
	v_cvt_i32_f32_e32 v85, v85
	v_cvt_i32_f32_e32 v86, v86
	v_mul_f32_e32 v95, v99, v102
	v_mul_f32_e32 v96, v100, v102
	v_add_u32_e32 v87, 8, v85
	v_add_u32_e32 v89, 8, v86
	v_lshrrev_b32_e32 v87, 4, v87
	v_and_b32_e32 v89, 0xf0, v89
	v_and_or_b32 v87, v87, 15, v89
	v_mul_f32_e32 v89, v97, v102
	v_lshlrev_b32_e32 v91, 4, v86
	v_add3_u32 v84, v84, v85, v86
	v_mul_f32_e32 v86, v98, v102
	v_rndne_f32_e32 v89, v89
	v_rndne_f32_e32 v86, v86
	v_cvt_i32_f32_e32 v89, v89
	v_cvt_i32_f32_e32 v86, v86
	v_rndne_f32_e32 v95, v95
	v_rndne_f32_e32 v96, v96
	v_mul_f32_e32 v72, v72, v102
	v_mul_f32_e32 v73, v73, v102
	v_cvt_i32_f32_e32 v95, v95
	v_cvt_i32_f32_e32 v96, v96
	v_rndne_f32_e32 v72, v72
	v_rndne_f32_e32 v73, v73
	v_cvt_i32_f32_e32 v72, v72
	v_cvt_i32_f32_e32 v73, v73
	v_add3_u32 v84, v84, v89, v86
	v_add3_u32 v84, v84, v95, v96
	v_and_b32_e32 v90, 15, v85
	v_add3_u32 v84, v84, v72, v73
	v_cvt_f32_i32_e32 v84, v84
	v_lshl_add_u32 v85, v89, 4, v196
	v_lshlrev_b32_e32 v89, 8, v89
	v_and_b32_e32 v97, 0xf00, v89
	v_mov_b32_e32 v98, v84
	s_nop 1
	v_permlane32_swap_b32 v98, v84
	v_lshl_add_u32 v89, v86, 8, v200
	v_and_b32_e32 v85, 0xf00, v85
	v_and_b32_e32 v89, 0xf000, v89
	v_or3_b32 v85, v87, v85, v89
	s_waitcnt lgkmcnt(0)
	v_add_f32_e32 v84, v98, v84
	v_mov_b32_e32 v87, v84
	s_nop 1
	v_permlane16_swap_b32 v87, v84
	v_lshl_add_u32 v89, v95, 12, v201
	v_lshl_add_u32 v98, v96, 16, v202
	v_and_b32_e32 v89, 0xf0000, v89
	v_and_b32_e32 v98, 0xf00000, v98
	s_waitcnt lgkmcnt(0)
	v_add_f32_e32 v84, v84, v87
	s_nop 1
	v_mov_b32_dpp v87, v84 row_ror:8 row_mask:0xf bank_mask:0xf
	v_or3_b32 v85, v85, v89, v98
	v_lshlrev_b32_e32 v89, 20, v96
	v_and_b32_e32 v96, 0xf00000, v89
	v_lshl_add_u32 v89, v72, 20, v203
	s_waitcnt lgkmcnt(0)
	v_add_f32_e32 v84, v84, v87
	s_nop 1
	v_mov_b32_dpp v87, v84 row_half_mirror row_mask:0xf bank_mask:0xf
	s_nop 1
	v_mov_b32_dpp v87, v87 quad_perm:[3,2,1,0] row_mask:0xf bank_mask:0xf
	v_lshl_add_u32 v98, v73, 24, v204
	v_and_b32_e32 v89, 0xf000000, v89
	v_and_b32_e32 v98, 0xf0000000, v98
	v_or3_b32 v89, v85, v89, v98
	s_waitcnt lgkmcnt(0)
	v_add_f32_e32 v84, v84, v87
	s_nop 1
	v_mov_b32_dpp v87, v84 quad_perm:[2,3,0,1] row_mask:0xf bank_mask:0xf
	v_and_b32_e32 v91, 0xf0, v91
	v_lshlrev_b32_e32 v86, 12, v86
	v_lshlrev_b32_e32 v95, 16, v95
	v_lshl_or_b32 v73, v73, 28, v90
	s_waitcnt lgkmcnt(0)
	v_add_f32_e32 v84, v84, v87
	s_nop 1
	v_mov_b32_dpp v85, v84 quad_perm:[1,0,3,2] row_mask:0xf bank_mask:0xf
	v_and_b32_e32 v86, 0xf000, v86
	v_and_b32_e32 v95, 0xf0000, v95
	v_lshlrev_b32_e32 v72, 24, v72
	v_or3_b32 v73, v73, v91, v97
	v_and_b32_e32 v72, 0xf000000, v72
	v_or3_b32 v73, v73, v86, v95
	v_or3_b32 v90, v73, v96, v72
	s_waitcnt lgkmcnt(0)
	v_add_f32_e32 v72, v84, v85
	v_mul_f32_e32 v91, 0x3c09ae41, v101
	v_mul_f32_e32 v95, 0.5, v72
	v_mov_b32_e32 v103, 0
	v_mov_b64_e32 v[72:73], v[34:35]
	v_mov_b32_e32 v102, 0
	v_mov_b32_e32 v101, 0
	v_mov_b32_e32 v100, 0
	v_mov_b32_e32 v99, 0
	v_mov_b32_e32 v98, 0
	v_mov_b32_e32 v97, 0
	v_mov_b32_e32 v96, 0
.LBB0_763:
	s_cmpk_eq_i32 s58, 0x80
	s_cselect_b64 s[12:13], -1, 0
	ds_bpermute_b32 v84, v93, v92
	s_and_b64 vcc, s[12:13], s[48:49]
	v_cndmask_b32_e32 v104, v0, v94, vcc
	v_ashrrev_i32_e32 v105, 31, v104
	s_and_b32 s12, s58, 0x70
	v_lshlrev_b64 v[104:105], 9, v[104:105]
	v_lshl_add_u64 v[104:105], s[94:95], 0, v[104:105]
	s_lshl_b32 s36, s12, 2
	s_waitcnt lgkmcnt(0)
	v_ashrrev_i32_e32 v85, 31, v84
	v_lshl_add_u64 v[104:105], v[104:105], 0, s[36:37]
	v_lshl_add_u64 v[84:85], v[84:85], 3, s[8:9]
	v_lshl_add_u64 v[104:105], v[104:105], 0, v[144:145]
	global_load_dwordx2 v[84:85], v[84:85], off
	s_nop 0
	global_load_dword v86, v[72:73], off
	global_load_dword v92, v[104:105], off
	s_waitcnt vmcnt(11)
	v_dot8_i32_i4 v87, v8, v1, 0
	v_dot8_i32_i4 v104, v8, v88, 0
	v_dot8_i32_i4 v87, v9, v89, v87
	v_dot8_i32_i4 v104, v9, v90, v104
	s_waitcnt vmcnt(10)
	v_dot8_i32_i4 v9, v10, v88, 0
	v_dot8_i32_i4 v9, v11, v90, v9
	v_lshl_add_u32 v8, v87, 4, v104
	v_cvt_f32_i32_e32 v87, v8
	v_dot8_i32_i4 v8, v10, v1, 0
	v_dot8_i32_i4 v8, v11, v89, v8
	s_add_i32 s58, s58, 16
	v_lshl_add_u64 v[72:73], v[72:73], 0, 64
	s_waitcnt vmcnt(2)
	v_mul_f32_e32 v85, v91, v85
	v_lshl_add_u32 v8, v8, 4, v9
	v_cvt_f32_i32_e32 v104, v8
	v_dot8_i32_i4 v8, v12, v1, 0
	v_dot8_i32_i4 v9, v12, v88, 0
	v_dot8_i32_i4 v8, v13, v89, v8
	v_dot8_i32_i4 v9, v13, v90, v9
	s_waitcnt vmcnt(0)
	v_readlane_b32 s12, v92, 0
	v_readlane_b32 s28, v92, 8
	v_readlane_b32 s30, v92, 9
	v_lshl_add_u32 v8, v8, 4, v9
	v_cvt_f32_i32_e32 v105, v8
	v_dot8_i32_i4 v8, v14, v1, 0
	v_dot8_i32_i4 v9, v14, v88, 0
	v_dot8_i32_i4 v8, v15, v89, v8
	v_dot8_i32_i4 v9, v15, v90, v9
	s_ashr_i32 s13, s12, 31
	v_readlane_b32 s14, v92, 1
	s_ashr_i32 s29, s28, 31
	v_lshl_add_u32 v8, v8, 4, v9
	v_cvt_f32_i32_e32 v106, v8
	v_dot8_i32_i4 v8, v16, v1, 0
	v_dot8_i32_i4 v9, v16, v88, 0
	v_dot8_i32_i4 v8, v17, v89, v8
	v_dot8_i32_i4 v9, v17, v90, v9
	s_ashr_i32 s31, s30, 31
	v_readlane_b32 s34, v92, 10
	s_lshl_b64 s[12:13], s[12:13], 9
	v_lshl_add_u32 v8, v8, 4, v9
	v_cvt_f32_i32_e32 v107, v8
	v_dot8_i32_i4 v8, v18, v1, 0
	v_dot8_i32_i4 v9, v18, v88, 0
	v_dot8_i32_i4 v8, v19, v89, v8
	v_dot8_i32_i4 v9, v19, v90, v9
	s_ashr_i32 s15, s14, 31
	v_readlane_b32 s16, v92, 2
	s_lshl_b64 s[28:29], s[28:29], 9
	v_lshl_add_u32 v8, v8, 4, v9
	v_cvt_f32_i32_e32 v108, v8
	v_dot8_i32_i4 v8, v20, v1, 0
	v_dot8_i32_i4 v9, v20, v88, 0
	v_dot8_i32_i4 v8, v21, v89, v8
	v_dot8_i32_i4 v9, v21, v90, v9
	s_lshl_b64 s[30:31], s[30:31], 9
	s_ashr_i32 s35, s34, 31
	v_readlane_b32 s38, v92, 11
	v_lshl_add_u32 v8, v8, 4, v9
	v_cvt_f32_i32_e32 v109, v8
	v_dot8_i32_i4 v8, v22, v1, 0
	v_dot8_i32_i4 v9, v22, v88, 0
	v_dot8_i32_i4 v8, v23, v89, v8
	v_dot8_i32_i4 v9, v23, v90, v9
	s_lshl_b64 s[14:15], s[14:15], 9
	s_ashr_i32 s17, s16, 31
	v_readlane_b32 s18, v92, 3
	v_lshl_add_u32 v8, v8, 4, v9
	v_cvt_f32_i32_e32 v110, v8
	v_dot8_i32_i4 v8, v24, v1, 0
	v_dot8_i32_i4 v9, v24, v88, 0
	v_dot8_i32_i4 v8, v25, v89, v8
	v_dot8_i32_i4 v9, v25, v90, v9
	v_lshl_add_u64 v[24:25], v[4:5], 0, s[28:29]
	s_lshl_b64 s[34:35], s[34:35], 9
	s_ashr_i32 s39, s38, 31
	v_lshl_add_u32 v8, v8, 4, v9
	v_cvt_f32_i32_e32 v111, v8
	v_dot8_i32_i4 v8, v38, v1, 0
	v_dot8_i32_i4 v9, v38, v88, 0
	v_dot8_i32_i4 v8, v39, v89, v8
	v_dot8_i32_i4 v9, v39, v90, v9
	v_permlane32_swap_b32 v87, v111
	s_nop 1
	v_lshl_add_u32 v8, v8, 4, v9
	v_cvt_f32_i32_e32 v112, v8
	v_dot8_i32_i4 v8, v50, v1, 0
	v_dot8_i32_i4 v9, v50, v88, 0
	v_dot8_i32_i4 v8, v51, v89, v8
	v_dot8_i32_i4 v9, v51, v90, v9
	s_waitcnt lgkmcnt(0)
	v_add_f32_e32 v87, v87, v111
	v_permlane32_swap_b32 v104, v112
	v_lshl_add_u32 v8, v8, 4, v9
	v_cvt_f32_i32_e32 v113, v8
	v_dot8_i32_i4 v8, v48, v1, 0
	v_dot8_i32_i4 v9, v48, v88, 0
	v_dot8_i32_i4 v8, v49, v89, v8
	v_dot8_i32_i4 v9, v49, v90, v9
	s_waitcnt lgkmcnt(0)
	v_add_f32_e32 v104, v104, v112
	v_permlane32_swap_b32 v105, v113
	v_lshl_add_u32 v8, v8, 4, v9
	v_cvt_f32_i32_e32 v114, v8
	v_dot8_i32_i4 v8, v46, v1, 0
	v_dot8_i32_i4 v9, v46, v88, 0
	v_dot8_i32_i4 v8, v47, v89, v8
	v_dot8_i32_i4 v9, v47, v90, v9
	s_waitcnt lgkmcnt(0)
	v_add_f32_e32 v105, v105, v113
	v_permlane32_swap_b32 v106, v114
	v_lshl_add_u32 v8, v8, 4, v9
	v_cvt_f32_i32_e32 v115, v8
	v_dot8_i32_i4 v8, v44, v1, 0
	v_dot8_i32_i4 v9, v44, v88, 0
	v_dot8_i32_i4 v8, v45, v89, v8
	v_dot8_i32_i4 v9, v45, v90, v9
	s_waitcnt lgkmcnt(0)
	v_add_f32_e32 v106, v106, v114
	v_permlane32_swap_b32 v107, v115
	v_lshl_add_u32 v8, v8, 4, v9
	v_cvt_f32_i32_e32 v116, v8
	v_dot8_i32_i4 v8, v42, v1, 0
	v_dot8_i32_i4 v9, v42, v88, 0
	v_dot8_i32_i4 v8, v43, v89, v8
	v_dot8_i32_i4 v9, v43, v90, v9
	s_waitcnt lgkmcnt(0)
	v_add_f32_e32 v107, v107, v115
	v_permlane32_swap_b32 v108, v116
	v_lshl_add_u32 v8, v8, 4, v9
	v_cvt_f32_i32_e32 v117, v8
	v_dot8_i32_i4 v8, v40, v1, 0
	v_dot8_i32_i4 v9, v40, v88, 0
	v_dot8_i32_i4 v8, v41, v89, v8
	v_dot8_i32_i4 v9, v41, v90, v9
	s_waitcnt lgkmcnt(0)
	v_add_f32_e32 v108, v108, v116
	v_permlane32_swap_b32 v109, v117
	v_lshl_add_u32 v8, v8, 4, v9
	v_cvt_f32_i32_e32 v118, v8
	v_lshl_add_u64 v[38:39], v[4:5], 0, s[30:31]
	s_waitcnt lgkmcnt(0)
	v_add_f32_e32 v109, v109, v117
	v_permlane32_swap_b32 v110, v118
	v_readlane_b32 s50, v92, 12
	s_lshl_b64 s[16:17], s[16:17], 9
	s_ashr_i32 s19, s18, 31
	s_waitcnt lgkmcnt(0)
	v_add_f32_e32 v110, v110, v118
	v_permlane16_swap_b32 v87, v107
	v_readlane_b32 s20, v92, 4
	global_load_dwordx2 v[24:25], v[24:25], off
	v_lshl_add_u64 v[40:41], v[4:5], 0, s[34:35]
	global_load_dwordx2 v[38:39], v[38:39], off
	s_waitcnt lgkmcnt(0)
	v_add_f32_e32 v87, v87, v107
	v_permlane16_swap_b32 v104, v108
	s_lshl_b64 s[38:39], s[38:39], 9
	s_ashr_i32 s51, s50, 31
	v_readlane_b32 s52, v92, 13
	s_waitcnt lgkmcnt(0)
	v_add_f32_e32 v104, v104, v108
	v_permlane16_swap_b32 v105, v109
	s_lshl_b64 s[18:19], s[18:19], 9
	s_ashr_i32 s21, s20, 31
	v_readlane_b32 s22, v92, 5
	s_waitcnt lgkmcnt(0)
	v_add_f32_e32 v105, v105, v109
	v_permlane16_swap_b32 v106, v110
	global_load_dwordx2 v[50:51], v[40:41], off
	s_lshl_b64 s[50:51], s[50:51], 9
	s_ashr_i32 s53, s52, 31
	s_waitcnt lgkmcnt(0)
	v_add_f32_e32 v106, v106, v110
	v_cndmask_b32_e64 v107, v87, v105, s[44:45]
	v_cndmask_b32_e64 v87, v105, v87, s[44:45]
	s_nop 0
	v_mov_b32_dpp v105, v107 row_ror:8 row_mask:0xf bank_mask:0xf
	v_readlane_b32 s54, v92, 14
	s_lshl_b64 s[20:21], s[20:21], 9
	s_ashr_i32 s23, s22, 31
	v_readlane_b32 s24, v92, 6
	s_waitcnt lgkmcnt(0)
	v_add_f32_e32 v87, v87, v105
	v_cndmask_b32_e64 v105, v104, v106, s[44:45]
	s_nop 1
	v_mov_b32_dpp v105, v105 row_ror:8 row_mask:0xf bank_mask:0xf
	v_cndmask_b32_e64 v104, v106, v104, s[44:45]
	s_lshl_b64 s[52:53], s[52:53], 9
	s_ashr_i32 s55, s54, 31
	v_readlane_b32 s56, v92, 15
	s_waitcnt lgkmcnt(0)
	v_add_f32_e32 v104, v104, v105
	v_cndmask_b32_e64 v105, v87, v104, s[46:47]
	v_cndmask_b32_e64 v87, v104, v87, s[46:47]
	s_nop 0
	v_mov_b32_dpp v104, v105 row_half_mirror row_mask:0xf bank_mask:0xf
	s_nop 1
	v_mov_b32_dpp v104, v104 quad_perm:[3,2,1,0] row_mask:0xf bank_mask:0xf
	s_lshl_b64 s[22:23], s[22:23], 9
	s_ashr_i32 s25, s24, 31
	v_readlane_b32 s26, v92, 7
	s_lshl_b64 s[54:55], s[54:55], 9
	s_waitcnt lgkmcnt(0)
	v_add_f32_e32 v87, v87, v104
	s_nop 1
	v_mov_b32_dpp v104, v87 quad_perm:[2,3,0,1] row_mask:0xf bank_mask:0xf
	s_ashr_i32 s57, s56, 31
	s_lshl_b64 s[24:25], s[24:25], 9
	s_ashr_i32 s27, s26, 31
	s_lshl_b64 s[56:57], s[56:57], 9
	s_waitcnt lgkmcnt(0)
	v_add_f32_e32 v87, v87, v104
	s_nop 1
	v_mov_b32_dpp v104, v87 quad_perm:[1,0,3,2] row_mask:0xf bank_mask:0xf
	s_lshl_b64 s[26:27], s[26:27], 9
	v_lshl_add_u64 v[8:9], v[4:5], 0, s[12:13]
	v_lshl_add_u64 v[10:11], v[4:5], 0, s[14:15]
	v_lshl_add_u64 v[12:13], v[4:5], 0, s[16:17]
	s_waitcnt lgkmcnt(0)
	v_add_f32_e32 v87, v87, v104
	v_add_f32_e32 v87, v95, v87
	v_mul_f32_e32 v85, v85, v87
	v_mul_f32_e32 v87, 0x3d372713, v85
	v_mul_f32_e32 v87, v85, v87
	v_fma_f32 v87, v85, v87, v85
	v_mul_f32_e32 v87, 0x3fcc422a, v87
	v_mul_f32_e32 v87, 0xbfb8aa3b, v87
	v_exp_f32_e32 v87, v87
	v_lshlrev_b32_e32 v104, 4, v82
	v_lshl_add_u64 v[14:15], v[4:5], 0, s[18:19]
	v_lshl_add_u64 v[16:17], v[4:5], 0, s[20:21]
	v_add_f32_e32 v87, 1.0, v87
	v_rcp_f32_e32 v87, v87
	v_lshl_add_u64 v[18:19], v[4:5], 0, s[22:23]
	v_lshl_add_u64 v[20:21], v[4:5], 0, s[24:25]
	v_lshl_add_u64 v[22:23], v[4:5], 0, s[26:27]
	v_pk_mul_f32 v[84:85], v[84:85], v[86:87]
	v_lshrrev_b32_e32 v87, 4, v82
	v_pk_mul_f32 v[84:85], v[84:85], v[84:85] op_sel:[0,1] op_sel_hi:[1,0]
	v_cvt_f16_f32_e32 v120, v84
	v_and_b32_e32 v86, 0x7070707, v82
	v_readlane_b32 s36, v120, 0
	v_and_b32_e32 v87, 0x7070707, v87
	v_perm_b32 v86, s2, v205, v86
	v_perm_b32 v87, s2, v205, v87
	v_and_or_b32 v86, v104, s4, v86
	v_and_or_b32 v82, v82, s4, v87
	v_perm_b32 v87, v82, v86, s5
	v_perm_b32 v104, v82, v86, s33
	v_perm_b32 v105, v82, v86, s0
	v_perm_b32 v82, v82, v86, s1
	v_pk_fma_f16 v86, v87, s36, v103 op_sel_hi:[1,0,1]
	v_pk_fma_f16 v87, v104, s36, v102 op_sel_hi:[1,0,1]
	v_lshrrev_b32_e32 v102, 4, v83
	v_pk_fma_f16 v82, v82, s36, v100 op_sel_hi:[1,0,1]
	v_and_b32_e32 v100, 0x7070707, v83
	v_and_b32_e32 v102, 0x7070707, v102
	v_perm_b32 v100, s2, v205, v100
	v_perm_b32 v102, s2, v205, v102
	v_lshlrev_b32_e32 v103, 4, v83
	v_and_or_b32 v100, v103, s4, v100
	v_and_or_b32 v83, v83, s4, v102
	v_perm_b32 v102, v83, v100, s5
	v_perm_b32 v103, v83, v100, s33
	v_perm_b32 v104, v83, v100, s0
	v_perm_b32 v83, v83, v100, s1
	v_readlane_b32 s59, v120, 4
	v_lshrrev_b32_e32 v100, 4, v80
	v_pk_fma_f16 v101, v105, s36, v101 op_sel_hi:[1,0,1]
	v_pk_fma_f16 v99, v102, s36, v99 op_sel_hi:[1,0,1]
	v_pk_fma_f16 v98, v103, s36, v98 op_sel_hi:[1,0,1]
	v_pk_fma_f16 v97, v104, s36, v97 op_sel_hi:[1,0,1]
	v_pk_fma_f16 v83, v83, s36, v96 op_sel_hi:[1,0,1]
	v_and_b32_e32 v96, 0x7070707, v80
	v_and_b32_e32 v100, 0x7070707, v100
	v_perm_b32 v96, s2, v205, v96
	v_perm_b32 v100, s2, v205, v100
	v_lshlrev_b32_e32 v102, 4, v80
	v_and_or_b32 v96, v102, s4, v96
	v_and_or_b32 v80, v80, s4, v100
	v_perm_b32 v100, v80, v96, s5
	v_perm_b32 v102, v80, v96, s33
	v_perm_b32 v103, v80, v96, s0
	v_perm_b32 v80, v80, v96, s1
	v_pk_fma_f16 v86, v100, s59, v86 op_sel_hi:[1,0,1]
	v_lshrrev_b32_e32 v100, 4, v81
	v_pk_fma_f16 v80, v80, s59, v82 op_sel_hi:[1,0,1]
	v_and_b32_e32 v82, 0x7070707, v81
	v_and_b32_e32 v100, 0x7070707, v100
	v_pk_fma_f16 v96, v103, s59, v101 op_sel_hi:[1,0,1]
	v_perm_b32 v82, s2, v205, v82
	v_perm_b32 v100, s2, v205, v100
	v_lshlrev_b32_e32 v101, 4, v81
	v_and_or_b32 v82, v101, s4, v82
	v_and_or_b32 v81, v81, s4, v100
	v_perm_b32 v100, v81, v82, s5
	v_pk_fma_f16 v87, v102, s59, v87 op_sel_hi:[1,0,1]
	v_perm_b32 v101, v81, v82, s33
	v_perm_b32 v102, v81, v82, s0
	v_perm_b32 v81, v81, v82, s1
	v_pk_fma_f16 v82, v100, s59, v99 op_sel_hi:[1,0,1]
	v_readlane_b32 s60, v120, 8
	v_lshrrev_b32_e32 v99, 4, v78
	v_pk_fma_f16 v98, v101, s59, v98 op_sel_hi:[1,0,1]
	v_pk_fma_f16 v97, v102, s59, v97 op_sel_hi:[1,0,1]
	v_pk_fma_f16 v81, v81, s59, v83 op_sel_hi:[1,0,1]
	v_and_b32_e32 v85, 0x7070707, v78
	v_and_b32_e32 v99, 0x7070707, v99
	v_perm_b32 v85, s2, v205, v85
	v_perm_b32 v99, s2, v205, v99
	v_lshlrev_b32_e32 v100, 4, v78
	v_and_or_b32 v85, v100, s4, v85
	v_and_or_b32 v78, v78, s4, v99
	v_perm_b32 v99, v78, v85, s5
	v_perm_b32 v100, v78, v85, s33
	v_perm_b32 v101, v78, v85, s0
	v_perm_b32 v78, v78, v85, s1
	v_pk_fma_f16 v85, v99, s60, v86 op_sel_hi:[1,0,1]
	v_pk_fma_f16 v86, v100, s60, v87 op_sel_hi:[1,0,1]
	v_pk_fma_f16 v87, v101, s60, v96 op_sel_hi:[1,0,1]
	v_lshrrev_b32_e32 v96, 4, v79
	v_pk_fma_f16 v78, v78, s60, v80 op_sel_hi:[1,0,1]
	v_and_b32_e32 v80, 0x7070707, v79
	v_and_b32_e32 v96, 0x7070707, v96
	v_perm_b32 v80, s2, v205, v80
	v_perm_b32 v96, s2, v205, v96
	v_lshlrev_b32_e32 v99, 4, v79
	v_and_or_b32 v80, v99, s4, v80
	v_and_or_b32 v79, v79, s4, v96
	v_perm_b32 v96, v79, v80, s5
	v_perm_b32 v100, v79, v80, s0
	v_perm_b32 v99, v79, v80, s33
	v_perm_b32 v79, v79, v80, s1
	v_pk_fma_f16 v80, v96, s60, v82 op_sel_hi:[1,0,1]
	v_pk_fma_f16 v96, v100, s60, v97 op_sel_hi:[1,0,1]
	v_readlane_b32 s36, v120, 12
	v_lshrrev_b32_e32 v97, 4, v76
	v_pk_fma_f16 v82, v99, s60, v98 op_sel_hi:[1,0,1]
	v_pk_fma_f16 v79, v79, s60, v81 op_sel_hi:[1,0,1]
	v_and_b32_e32 v83, 0x7070707, v76
	v_and_b32_e32 v97, 0x7070707, v97
	v_perm_b32 v83, s2, v205, v83
	v_perm_b32 v97, s2, v205, v97
	v_lshlrev_b32_e32 v98, 4, v76
	v_and_or_b32 v83, v98, s4, v83
	v_and_or_b32 v76, v76, s4, v97
	v_perm_b32 v97, v76, v83, s5
	v_perm_b32 v98, v76, v83, s33
	v_perm_b32 v99, v76, v83, s0
	v_perm_b32 v76, v76, v83, s1
	v_pk_fma_f16 v83, v97, s36, v85 op_sel_hi:[1,0,1]
	v_pk_fma_f16 v85, v98, s36, v86 op_sel_hi:[1,0,1]
	v_pk_fma_f16 v86, v99, s36, v87 op_sel_hi:[1,0,1]
	v_lshrrev_b32_e32 v87, 4, v77
	v_pk_fma_f16 v76, v76, s36, v78 op_sel_hi:[1,0,1]
	v_and_b32_e32 v78, 0x7070707, v77
	v_and_b32_e32 v87, 0x7070707, v87
	v_perm_b32 v78, s2, v205, v78
	v_perm_b32 v87, s2, v205, v87
	v_lshlrev_b32_e32 v97, 4, v77
	v_and_or_b32 v78, v97, s4, v78
	v_and_or_b32 v77, v77, s4, v87
	v_perm_b32 v87, v77, v78, s5
	v_perm_b32 v97, v77, v78, s33
	v_perm_b32 v98, v77, v78, s0
	v_perm_b32 v77, v77, v78, s1
	v_pk_fma_f16 v78, v87, s36, v80 op_sel_hi:[1,0,1]
	v_readlane_b32 s59, v120, 16
	v_lshrrev_b32_e32 v87, 4, v74
	v_pk_fma_f16 v80, v97, s36, v82 op_sel_hi:[1,0,1]
	v_pk_fma_f16 v82, v98, s36, v96 op_sel_hi:[1,0,1]
	v_pk_fma_f16 v77, v77, s36, v79 op_sel_hi:[1,0,1]
	v_and_b32_e32 v81, 0x7070707, v74
	v_and_b32_e32 v87, 0x7070707, v87
	v_perm_b32 v81, s2, v205, v81
	v_perm_b32 v87, s2, v205, v87
	v_lshlrev_b32_e32 v96, 4, v74
	v_and_or_b32 v81, v96, s4, v81
	v_and_or_b32 v74, v74, s4, v87
	v_perm_b32 v87, v74, v81, s5
	v_perm_b32 v96, v74, v81, s33
	v_perm_b32 v97, v74, v81, s0
	v_perm_b32 v74, v74, v81, s1
	v_pk_fma_f16 v81, v87, s59, v83 op_sel_hi:[1,0,1]
	v_pk_fma_f16 v83, v96, s59, v85 op_sel_hi:[1,0,1]
	v_pk_fma_f16 v85, v97, s59, v86 op_sel_hi:[1,0,1]
	v_lshrrev_b32_e32 v86, 4, v75
	v_pk_fma_f16 v74, v74, s59, v76 op_sel_hi:[1,0,1]
	v_and_b32_e32 v76, 0x7070707, v75
	v_and_b32_e32 v86, 0x7070707, v86
	v_perm_b32 v76, s2, v205, v76
	v_perm_b32 v86, s2, v205, v86
	v_lshlrev_b32_e32 v87, 4, v75
	v_and_or_b32 v76, v87, s4, v76
	v_and_or_b32 v75, v75, s4, v86
	v_perm_b32 v86, v75, v76, s5
	v_perm_b32 v87, v75, v76, s33
	v_perm_b32 v96, v75, v76, s0
	v_perm_b32 v75, v75, v76, s1
	v_pk_fma_f16 v76, v86, s59, v78 op_sel_hi:[1,0,1]
	v_pk_fma_f16 v78, v87, s59, v80 op_sel_hi:[1,0,1]
	v_pk_fma_f16 v80, v96, s59, v82 op_sel_hi:[1,0,1]
	v_readlane_b32 s60, v120, 20
	v_lshrrev_b32_e32 v82, 4, v70
	v_pk_fma_f16 v75, v75, s59, v77 op_sel_hi:[1,0,1]
	v_and_b32_e32 v79, 0x7070707, v70
	v_and_b32_e32 v82, 0x7070707, v82
	v_perm_b32 v79, s2, v205, v79
	v_perm_b32 v82, s2, v205, v82
	v_lshlrev_b32_e32 v86, 4, v70
	v_and_or_b32 v79, v86, s4, v79
	v_and_or_b32 v70, v70, s4, v82
	v_perm_b32 v82, v70, v79, s5
	v_perm_b32 v86, v70, v79, s33
	v_perm_b32 v87, v70, v79, s0
	v_perm_b32 v70, v70, v79, s1
	v_pk_fma_f16 v79, v82, s60, v81 op_sel_hi:[1,0,1]
	v_pk_fma_f16 v81, v86, s60, v83 op_sel_hi:[1,0,1]
	v_lshrrev_b32_e32 v83, 4, v71
	v_pk_fma_f16 v70, v70, s60, v74 op_sel_hi:[1,0,1]
	v_and_b32_e32 v74, 0x7070707, v71
	v_and_b32_e32 v83, 0x7070707, v83
	v_pk_fma_f16 v82, v87, s60, v85 op_sel_hi:[1,0,1]
	v_perm_b32 v74, s2, v205, v74
	v_perm_b32 v83, s2, v205, v83
	v_lshlrev_b32_e32 v85, 4, v71
	v_and_or_b32 v74, v85, s4, v74
	v_and_or_b32 v71, v71, s4, v83
	v_perm_b32 v83, v71, v74, s5
	v_perm_b32 v85, v71, v74, s33
	v_perm_b32 v86, v71, v74, s0
	v_perm_b32 v71, v71, v74, s1
	v_pk_fma_f16 v74, v83, s60, v76 op_sel_hi:[1,0,1]
	v_pk_fma_f16 v76, v85, s60, v78 op_sel_hi:[1,0,1]
	v_pk_fma_f16 v78, v86, s60, v80 op_sel_hi:[1,0,1]
	v_readlane_b32 s36, v120, 24
	v_lshrrev_b32_e32 v80, 4, v68
	v_pk_fma_f16 v71, v71, s60, v75 op_sel_hi:[1,0,1]
	v_and_b32_e32 v77, 0x7070707, v68
	v_and_b32_e32 v80, 0x7070707, v80
	v_perm_b32 v77, s2, v205, v77
	v_perm_b32 v80, s2, v205, v80
	v_lshlrev_b32_e32 v83, 4, v68
	v_and_or_b32 v77, v83, s4, v77
	v_and_or_b32 v68, v68, s4, v80
	v_perm_b32 v80, v68, v77, s5
	v_perm_b32 v83, v68, v77, s33
	v_perm_b32 v85, v68, v77, s0
	v_perm_b32 v68, v68, v77, s1
	v_pk_fma_f16 v77, v80, s36, v79 op_sel_hi:[1,0,1]
	v_pk_fma_f16 v79, v83, s36, v81 op_sel_hi:[1,0,1]
	v_lshrrev_b32_e32 v81, 4, v69
	v_pk_fma_f16 v68, v68, s36, v70 op_sel_hi:[1,0,1]
	v_and_b32_e32 v70, 0x7070707, v69
	v_and_b32_e32 v81, 0x7070707, v81
	v_pk_fma_f16 v80, v85, s36, v82 op_sel_hi:[1,0,1]
	v_perm_b32 v70, s2, v205, v70
	v_perm_b32 v81, s2, v205, v81
	v_lshlrev_b32_e32 v82, 4, v69
	v_and_or_b32 v70, v82, s4, v70
	v_and_or_b32 v69, v69, s4, v81
	v_perm_b32 v81, v69, v70, s5
	v_perm_b32 v82, v69, v70, s33
	v_perm_b32 v83, v69, v70, s0
	v_perm_b32 v69, v69, v70, s1
	v_pk_fma_f16 v70, v81, s36, v74 op_sel_hi:[1,0,1]
	v_pk_fma_f16 v74, v82, s36, v76 op_sel_hi:[1,0,1]
	v_pk_fma_f16 v76, v83, s36, v78 op_sel_hi:[1,0,1]
	v_readlane_b32 s59, v120, 28
	v_lshrrev_b32_e32 v78, 4, v64
	v_pk_fma_f16 v69, v69, s36, v71 op_sel_hi:[1,0,1]
	v_and_b32_e32 v75, 0x7070707, v64
	v_and_b32_e32 v78, 0x7070707, v78
	v_perm_b32 v75, s2, v205, v75
	v_perm_b32 v78, s2, v205, v78
	v_lshlrev_b32_e32 v81, 4, v64
	v_and_or_b32 v75, v81, s4, v75
	v_and_or_b32 v64, v64, s4, v78
	v_perm_b32 v78, v64, v75, s5
	v_perm_b32 v81, v64, v75, s33
	v_perm_b32 v82, v64, v75, s0
	v_perm_b32 v64, v64, v75, s1
	v_pk_fma_f16 v75, v78, s59, v77 op_sel_hi:[1,0,1]
	v_pk_fma_f16 v77, v81, s59, v79 op_sel_hi:[1,0,1]
	v_lshrrev_b32_e32 v79, 4, v65
	v_pk_fma_f16 v64, v64, s59, v68 op_sel_hi:[1,0,1]
	v_and_b32_e32 v68, 0x7070707, v65
	v_and_b32_e32 v79, 0x7070707, v79
	v_pk_fma_f16 v78, v82, s59, v80 op_sel_hi:[1,0,1]
	v_perm_b32 v68, s2, v205, v68
	v_perm_b32 v79, s2, v205, v79
	v_lshlrev_b32_e32 v80, 4, v65
	v_and_or_b32 v68, v80, s4, v68
	v_and_or_b32 v65, v65, s4, v79
	v_perm_b32 v79, v65, v68, s5
	v_perm_b32 v80, v65, v68, s33
	v_perm_b32 v81, v65, v68, s0
	v_perm_b32 v65, v65, v68, s1
	v_pk_fma_f16 v68, v79, s59, v70 op_sel_hi:[1,0,1]
	v_pk_fma_f16 v70, v80, s59, v74 op_sel_hi:[1,0,1]
	v_pk_fma_f16 v74, v81, s59, v76 op_sel_hi:[1,0,1]
	v_readlane_b32 s60, v120, 32
	v_lshrrev_b32_e32 v76, 4, v62
	v_pk_fma_f16 v65, v65, s59, v69 op_sel_hi:[1,0,1]
	v_and_b32_e32 v71, 0x7070707, v62
	v_and_b32_e32 v76, 0x7070707, v76
	v_perm_b32 v71, s2, v205, v71
	v_perm_b32 v76, s2, v205, v76
	v_lshlrev_b32_e32 v79, 4, v62
	v_and_or_b32 v71, v79, s4, v71
	v_and_or_b32 v62, v62, s4, v76
	v_perm_b32 v76, v62, v71, s5
	v_perm_b32 v79, v62, v71, s33
	v_perm_b32 v80, v62, v71, s0
	v_perm_b32 v62, v62, v71, s1
	v_pk_fma_f16 v71, v76, s60, v75 op_sel_hi:[1,0,1]
	v_pk_fma_f16 v75, v79, s60, v77 op_sel_hi:[1,0,1]
	v_lshrrev_b32_e32 v77, 4, v63
	v_pk_fma_f16 v62, v62, s60, v64 op_sel_hi:[1,0,1]
	v_and_b32_e32 v64, 0x7070707, v63
	v_and_b32_e32 v77, 0x7070707, v77
	v_pk_fma_f16 v76, v80, s60, v78 op_sel_hi:[1,0,1]
	v_perm_b32 v64, s2, v205, v64
	v_perm_b32 v77, s2, v205, v77
	v_lshlrev_b32_e32 v78, 4, v63
	v_and_or_b32 v64, v78, s4, v64
	v_and_or_b32 v63, v63, s4, v77
	v_perm_b32 v77, v63, v64, s5
	v_perm_b32 v78, v63, v64, s33
	v_perm_b32 v79, v63, v64, s0
	v_perm_b32 v63, v63, v64, s1
	v_pk_fma_f16 v64, v77, s60, v68 op_sel_hi:[1,0,1]
	v_pk_fma_f16 v68, v78, s60, v70 op_sel_hi:[1,0,1]
	v_pk_fma_f16 v70, v79, s60, v74 op_sel_hi:[1,0,1]
	v_readlane_b32 s36, v120, 36
	v_lshrrev_b32_e32 v74, 4, v66
	v_pk_fma_f16 v63, v63, s60, v65 op_sel_hi:[1,0,1]
	v_and_b32_e32 v69, 0x7070707, v66
	v_and_b32_e32 v74, 0x7070707, v74
	v_perm_b32 v69, s2, v205, v69
	v_perm_b32 v74, s2, v205, v74
	v_lshlrev_b32_e32 v77, 4, v66
	v_and_or_b32 v69, v77, s4, v69
	v_and_or_b32 v66, v66, s4, v74
	v_perm_b32 v74, v66, v69, s5
	v_perm_b32 v77, v66, v69, s33
	v_perm_b32 v78, v66, v69, s0
	v_perm_b32 v66, v66, v69, s1
	v_pk_fma_f16 v69, v74, s36, v71 op_sel_hi:[1,0,1]
	v_pk_fma_f16 v71, v77, s36, v75 op_sel_hi:[1,0,1]
	v_lshrrev_b32_e32 v75, 4, v67
	v_pk_fma_f16 v62, v66, s36, v62 op_sel_hi:[1,0,1]
	v_and_b32_e32 v66, 0x7070707, v67
	v_and_b32_e32 v75, 0x7070707, v75
	v_pk_fma_f16 v74, v78, s36, v76 op_sel_hi:[1,0,1]
	v_perm_b32 v66, s2, v205, v66
	v_perm_b32 v75, s2, v205, v75
	v_lshlrev_b32_e32 v76, 4, v67
	v_and_or_b32 v66, v76, s4, v66
	v_and_or_b32 v67, v67, s4, v75
	v_perm_b32 v76, v67, v66, s33
	v_perm_b32 v77, v67, v66, s0
	v_perm_b32 v75, v67, v66, s5
	v_perm_b32 v66, v67, v66, s1
	v_pk_fma_f16 v67, v76, s36, v68 op_sel_hi:[1,0,1]
	v_pk_fma_f16 v68, v77, s36, v70 op_sel_hi:[1,0,1]
	v_readlane_b32 s59, v120, 40
	v_lshrrev_b32_e32 v70, 4, v60
	v_pk_fma_f16 v64, v75, s36, v64 op_sel_hi:[1,0,1]
	v_pk_fma_f16 v63, v66, s36, v63 op_sel_hi:[1,0,1]
	v_and_b32_e32 v66, 0x7070707, v60
	v_and_b32_e32 v70, 0x7070707, v70
	v_perm_b32 v66, s2, v205, v66
	v_perm_b32 v70, s2, v205, v70
	v_lshlrev_b32_e32 v75, 4, v60
	v_and_or_b32 v66, v75, s4, v66
	v_and_or_b32 v60, v60, s4, v70
	v_perm_b32 v70, v60, v66, s5
	v_perm_b32 v75, v60, v66, s33
	v_perm_b32 v76, v60, v66, s0
	v_perm_b32 v60, v60, v66, s1
	v_pk_fma_f16 v66, v70, s59, v69 op_sel_hi:[1,0,1]
	v_pk_fma_f16 v69, v75, s59, v71 op_sel_hi:[1,0,1]
	v_lshrrev_b32_e32 v71, 4, v61
	v_pk_fma_f16 v60, v60, s59, v62 op_sel_hi:[1,0,1]
	v_and_b32_e32 v62, 0x7070707, v61
	v_and_b32_e32 v71, 0x7070707, v71
	v_pk_fma_f16 v70, v76, s59, v74 op_sel_hi:[1,0,1]
	v_perm_b32 v62, s2, v205, v62
	v_perm_b32 v71, s2, v205, v71
	v_lshlrev_b32_e32 v74, 4, v61
	v_and_or_b32 v62, v74, s4, v62
	v_and_or_b32 v61, v61, s4, v71
	v_perm_b32 v71, v61, v62, s5
	v_perm_b32 v74, v61, v62, s33
	v_perm_b32 v75, v61, v62, s0
	v_perm_b32 v61, v61, v62, s1
	v_pk_fma_f16 v62, v71, s59, v64 op_sel_hi:[1,0,1]
	v_pk_fma_f16 v64, v74, s59, v67 op_sel_hi:[1,0,1]
	v_pk_fma_f16 v67, v75, s59, v68 op_sel_hi:[1,0,1]
	v_readlane_b32 s60, v120, 44
	v_lshrrev_b32_e32 v68, 4, v58
	v_pk_fma_f16 v61, v61, s59, v63 op_sel_hi:[1,0,1]
	v_and_b32_e32 v65, 0x7070707, v58
	v_and_b32_e32 v68, 0x7070707, v68
	v_perm_b32 v65, s2, v205, v65
	v_perm_b32 v68, s2, v205, v68
	v_lshlrev_b32_e32 v71, 4, v58
	v_and_or_b32 v65, v71, s4, v65
	v_and_or_b32 v58, v58, s4, v68
	v_perm_b32 v68, v58, v65, s5
	v_perm_b32 v71, v58, v65, s33
	v_perm_b32 v74, v58, v65, s0
	v_perm_b32 v58, v58, v65, s1
	v_pk_fma_f16 v65, v68, s60, v66 op_sel_hi:[1,0,1]
	v_pk_fma_f16 v66, v71, s60, v69 op_sel_hi:[1,0,1]
	v_lshrrev_b32_e32 v69, 4, v59
	v_pk_fma_f16 v58, v58, s60, v60 op_sel_hi:[1,0,1]
	v_and_b32_e32 v60, 0x7070707, v59
	v_and_b32_e32 v69, 0x7070707, v69
	v_pk_fma_f16 v68, v74, s60, v70 op_sel_hi:[1,0,1]
	v_perm_b32 v60, s2, v205, v60
	v_perm_b32 v69, s2, v205, v69
	v_lshlrev_b32_e32 v70, 4, v59
	v_and_or_b32 v60, v70, s4, v60
	v_and_or_b32 v59, v59, s4, v69
	v_perm_b32 v69, v59, v60, s5
	v_perm_b32 v70, v59, v60, s33
	v_perm_b32 v71, v59, v60, s0
	v_perm_b32 v59, v59, v60, s1
	v_pk_fma_f16 v60, v69, s60, v62 op_sel_hi:[1,0,1]
	v_pk_fma_f16 v62, v70, s60, v64 op_sel_hi:[1,0,1]
	v_pk_fma_f16 v64, v71, s60, v67 op_sel_hi:[1,0,1]
	v_readlane_b32 s36, v120, 48
	v_lshrrev_b32_e32 v67, 4, v56
	v_pk_fma_f16 v59, v59, s60, v61 op_sel_hi:[1,0,1]
	v_and_b32_e32 v63, 0x7070707, v56
	v_and_b32_e32 v67, 0x7070707, v67
	v_perm_b32 v63, s2, v205, v63
	v_perm_b32 v67, s2, v205, v67
	v_lshlrev_b32_e32 v69, 4, v56
	v_and_or_b32 v63, v69, s4, v63
	v_and_or_b32 v56, v56, s4, v67
	v_perm_b32 v67, v56, v63, s5
	v_perm_b32 v69, v56, v63, s33
	v_perm_b32 v70, v56, v63, s0
	v_perm_b32 v56, v56, v63, s1
	v_pk_fma_f16 v63, v67, s36, v65 op_sel_hi:[1,0,1]
	v_lshrrev_b32_e32 v67, 4, v57
	v_pk_fma_f16 v56, v56, s36, v58 op_sel_hi:[1,0,1]
	v_and_b32_e32 v58, 0x7070707, v57
	v_and_b32_e32 v67, 0x7070707, v67
	v_pk_fma_f16 v65, v69, s36, v66 op_sel_hi:[1,0,1]
	v_pk_fma_f16 v66, v70, s36, v68 op_sel_hi:[1,0,1]
	v_perm_b32 v58, s2, v205, v58
	v_perm_b32 v67, s2, v205, v67
	v_lshlrev_b32_e32 v68, 4, v57
	v_and_or_b32 v58, v68, s4, v58
	v_and_or_b32 v57, v57, s4, v67
	v_perm_b32 v67, v57, v58, s5
	v_perm_b32 v68, v57, v58, s33
	v_perm_b32 v69, v57, v58, s0
	v_perm_b32 v57, v57, v58, s1
	v_pk_fma_f16 v58, v67, s36, v60 op_sel_hi:[1,0,1]
	v_pk_fma_f16 v60, v68, s36, v62 op_sel_hi:[1,0,1]
	v_pk_fma_f16 v62, v69, s36, v64 op_sel_hi:[1,0,1]
	v_readlane_b32 s59, v120, 52
	v_lshrrev_b32_e32 v64, 4, v54
	v_pk_fma_f16 v57, v57, s36, v59 op_sel_hi:[1,0,1]
	v_and_b32_e32 v61, 0x7070707, v54
	v_and_b32_e32 v64, 0x7070707, v64
	v_perm_b32 v61, s2, v205, v61
	v_perm_b32 v64, s2, v205, v64
	v_lshlrev_b32_e32 v67, 4, v54
	v_and_or_b32 v61, v67, s4, v61
	v_and_or_b32 v54, v54, s4, v64
	v_perm_b32 v64, v54, v61, s5
	v_perm_b32 v67, v54, v61, s33
	v_perm_b32 v68, v54, v61, s0
	v_perm_b32 v54, v54, v61, s1
	v_pk_fma_f16 v61, v64, s59, v63 op_sel_hi:[1,0,1]
	v_pk_fma_f16 v63, v67, s59, v65 op_sel_hi:[1,0,1]
	v_lshrrev_b32_e32 v65, 4, v55
	v_pk_fma_f16 v54, v54, s59, v56 op_sel_hi:[1,0,1]
	v_and_b32_e32 v56, 0x7070707, v55
	v_and_b32_e32 v65, 0x7070707, v65
	v_pk_fma_f16 v64, v68, s59, v66 op_sel_hi:[1,0,1]
	v_perm_b32 v56, s2, v205, v56
	v_perm_b32 v65, s2, v205, v65
	v_lshlrev_b32_e32 v66, 4, v55
	v_and_or_b32 v56, v66, s4, v56
	v_and_or_b32 v55, v55, s4, v65
	v_perm_b32 v65, v55, v56, s5
	v_perm_b32 v66, v55, v56, s33
	v_perm_b32 v67, v55, v56, s0
	v_perm_b32 v55, v55, v56, s1
	v_pk_fma_f16 v56, v65, s59, v58 op_sel_hi:[1,0,1]
	v_pk_fma_f16 v58, v66, s59, v60 op_sel_hi:[1,0,1]
	v_pk_fma_f16 v60, v67, s59, v62 op_sel_hi:[1,0,1]
	v_readlane_b32 s60, v120, 56
	v_lshrrev_b32_e32 v62, 4, v52
	v_pk_fma_f16 v55, v55, s59, v57 op_sel_hi:[1,0,1]
	v_and_b32_e32 v59, 0x7070707, v52
	v_and_b32_e32 v62, 0x7070707, v62
	v_perm_b32 v59, s2, v205, v59
	v_perm_b32 v62, s2, v205, v62
	v_lshlrev_b32_e32 v65, 4, v52
	v_and_or_b32 v59, v65, s4, v59
	v_and_or_b32 v52, v52, s4, v62
	v_perm_b32 v62, v52, v59, s5
	v_perm_b32 v65, v52, v59, s33
	v_perm_b32 v66, v52, v59, s0
	v_perm_b32 v52, v52, v59, s1
	v_pk_fma_f16 v59, v62, s60, v61 op_sel_hi:[1,0,1]
	v_pk_fma_f16 v61, v65, s60, v63 op_sel_hi:[1,0,1]
	v_lshrrev_b32_e32 v63, 4, v53
	v_pk_fma_f16 v52, v52, s60, v54 op_sel_hi:[1,0,1]
	v_and_b32_e32 v54, 0x7070707, v53
	v_and_b32_e32 v63, 0x7070707, v63
	v_pk_fma_f16 v62, v66, s60, v64 op_sel_hi:[1,0,1]
	v_perm_b32 v54, s2, v205, v54
	v_perm_b32 v63, s2, v205, v63
	v_lshlrev_b32_e32 v64, 4, v53
	v_and_or_b32 v54, v64, s4, v54
	v_and_or_b32 v53, v53, s4, v63
	v_perm_b32 v63, v53, v54, s5
	v_perm_b32 v64, v53, v54, s33
	v_perm_b32 v65, v53, v54, s0
	v_perm_b32 v53, v53, v54, s1
	v_pk_fma_f16 v54, v63, s60, v56 op_sel_hi:[1,0,1]
	v_pk_fma_f16 v56, v64, s60, v58 op_sel_hi:[1,0,1]
	v_pk_fma_f16 v58, v65, s60, v60 op_sel_hi:[1,0,1]
	v_readlane_b32 s36, v120, 60
	v_lshrrev_b32_e32 v60, 4, v36
	v_pk_fma_f16 v53, v53, s60, v55 op_sel_hi:[1,0,1]
	v_and_b32_e32 v57, 0x7070707, v36
	v_and_b32_e32 v60, 0x7070707, v60
	v_perm_b32 v57, s2, v205, v57
	v_perm_b32 v60, s2, v205, v60
	v_lshlrev_b32_e32 v63, 4, v36
	v_and_or_b32 v57, v63, s4, v57
	v_and_or_b32 v36, v36, s4, v60
	v_perm_b32 v60, v36, v57, s5
	v_perm_b32 v63, v36, v57, s33
	v_perm_b32 v64, v36, v57, s0
	v_perm_b32 v36, v36, v57, s1
	v_pk_fma_f16 v100, v36, s36, v52 op_sel_hi:[1,0,1]
	v_lshrrev_b32_e32 v52, 4, v37
	v_and_b32_e32 v36, 0x7070707, v37
	v_and_b32_e32 v52, 0x7070707, v52
	v_perm_b32 v36, s2, v205, v36
	v_perm_b32 v52, s2, v205, v52
	v_lshlrev_b32_e32 v57, 4, v37
	v_and_or_b32 v36, v57, s4, v36
	v_and_or_b32 v37, v37, s4, v52
	v_pk_fma_f16 v103, v60, s36, v59 op_sel_hi:[1,0,1]
	v_perm_b32 v52, v37, v36, s5
	v_perm_b32 v57, v37, v36, s33
	v_perm_b32 v59, v37, v36, s0
	v_perm_b32 v36, v37, v36, s1
	v_pk_fma_f16 v96, v36, s36, v53 op_sel_hi:[1,0,1]
	v_lshl_add_u64 v[36:37], v[6:7], 0, s[12:13]
	global_load_dwordx2 v[82:83], v[36:37], off
	v_lshl_add_u64 v[36:37], v[6:7], 0, s[14:15]
	global_load_dwordx2 v[80:81], v[36:37], off
	v_lshl_add_u64 v[40:41], v[4:5], 0, s[38:39]
	v_lshl_add_u64 v[36:37], v[6:7], 0, s[16:17]
	global_load_dwordx2 v[48:49], v[40:41], off
	global_load_dwordx2 v[78:79], v[36:37], off
	v_lshl_add_u64 v[40:41], v[4:5], 0, s[50:51]
	v_lshl_add_u64 v[36:37], v[6:7], 0, s[18:19]
	global_load_dwordx2 v[46:47], v[40:41], off
	global_load_dwordx2 v[76:77], v[36:37], off
	v_lshl_add_u64 v[40:41], v[4:5], 0, s[52:53]
	v_lshl_add_u64 v[36:37], v[6:7], 0, s[20:21]
	global_load_dwordx2 v[44:45], v[40:41], off
	global_load_dwordx2 v[74:75], v[36:37], off
	v_lshl_add_u64 v[40:41], v[4:5], 0, s[54:55]
	v_lshl_add_u64 v[36:37], v[6:7], 0, s[22:23]
	global_load_dwordx2 v[42:43], v[40:41], off
	global_load_dwordx2 v[70:71], v[36:37], off
	v_lshl_add_u64 v[40:41], v[4:5], 0, s[56:57]
	v_lshl_add_u64 v[36:37], v[6:7], 0, s[24:25]
	global_load_dwordx2 v[40:41], v[40:41], off
	v_pk_fma_f16 v101, v64, s36, v62 op_sel_hi:[1,0,1]
	global_load_dwordx2 v[68:69], v[36:37], off
	v_lshl_add_u64 v[36:37], v[6:7], 0, s[26:27]
	global_load_dwordx2 v[64:65], v[36:37], off
	v_lshl_add_u64 v[36:37], v[6:7], 0, s[28:29]
	v_pk_fma_f16 v102, v63, s36, v61 op_sel_hi:[1,0,1]
	global_load_dwordx2 v[62:63], v[36:37], off
	v_lshl_add_u64 v[36:37], v[6:7], 0, s[30:31]
	global_load_dwordx2 v[66:67], v[36:37], off
	v_lshl_add_u64 v[36:37], v[6:7], 0, s[34:35]
	global_load_dwordx2 v[60:61], v[36:37], off
	v_lshl_add_u64 v[36:37], v[6:7], 0, s[38:39]
	v_pk_fma_f16 v97, v59, s36, v58 op_sel_hi:[1,0,1]
	global_load_dwordx2 v[58:59], v[36:37], off
	v_lshl_add_u64 v[36:37], v[6:7], 0, s[50:51]
	v_pk_fma_f16 v98, v57, s36, v56 op_sel_hi:[1,0,1]
	global_load_dwordx2 v[56:57], v[36:37], off
	v_lshl_add_u64 v[36:37], v[6:7], 0, s[52:53]
	v_pk_fma_f16 v99, v52, s36, v54 op_sel_hi:[1,0,1]
	global_load_dwordx2 v[54:55], v[36:37], off
	v_lshl_add_u64 v[36:37], v[6:7], 0, s[54:55]
	global_load_dwordx2 v[52:53], v[36:37], off
	v_lshl_add_u64 v[36:37], v[6:7], 0, s[56:57]
	global_load_dwordx2 v[8:9], v[8:9], off
	s_cmpk_eq_i32 s58, 0x90
	global_load_dwordx2 v[10:11], v[10:11], off
	s_nop 0
	global_load_dwordx2 v[12:13], v[12:13], off
	s_nop 0
	global_load_dwordx2 v[14:15], v[14:15], off
	s_nop 0
	global_load_dwordx2 v[16:17], v[16:17], off
	s_nop 0
	global_load_dwordx2 v[18:19], v[18:19], off
	s_nop 0
	global_load_dwordx2 v[20:21], v[20:21], off
	s_nop 0
	global_load_dwordx2 v[22:23], v[22:23], off
	s_nop 0
	global_load_dwordx2 v[36:37], v[36:37], off
	s_cbranch_scc0 .LBB0_763
	v_lshlrev_b64 v[0:1], 2, v[2:3]
	v_lshl_add_u64 v[2:3], v[28:29], 0, v[0:1]
	v_mov_b32_e32 v104, v208
	v_mov_b32_e32 v105, v209
	v_mov_b32_e32 v106, v210
	v_mov_b32_e32 v107, v211
	v_mov_b32_e32 v108, v212
	v_mov_b32_e32 v109, v213
	v_mov_b32_e32 v110, v214
	v_mov_b32_e32 v111, v215
	v_mov_b32_e32 v86, v216
	v_mov_b32_e32 v87, v217
	v_mov_b32_e32 v88, v218
	v_mov_b32_e32 v89, v219
	v_mov_b32_e32 v112, v220
	v_mov_b32_e32 v113, v221
	v_mov_b32_e32 v114, v222
	v_mov_b32_e32 v115, v223
	v_lshl_add_u64 v[72:73], v[32:33], 0, v[0:1]
	v_cvt_f32_f16_sdwa v1, v103 dst_sel:DWORD dst_unused:UNUSED_PAD src0_sel:WORD_1
	v_cvt_f32_f16_e32 v0, v103
	v_cvt_f32_f16_sdwa v91, v102 dst_sel:DWORD dst_unused:UNUSED_PAD src0_sel:WORD_1
	v_cvt_f32_f16_e32 v90, v102
	v_cvt_f32_f16_sdwa v103, v101 dst_sel:DWORD dst_unused:UNUSED_PAD src0_sel:WORD_1
	v_cvt_f32_f16_e32 v102, v101
	v_cvt_f32_f16_sdwa v101, v100 dst_sel:DWORD dst_unused:UNUSED_PAD src0_sel:WORD_1
	v_cvt_f32_f16_e32 v100, v100
	s_mov_b32 s18, 0x800000
	v_readlane_b32 s12, v255, 5
	v_readlane_b32 s13, v255, 6
	v_pk_add_f32 v[86:87], v[86:87], v[102:103]
	v_pk_add_f32 v[84:85], v[112:113], v[0:1]
	v_mov_b32_e32 v102, v85
	v_mov_b32_e32 v103, v87
	v_pk_add_f32 v[90:91], v[114:115], v[90:91]
	v_pk_add_f32 v[88:89], v[88:89], v[100:101]
	v_mov_b32_e32 v100, v84
	v_mov_b32_e32 v101, v86
	v_pk_mul_f32 v[102:103], v[102:103], v[102:103]
	v_mov_b32_e32 v112, v91
	v_pk_fma_f32 v[100:101], v[100:101], v[100:101], v[102:103]
	v_mov_b32_e32 v102, v90
	v_mov_b32_e32 v103, v88
	v_pk_fma_f32 v[100:101], v[102:103], v[102:103], v[100:101]
	v_cvt_f32_f16_sdwa v103, v99 dst_sel:DWORD dst_unused:UNUSED_PAD src0_sel:WORD_1
	v_cvt_f32_f16_e32 v102, v99
	v_cvt_f32_f16_sdwa v99, v98 dst_sel:DWORD dst_unused:UNUSED_PAD src0_sel:WORD_1
	v_cvt_f32_f16_e32 v98, v98
	v_mov_b32_e32 v113, v89
	v_pk_add_f32 v[102:103], v[108:109], v[102:103]
	v_cvt_f32_f16_sdwa v109, v97 dst_sel:DWORD dst_unused:UNUSED_PAD src0_sel:WORD_1
	v_cvt_f32_f16_e32 v108, v97
	v_cvt_f32_f16_sdwa v97, v96 dst_sel:DWORD dst_unused:UNUSED_PAD src0_sel:WORD_1
	v_cvt_f32_f16_e32 v96, v96
	v_pk_add_f32 v[98:99], v[110:111], v[98:99]
	v_pk_add_f32 v[104:105], v[104:105], v[108:109]
	v_mov_b32_e32 v108, v103
	v_mov_b32_e32 v109, v105
	v_pk_add_f32 v[96:97], v[106:107], v[96:97]
	v_mov_b32_e32 v106, v102
	v_mov_b32_e32 v107, v104
	v_pk_mul_f32 v[108:109], v[108:109], v[108:109]
	v_pk_fma_f32 v[100:101], v[112:113], v[112:113], v[100:101]
	v_pk_fma_f32 v[106:107], v[106:107], v[106:107], v[108:109]
	v_mov_b32_e32 v108, v98
	v_mov_b32_e32 v109, v96
	v_mov_b32_e32 v110, v99
	v_mov_b32_e32 v111, v97
	v_pk_fma_f32 v[106:107], v[108:109], v[108:109], v[106:107]
	v_add_f32_e32 v95, v100, v101
	v_pk_fma_f32 v[106:107], v[110:111], v[110:111], v[106:107]
	v_lshl_add_u64 v[34:35], v[34:35], 0, s[12:13]
	v_add_f32_e32 v95, v95, v106
	v_add_f32_e32 v95, v95, v107
	v_mov_b32_e32 v100, v95
	s_nop 1
	v_permlane32_swap_b32 v100, v95
	s_waitcnt lgkmcnt(0)
	v_add_f32_e32 v95, v95, v100
	v_mov_b32_e32 v100, v95
	s_nop 1
	v_permlane16_swap_b32 v100, v95
	s_waitcnt lgkmcnt(0)
	v_add_f32_e32 v95, v95, v100
	s_nop 1
	v_mov_b32_dpp v100, v95 row_ror:8 row_mask:0xf bank_mask:0xf
	s_waitcnt lgkmcnt(0)
	v_add_f32_e32 v95, v95, v100
	s_nop 1
	v_mov_b32_dpp v100, v95 row_half_mirror row_mask:0xf bank_mask:0xf
	s_nop 1
	v_mov_b32_dpp v100, v100 quad_perm:[3,2,1,0] row_mask:0xf bank_mask:0xf
	s_waitcnt lgkmcnt(0)
	v_add_f32_e32 v95, v95, v100
	s_nop 1
	v_mov_b32_dpp v100, v95 quad_perm:[2,3,0,1] row_mask:0xf bank_mask:0xf
	s_waitcnt lgkmcnt(0)
	v_add_f32_e32 v95, v95, v100
	s_nop 1
	v_mov_b32_dpp v100, v95 quad_perm:[1,0,3,2] row_mask:0xf bank_mask:0xf
	s_waitcnt lgkmcnt(0)
	v_add_f32_e32 v95, v95, v100
	v_fmamk_f32 v95, v95, 0x3a800000, v191
	v_cmp_gt_f32_e32 vcc, s18, v95
	v_mul_f32_e32 v100, 0x4b800000, v95
	s_nop 0
	v_cndmask_b32_e32 v95, v95, v100, vcc
	v_rsq_f32_e32 v95, v95
	s_nop 0
	v_mul_f32_e32 v100, 0x45800000, v95
	v_cndmask_b32_e32 v100, v95, v100, vcc
	v_pk_mul_f32 v[84:85], v[84:85], v[100:101] op_sel_hi:[1,0]
	v_pk_mul_f32 v[0:1], v[124:125], v[84:85]
	v_pk_mul_f32 v[84:85], v[90:91], v[100:101] op_sel_hi:[1,0]
	s_nop 0
	v_pk_mul_f32 v[2:3], v[126:127], v[84:85]
	global_store_dwordx4 v[72:73], v[0:3], off
	s_nop 1
	v_pk_mul_f32 v[84:85], v[86:87], v[100:101] op_sel_hi:[1,0]
	v_pk_mul_f32 v[0:1], v[128:129], v[84:85]
	v_pk_mul_f32 v[84:85], v[88:89], v[100:101] op_sel_hi:[1,0]
	s_nop 0
	v_pk_mul_f32 v[2:3], v[130:131], v[84:85]
	global_store_dwordx4 v[72:73], v[0:3], off offset:16
	s_nop 1
	v_pk_mul_f32 v[84:85], v[102:103], v[100:101] op_sel_hi:[1,0]
	v_pk_mul_f32 v[0:1], v[84:85], v[132:133]
	v_pk_mul_f32 v[84:85], v[98:99], v[100:101] op_sel_hi:[1,0]
	s_nop 0
	v_pk_mul_f32 v[2:3], v[84:85], v[134:135]
	global_store_dwordx4 v[72:73], v[0:3], off offset:32
	s_nop 1
	v_pk_mul_f32 v[84:85], v[104:105], v[100:101] op_sel_hi:[1,0]
	v_pk_mul_f32 v[0:1], v[84:85], v[136:137]
	v_pk_mul_f32 v[84:85], v[96:97], v[100:101] op_sel_hi:[1,0]
	s_nop 0
	v_pk_mul_f32 v[2:3], v[84:85], v[138:139]
	global_store_dwordx4 v[72:73], v[0:3], off offset:48
	s_nop 1
	v_mov_b32_e32 v0, v94
	s_andn2_b64 exec, exec, s[10:11]
	s_cbranch_execnz .LBB0_762

.LBB0_769:
	v_ashrrev_i32_e32 v1, 31, v0
	v_lshlrev_b64 v[2:3], 6, v[0:1]
	v_lshl_add_u64 v[14:15], s[96:97], 0, v[2:3]
	global_load_dwordx4 v[2:5], v[14:15], off
	global_load_dwordx4 v[6:9], v[14:15], off offset:16
	v_lshlrev_b64 v[74:75], 11, v[0:1]
	global_load_dwordx4 v[10:13], v[14:15], off offset:32
	v_lshl_add_u64 v[74:75], v[42:43], 0, v[74:75]
	global_load_dwordx4 v[98:101], v[74:75], off
	global_load_dwordx4 v[102:105], v[74:75], off offset:16
	global_load_dwordx4 v[106:109], v[14:15], off offset:48
	s_mov_b32 s56, 16
	s_waitcnt vmcnt(5)
	v_mov_b32_e32 v14, v3
	v_mov_b32_e32 v15, v4
	s_waitcnt vmcnt(4)
	v_mov_b32_e32 v94, v7
	v_mov_b32_e32 v95, v8
	v_mov_b32_e32 v3, v5
	v_mov_b32_e32 v7, v9
	s_waitcnt vmcnt(3)
	v_mov_b32_e32 v4, v11
	v_mov_b32_e32 v8, v13
	v_pk_add_f32 v[2:3], v[14:15], v[2:3]
	v_pk_add_f32 v[6:7], v[94:95], v[6:7]
	v_pk_add_f32 v[4:5], v[10:11], v[4:5]
	v_pk_add_f32 v[8:9], v[12:13], v[8:9]
	v_pk_add_f32 v[2:3], v[2:3], v[2:3] op_sel:[0,1] op_sel_hi:[1,0]
	v_pk_add_f32 v[6:7], v[6:7], v[6:7] op_sel:[0,1] op_sel_hi:[1,0]
	s_waitcnt vmcnt(0)
	v_mov_b32_e32 v5, v108
	v_mov_b32_e32 v9, v109
	v_mov_b32_e32 v3, v106
	v_mov_b32_e32 v7, v107
	v_pk_add_f32 v[4:5], v[4:5], v[8:9]
	v_pk_add_f32 v[2:3], v[2:3], v[6:7]
	v_lshlrev_b32_e32 v110, 16, v98
	v_pk_add_f32 v[2:3], v[2:3], v[4:5]
	v_and_b32_e32 v98, 0xffff0000, v98
	v_add_f32_e32 v2, v2, v3
	v_fmamk_f32 v2, v2, 0x3a800000, v191
	v_mul_f32_e32 v3, 0x4b800000, v2
	v_cmp_gt_f32_e32 vcc, s12, v2
	v_lshlrev_b32_e32 v111, 16, v99
	v_and_b32_e32 v99, 0xffff0000, v99
	v_cndmask_b32_e32 v2, v2, v3, vcc
	v_rsq_f32_e32 v2, v2
	v_lshlrev_b32_e32 v112, 16, v100
	v_and_b32_e32 v100, 0xffff0000, v100
	v_lshlrev_b32_e32 v113, 16, v101
	v_mul_f32_e32 v6, 0x45800000, v2
	v_cndmask_b32_e32 v2, v2, v6, vcc
	v_and_b32_e32 v101, 0xffff0000, v101
	v_lshlrev_b32_e32 v114, 16, v102
	v_and_b32_e32 v102, 0xffff0000, v102
	v_lshlrev_b32_e32 v115, 16, v103
	v_and_b32_e32 v103, 0xffff0000, v103
	v_lshlrev_b32_e32 v116, 16, v104
	v_and_b32_e32 v3, 0xffff0000, v104
	v_lshlrev_b32_e32 v4, 16, v105
	v_and_b32_e32 v5, 0xffff0000, v105
	v_mul_f32_e32 v6, v2, v110
	v_mul_f32_e32 v7, v2, v98
	v_mul_f32_e32 v8, v2, v111
	v_mul_f32_e32 v9, v2, v99
	v_mul_f32_e32 v10, v2, v112
	v_mul_f32_e32 v11, v2, v100
	v_mul_f32_e32 v12, v2, v113
	v_mul_f32_e32 v13, v2, v101
	v_mul_f32_e32 v14, v2, v114
	v_mul_f32_e32 v15, v2, v102
	v_mul_f32_e32 v94, v2, v115
	v_mul_f32_e32 v95, v2, v103
	v_mul_f32_e32 v99, v2, v116
	v_mul_f32_e32 v100, v2, v3
	v_mul_f32_e32 v4, v2, v4
	v_mul_f32_e32 v5, v2, v5
	v_max_f32_e64 v2, |v6|, |v7|
	v_max_f32_e64 v3, |v8|, |v9|
	v_max_f32_e64 v98, |v10|, |v11|
	v_max_f32_e64 v101, |v12|, |v13|
	v_max3_f32 v2, v2, 0, v3
	v_max_f32_e64 v102, |v14|, |v15|
	v_max_f32_e64 v103, |v94|, |v95|
	v_max3_f32 v2, v2, v98, v101
	v_max_f32_e64 v104, |v99|, |v100|
	v_max_f32_e64 v105, |v4|, |v5|
	v_max3_f32 v2, v2, v102, v103
	v_max3_f32 v2, v2, v104, v105
	v_mov_b32_e32 v3, v2
	s_nop 1
	v_permlane32_swap_b32 v3, v2
	s_mov_b32 s12, 0x42ee0000
	v_add_u32_e32 v98, s86, v0
	v_cmp_gt_i32_e64 s[48:49], s87, v98
	s_waitcnt lgkmcnt(0)
	v_max_f32_e32 v3, v3, v3
	v_max_f32_e32 v2, v2, v3
	v_mov_b32_e32 v3, v2
	s_nop 1
	v_permlane16_swap_b32 v3, v2
	s_waitcnt lgkmcnt(0)
	v_max_f32_e32 v3, v3, v3
	v_max_f32_e32 v2, v2, v3
	s_nop 1
	v_mov_b32_dpp v3, v2 row_ror:8 row_mask:0xf bank_mask:0xf
	s_waitcnt lgkmcnt(0)
	v_max_f32_e32 v3, v3, v3
	v_max_f32_e32 v2, v2, v3
	s_nop 1
	v_mov_b32_dpp v3, v2 row_half_mirror row_mask:0xf bank_mask:0xf
	s_nop 1
	v_mov_b32_dpp v3, v3 quad_perm:[3,2,1,0] row_mask:0xf bank_mask:0xf
	s_waitcnt lgkmcnt(0)
	v_max_f32_e32 v3, v3, v3
	v_max_f32_e32 v2, v2, v3
	s_nop 1
	v_mov_b32_dpp v3, v2 quad_perm:[2,3,0,1] row_mask:0xf bank_mask:0xf
	s_waitcnt lgkmcnt(0)
	v_max_f32_e32 v3, v3, v3
	v_max_f32_e32 v101, v2, v3
	s_nop 1
	v_mov_b32_dpp v102, v101 quad_perm:[1,0,3,2] row_mask:0xf bank_mask:0xf
	v_lshlrev_b64 v[2:3], 10, v[0:1]
	v_lshl_add_u64 v[206:207], v[2:3], 2, v[44:45]
	global_load_dwordx4 v[208:211], v[206:207], off offset:48
	global_load_dwordx4 v[212:215], v[206:207], off offset:32
	global_load_dwordx4 v[216:219], v[206:207], off offset:16
	global_load_dwordx4 v[220:223], v[206:207], off
	s_waitcnt lgkmcnt(0)
	v_max_f32_e32 v1, v102, v102
	v_max_f32_e32 v101, v101, v1
	v_div_scale_f32 v1, s[10:11], v101, v101, s12
	v_rcp_f32_e32 v102, v1
	v_div_scale_f32 v103, vcc, s12, v101, s12
	s_movk_i32 s10, 0x3fff
	v_fma_f32 v104, -v1, v102, 1.0
	v_fmac_f32_e32 v102, v104, v102
	v_mul_f32_e32 v104, v103, v102
	v_fma_f32 v105, -v1, v104, v103
	v_fmac_f32_e32 v104, v105, v102
	v_fma_f32 v1, -v1, v104, v103
	v_div_fmas_f32 v1, v1, v102, v104
	v_div_fixup_f32 v1, v1, v101, s12
	v_cmp_lt_f32_e32 vcc, 0, v101
	v_cmp_lt_i32_e64 s[50:51], s10, v98
	s_or_b64 s[8:9], s[50:51], s[8:9]
	v_cndmask_b32_e32 v102, 0, v1, vcc
	v_mul_f32_e32 v1, v6, v102
	v_mul_f32_e32 v6, v7, v102
	v_mul_f32_e32 v7, v8, v102
	v_mul_f32_e32 v8, v9, v102
	v_rndne_f32_e32 v1, v1
	v_rndne_f32_e32 v6, v6
	v_mul_f32_e32 v9, v10, v102
	v_mul_f32_e32 v10, v11, v102
	v_rndne_f32_e32 v7, v7
	v_rndne_f32_e32 v8, v8
	v_cvt_i32_f32_e32 v1, v1
	v_cvt_i32_f32_e32 v6, v6
	v_rndne_f32_e32 v9, v9
	v_rndne_f32_e32 v10, v10
	v_cvt_i32_f32_e32 v7, v7
	v_cvt_i32_f32_e32 v8, v8
	v_cvt_i32_f32_e32 v9, v9
	v_cvt_i32_f32_e32 v10, v10
	v_mul_f32_e32 v11, v12, v102
	v_add_u32_e32 v12, 8, v1
	v_add_u32_e32 v104, 8, v6
	v_and_b32_e32 v103, 15, v1
	v_lshlrev_b32_e32 v105, 4, v6
	v_add_u32_e32 v1, v1, v6
	v_lshl_add_u32 v6, v7, 4, v196
	v_lshl_add_u32 v107, v8, 8, v200
	v_lshrrev_b32_e32 v12, 4, v12
	v_and_b32_e32 v104, 0xf0, v104
	v_lshl_add_u32 v109, v9, 12, v201
	v_lshl_add_u32 v111, v10, 16, v202
	v_and_b32_e32 v6, 0xf00, v6
	v_and_b32_e32 v107, 0xf000, v107
	v_and_or_b32 v12, v12, 15, v104
	v_lshlrev_b32_e32 v106, 8, v7
	v_add3_u32 v1, v1, v7, v8
	v_and_b32_e32 v7, 0xf0000, v109
	v_and_b32_e32 v109, 0xf00000, v111
	v_or3_b32 v6, v12, v6, v107
	v_lshlrev_b32_e32 v110, 16, v9
	v_or3_b32 v6, v6, v7, v109
	v_add3_u32 v7, v1, v9, v10
	v_mul_f32_e32 v9, v13, v102
	v_rndne_f32_e32 v11, v11
	v_rndne_f32_e32 v9, v9
	v_cvt_i32_f32_e32 v11, v11
	v_cvt_i32_f32_e32 v9, v9
	v_lshlrev_b32_e32 v108, 12, v8
	v_and_b32_e32 v105, 0xf0, v105
	v_lshl_add_u32 v1, v11, 20, v203
	v_lshl_add_u32 v12, v9, 24, v204
	v_and_b32_e32 v1, 0xf000000, v1
	v_and_b32_e32 v12, 0xf0000000, v12
	v_and_b32_e32 v106, 0xf00, v106
	v_or3_b32 v1, v6, v1, v12
	v_lshl_or_b32 v6, v9, 28, v103
	v_lshlrev_b32_e32 v112, 20, v10
	v_and_b32_e32 v108, 0xf000, v108
	v_and_b32_e32 v8, 0xf0000, v110
	v_lshlrev_b32_e32 v10, 24, v11
	v_or3_b32 v6, v6, v105, v106
	v_and_b32_e32 v110, 0xf00000, v112
	v_and_b32_e32 v10, 0xf000000, v10
	v_or3_b32 v6, v6, v108, v8
	v_or3_b32 v10, v6, v110, v10
	v_add3_u32 v6, v7, v11, v9
	v_mul_f32_e32 v7, v14, v102
	v_mul_f32_e32 v8, v15, v102
	v_rndne_f32_e32 v7, v7
	v_rndne_f32_e32 v8, v8
	v_cvt_i32_f32_e32 v7, v7
	v_cvt_i32_f32_e32 v8, v8
	v_mul_f32_e32 v14, v99, v102
	v_mul_f32_e32 v15, v100, v102
	v_add_u32_e32 v9, 8, v7
	v_add_u32_e32 v11, 8, v8
	v_lshrrev_b32_e32 v9, 4, v9
	v_and_b32_e32 v11, 0xf0, v11
	v_and_or_b32 v9, v9, 15, v11
	v_mul_f32_e32 v11, v94, v102
	v_lshlrev_b32_e32 v13, 4, v8
	v_add3_u32 v6, v6, v7, v8
	v_mul_f32_e32 v8, v95, v102
	v_rndne_f32_e32 v11, v11
	v_rndne_f32_e32 v8, v8
	v_cvt_i32_f32_e32 v11, v11
	v_cvt_i32_f32_e32 v8, v8
	v_rndne_f32_e32 v14, v14
	v_rndne_f32_e32 v15, v15
	v_mul_f32_e32 v4, v4, v102
	v_mul_f32_e32 v5, v5, v102
	v_cvt_i32_f32_e32 v14, v14
	v_cvt_i32_f32_e32 v15, v15
	v_rndne_f32_e32 v4, v4
	v_rndne_f32_e32 v5, v5
	v_cvt_i32_f32_e32 v4, v4
	v_cvt_i32_f32_e32 v5, v5
	v_add3_u32 v6, v6, v11, v8
	v_add3_u32 v6, v6, v14, v15
	v_and_b32_e32 v12, 15, v7
	v_add3_u32 v6, v6, v4, v5
	v_cvt_f32_i32_e32 v6, v6
	v_lshl_add_u32 v7, v11, 4, v196
	v_lshlrev_b32_e32 v11, 8, v11
	v_and_b32_e32 v94, 0xf00, v11
	v_mov_b32_e32 v95, v6
	s_nop 1
	v_permlane32_swap_b32 v95, v6
	v_lshl_add_u32 v11, v8, 8, v200
	v_and_b32_e32 v7, 0xf00, v7
	v_and_b32_e32 v11, 0xf000, v11
	v_or3_b32 v7, v9, v7, v11
	s_waitcnt lgkmcnt(0)
	v_add_f32_e32 v6, v95, v6
	v_mov_b32_e32 v9, v6
	s_nop 1
	v_permlane16_swap_b32 v9, v6
	v_lshl_add_u32 v11, v14, 12, v201
	v_lshl_add_u32 v95, v15, 16, v202
	v_and_b32_e32 v11, 0xf0000, v11
	v_and_b32_e32 v95, 0xf00000, v95
	s_waitcnt lgkmcnt(0)
	v_add_f32_e32 v6, v6, v9
	s_nop 1
	v_mov_b32_dpp v9, v6 row_ror:8 row_mask:0xf bank_mask:0xf
	v_or3_b32 v7, v7, v11, v95
	v_lshlrev_b32_e32 v11, 20, v15
	v_and_b32_e32 v15, 0xf00000, v11
	v_lshl_add_u32 v11, v4, 20, v203
	s_waitcnt lgkmcnt(0)
	v_add_f32_e32 v6, v6, v9
	s_nop 1
	v_mov_b32_dpp v9, v6 row_half_mirror row_mask:0xf bank_mask:0xf
	s_nop 1
	v_mov_b32_dpp v9, v9 quad_perm:[3,2,1,0] row_mask:0xf bank_mask:0xf
	v_lshl_add_u32 v95, v5, 24, v204
	v_and_b32_e32 v11, 0xf000000, v11
	v_and_b32_e32 v95, 0xf0000000, v95
	v_or3_b32 v11, v7, v11, v95
	s_waitcnt lgkmcnt(0)
	v_add_f32_e32 v6, v6, v9
	s_nop 1
	v_mov_b32_dpp v9, v6 quad_perm:[2,3,0,1] row_mask:0xf bank_mask:0xf
	v_and_b32_e32 v13, 0xf0, v13
	v_lshlrev_b32_e32 v8, 12, v8
	v_lshlrev_b32_e32 v14, 16, v14
	v_lshl_or_b32 v5, v5, 28, v12
	s_waitcnt lgkmcnt(0)
	v_add_f32_e32 v6, v6, v9
	s_nop 1
	v_mov_b32_dpp v7, v6 quad_perm:[1,0,3,2] row_mask:0xf bank_mask:0xf
	v_and_b32_e32 v8, 0xf000, v8
	v_and_b32_e32 v14, 0xf0000, v14
	v_lshlrev_b32_e32 v4, 24, v4
	v_or3_b32 v5, v5, v13, v94
	v_and_b32_e32 v4, 0xf000000, v4
	v_or3_b32 v5, v5, v8, v14
	v_or3_b32 v12, v5, v15, v4
	s_waitcnt lgkmcnt(0)
	v_add_f32_e32 v4, v6, v7
	v_mul_f32_e32 v13, 0x3c09ae41, v101
	v_mul_f32_e32 v14, 0.5, v4
	v_mov_b32_e32 v105, 0
	v_mov_b64_e32 v[4:5], v[48:49]
	v_mov_b32_e32 v104, 0
	v_mov_b32_e32 v103, 0
	v_mov_b32_e32 v102, 0
	v_mov_b32_e32 v101, 0
	v_mov_b32_e32 v100, 0
	v_mov_b32_e32 v99, 0
	v_mov_b32_e32 v15, 0
.LBB0_770:
	s_cmpk_eq_i32 s56, 0x80
	s_cselect_b64 s[10:11], -1, 0
	ds_bpermute_b32 v6, v97, v96
	s_and_b64 vcc, s[10:11], s[48:49]
	v_cndmask_b32_e32 v94, v0, v98, vcc
	v_ashrrev_i32_e32 v95, 31, v94
	s_and_b32 s10, s56, 0x70
	v_lshlrev_b64 v[94:95], 9, v[94:95]
	v_lshl_add_u64 v[94:95], s[94:95], 0, v[94:95]
	s_lshl_b32 s36, s10, 2
	s_waitcnt lgkmcnt(0)
	v_ashrrev_i32_e32 v7, 31, v6
	v_lshl_add_u64 v[94:95], v[94:95], 0, s[36:37]
	v_lshl_add_u64 v[6:7], v[6:7], 3, s[88:89]
	v_lshl_add_u64 v[94:95], v[94:95], 0, v[144:145]
	global_load_dwordx2 v[6:7], v[6:7], off
	s_nop 0
	global_load_dword v8, v[4:5], off
	global_load_dword v96, v[94:95], off
	s_waitcnt vmcnt(33)
	v_dot8_i32_i4 v9, v20, v1, 0
	v_dot8_i32_i4 v94, v20, v10, 0
	v_dot8_i32_i4 v9, v21, v11, v9
	v_dot8_i32_i4 v94, v21, v12, v94
	v_dot8_i32_i4 v20, v22, v1, 0
	v_dot8_i32_i4 v21, v22, v10, 0
	v_dot8_i32_i4 v20, v23, v11, v20
	v_dot8_i32_i4 v21, v23, v12, v21
	v_lshl_add_u32 v9, v9, 4, v94
	v_cvt_f32_i32_e32 v9, v9
	s_add_i32 s56, s56, 16
	v_lshl_add_u32 v20, v20, 4, v21
	v_cvt_f32_i32_e32 v94, v20
	s_waitcnt vmcnt(32)
	v_dot8_i32_i4 v20, v24, v1, 0
	v_dot8_i32_i4 v21, v24, v10, 0
	v_dot8_i32_i4 v20, v25, v11, v20
	v_dot8_i32_i4 v21, v25, v12, v21
	v_lshl_add_u64 v[4:5], v[4:5], 0, 64
	s_waitcnt vmcnt(2)
	v_mul_f32_e32 v7, v13, v7
	v_lshl_add_u32 v20, v20, 4, v21
	v_cvt_f32_i32_e32 v95, v20
	v_dot8_i32_i4 v20, v26, v1, 0
	v_dot8_i32_i4 v21, v26, v10, 0
	v_dot8_i32_i4 v20, v27, v11, v20
	v_dot8_i32_i4 v21, v27, v12, v21
	s_waitcnt vmcnt(0)
	v_readlane_b32 s10, v96, 0
	s_ashr_i32 s11, s10, 31
	v_readlane_b32 s12, v96, 1
	v_lshl_add_u32 v20, v20, 4, v21
	v_cvt_f32_i32_e32 v106, v20
	v_dot8_i32_i4 v20, v28, v1, 0
	v_dot8_i32_i4 v21, v28, v10, 0
	v_dot8_i32_i4 v20, v29, v11, v20
	v_dot8_i32_i4 v21, v29, v12, v21
	s_lshl_b64 s[10:11], s[10:11], 9
	s_ashr_i32 s13, s12, 31
	v_readlane_b32 s14, v96, 2
	v_lshl_add_u32 v20, v20, 4, v21
	v_cvt_f32_i32_e32 v107, v20
	v_dot8_i32_i4 v20, v30, v1, 0
	v_dot8_i32_i4 v21, v30, v10, 0
	v_dot8_i32_i4 v20, v31, v11, v20
	v_dot8_i32_i4 v21, v31, v12, v21
	s_lshl_b64 s[12:13], s[12:13], 9
	s_ashr_i32 s15, s14, 31
	v_readlane_b32 s16, v96, 3
	v_lshl_add_u32 v20, v20, 4, v21
	v_cvt_f32_i32_e32 v108, v20
	v_dot8_i32_i4 v20, v32, v1, 0
	v_dot8_i32_i4 v21, v32, v10, 0
	v_dot8_i32_i4 v20, v33, v11, v20
	v_dot8_i32_i4 v21, v33, v12, v21
	v_lshl_add_u64 v[22:23], v[16:17], 0, s[12:13]
	s_lshl_b64 s[14:15], s[14:15], 9
	s_ashr_i32 s17, s16, 31
	v_lshl_add_u32 v20, v20, 4, v21
	v_cvt_f32_i32_e32 v109, v20
	v_dot8_i32_i4 v20, v34, v1, 0
	v_dot8_i32_i4 v21, v34, v10, 0
	v_dot8_i32_i4 v20, v35, v11, v20
	v_dot8_i32_i4 v21, v35, v12, v21
	v_readlane_b32 s18, v96, 4
	global_load_dwordx2 v[22:23], v[22:23], off
	v_lshl_add_u64 v[24:25], v[16:17], 0, s[14:15]
	v_lshl_add_u32 v20, v20, 4, v21
	v_cvt_f32_i32_e32 v110, v20
	v_dot8_i32_i4 v20, v36, v1, 0
	v_dot8_i32_i4 v21, v36, v10, 0
	v_dot8_i32_i4 v20, v37, v11, v20
	v_dot8_i32_i4 v21, v37, v12, v21
	s_lshl_b64 s[16:17], s[16:17], 9
	s_ashr_i32 s19, s18, 31
	v_readlane_b32 s20, v96, 5
	v_lshl_add_u32 v20, v20, 4, v21
	v_cvt_f32_i32_e32 v111, v20
	v_dot8_i32_i4 v20, v38, v1, 0
	v_dot8_i32_i4 v21, v38, v10, 0
	v_dot8_i32_i4 v20, v39, v11, v20
	v_dot8_i32_i4 v21, v39, v12, v21
	v_permlane32_swap_b32 v9, v111
	s_nop 1
	v_lshl_add_u32 v20, v20, 4, v21
	v_cvt_f32_i32_e32 v112, v20
	v_dot8_i32_i4 v20, v40, v1, 0
	v_dot8_i32_i4 v21, v40, v10, 0
	v_dot8_i32_i4 v20, v41, v11, v20
	v_dot8_i32_i4 v21, v41, v12, v21
	s_waitcnt lgkmcnt(0)
	v_add_f32_e32 v9, v9, v111
	v_permlane32_swap_b32 v94, v112
	v_lshl_add_u32 v20, v20, 4, v21
	v_cvt_f32_i32_e32 v113, v20
	v_dot8_i32_i4 v20, v60, v1, 0
	v_dot8_i32_i4 v21, v60, v10, 0
	v_dot8_i32_i4 v20, v61, v11, v20
	v_dot8_i32_i4 v21, v61, v12, v21
	s_waitcnt lgkmcnt(0)
	v_add_f32_e32 v94, v94, v112
	v_permlane32_swap_b32 v95, v113
	v_lshl_add_u32 v20, v20, 4, v21
	v_cvt_f32_i32_e32 v114, v20
	v_dot8_i32_i4 v20, v58, v1, 0
	v_dot8_i32_i4 v21, v58, v10, 0
	v_dot8_i32_i4 v20, v59, v11, v20
	v_dot8_i32_i4 v21, v59, v12, v21
	s_waitcnt lgkmcnt(0)
	v_add_f32_e32 v95, v95, v113
	v_permlane32_swap_b32 v106, v114
	v_lshl_add_u32 v20, v20, 4, v21
	v_cvt_f32_i32_e32 v115, v20
	v_dot8_i32_i4 v20, v56, v1, 0
	v_dot8_i32_i4 v21, v56, v10, 0
	v_dot8_i32_i4 v20, v57, v11, v20
	v_dot8_i32_i4 v21, v57, v12, v21
	s_waitcnt lgkmcnt(0)
	v_add_f32_e32 v106, v106, v114
	v_permlane32_swap_b32 v107, v115
	v_lshl_add_u32 v20, v20, 4, v21
	v_cvt_f32_i32_e32 v116, v20
	v_dot8_i32_i4 v20, v54, v1, 0
	v_dot8_i32_i4 v21, v54, v10, 0
	v_dot8_i32_i4 v20, v55, v11, v20
	v_dot8_i32_i4 v21, v55, v12, v21
	s_waitcnt lgkmcnt(0)
	v_add_f32_e32 v107, v107, v115
	v_permlane32_swap_b32 v108, v116
	v_lshl_add_u32 v20, v20, 4, v21
	v_cvt_f32_i32_e32 v117, v20
	v_dot8_i32_i4 v20, v52, v1, 0
	v_dot8_i32_i4 v21, v52, v10, 0
	v_dot8_i32_i4 v20, v53, v11, v20
	v_dot8_i32_i4 v21, v53, v12, v21
	s_waitcnt lgkmcnt(0)
	v_add_f32_e32 v108, v108, v116
	v_permlane32_swap_b32 v109, v117
	v_lshl_add_u32 v20, v20, 4, v21
	v_cvt_f32_i32_e32 v118, v20
	v_lshl_add_u64 v[20:21], v[16:17], 0, s[10:11]
	s_waitcnt lgkmcnt(0)
	v_add_f32_e32 v109, v109, v117
	v_permlane32_swap_b32 v110, v118
	global_load_dwordx2 v[20:21], v[20:21], off
	v_lshl_add_u64 v[26:27], v[16:17], 0, s[16:17]
	global_load_dwordx2 v[24:25], v[24:25], off
	s_waitcnt lgkmcnt(0)
	v_add_f32_e32 v110, v110, v118
	v_permlane16_swap_b32 v9, v107
	s_lshl_b64 s[18:19], s[18:19], 9
	s_ashr_i32 s21, s20, 31
	v_readlane_b32 s22, v96, 6
	global_load_dwordx2 v[26:27], v[26:27], off
	s_waitcnt lgkmcnt(0)
	v_add_f32_e32 v9, v9, v107
	v_permlane16_swap_b32 v94, v108
	v_lshl_add_u64 v[28:29], v[16:17], 0, s[18:19]
	s_lshl_b64 s[20:21], s[20:21], 9
	s_ashr_i32 s23, s22, 31
	s_waitcnt lgkmcnt(0)
	v_add_f32_e32 v94, v94, v108
	v_permlane16_swap_b32 v95, v109
	v_readlane_b32 s24, v96, 7
	global_load_dwordx2 v[28:29], v[28:29], off
	v_lshl_add_u64 v[30:31], v[16:17], 0, s[20:21]
	s_waitcnt lgkmcnt(0)
	v_add_f32_e32 v95, v95, v109
	v_permlane16_swap_b32 v106, v110
	s_lshl_b64 s[22:23], s[22:23], 9
	s_ashr_i32 s25, s24, 31
	v_readlane_b32 s26, v96, 8
	s_waitcnt lgkmcnt(0)
	v_add_f32_e32 v106, v106, v110
	v_cndmask_b32_e64 v107, v9, v95, s[44:45]
	v_cndmask_b32_e64 v9, v95, v9, s[44:45]
	s_nop 0
	v_mov_b32_dpp v95, v107 row_ror:8 row_mask:0xf bank_mask:0xf
	global_load_dwordx2 v[30:31], v[30:31], off
	v_lshl_add_u64 v[32:33], v[16:17], 0, s[22:23]
	s_lshl_b64 s[24:25], s[24:25], 9
	s_ashr_i32 s27, s26, 31
	s_waitcnt lgkmcnt(0)
	v_add_f32_e32 v9, v9, v95
	v_cndmask_b32_e64 v95, v94, v106, s[44:45]
	s_nop 1
	v_mov_b32_dpp v95, v95 row_ror:8 row_mask:0xf bank_mask:0xf
	v_cndmask_b32_e64 v94, v106, v94, s[44:45]
	v_readlane_b32 s28, v96, 9
	global_load_dwordx2 v[32:33], v[32:33], off
	v_lshl_add_u64 v[34:35], v[16:17], 0, s[24:25]
	s_waitcnt lgkmcnt(0)
	v_add_f32_e32 v94, v94, v95
	v_cndmask_b32_e64 v95, v9, v94, s[46:47]
	v_cndmask_b32_e64 v9, v94, v9, s[46:47]
	s_nop 0
	v_mov_b32_dpp v94, v95 row_half_mirror row_mask:0xf bank_mask:0xf
	s_nop 1
	v_mov_b32_dpp v94, v94 quad_perm:[3,2,1,0] row_mask:0xf bank_mask:0xf
	s_lshl_b64 s[26:27], s[26:27], 9
	s_ashr_i32 s29, s28, 31
	v_readlane_b32 s30, v96, 10
	global_load_dwordx2 v[34:35], v[34:35], off
	s_waitcnt lgkmcnt(0)
	v_add_f32_e32 v9, v9, v94
	s_nop 1
	v_mov_b32_dpp v94, v9 quad_perm:[2,3,0,1] row_mask:0xf bank_mask:0xf
	v_lshl_add_u64 v[36:37], v[16:17], 0, s[26:27]
	s_lshl_b64 s[28:29], s[28:29], 9
	s_ashr_i32 s31, s30, 31
	v_readlane_b32 s34, v96, 11
	s_waitcnt lgkmcnt(0)
	v_add_f32_e32 v9, v9, v94
	s_nop 1
	v_mov_b32_dpp v94, v9 quad_perm:[1,0,3,2] row_mask:0xf bank_mask:0xf
	global_load_dwordx2 v[36:37], v[36:37], off
	v_lshl_add_u64 v[38:39], v[16:17], 0, s[28:29]
	s_lshl_b64 s[30:31], s[30:31], 9
	s_ashr_i32 s35, s34, 31
	s_waitcnt lgkmcnt(0)
	v_add_f32_e32 v9, v9, v94
	v_add_f32_e32 v9, v14, v9
	v_mul_f32_e32 v7, v7, v9
	v_mul_f32_e32 v9, 0x3d372713, v7
	v_mul_f32_e32 v9, v7, v9
	v_fma_f32 v9, v7, v9, v7
	v_mul_f32_e32 v9, 0x3fcc422a, v9
	v_mul_f32_e32 v9, 0xbfb8aa3b, v9
	v_exp_f32_e32 v9, v9
	v_lshlrev_b32_e32 v94, 4, v92
	v_readlane_b32 s38, v96, 12
	global_load_dwordx2 v[38:39], v[38:39], off
	v_add_f32_e32 v9, 1.0, v9
	v_rcp_f32_e32 v9, v9
	v_lshl_add_u64 v[40:41], v[16:17], 0, s[30:31]
	s_lshl_b64 s[34:35], s[34:35], 9
	s_ashr_i32 s39, s38, 31
	v_pk_mul_f32 v[6:7], v[6:7], v[8:9]
	v_lshrrev_b32_e32 v9, 4, v92
	v_pk_mul_f32 v[6:7], v[6:7], v[6:7] op_sel:[0,1] op_sel_hi:[1,0]
	v_cvt_f16_f32_e32 v120, v6
	v_and_b32_e32 v8, 0x7070707, v92
	v_readlane_b32 s36, v120, 0
	v_and_b32_e32 v9, 0x7070707, v9
	v_perm_b32 v8, s2, v205, v8
	v_perm_b32 v9, s2, v205, v9
	v_and_or_b32 v8, v94, s4, v8
	v_and_or_b32 v9, v92, s4, v9
	v_perm_b32 v92, v9, v8, s5
	v_perm_b32 v94, v9, v8, s33
	v_perm_b32 v95, v9, v8, s0
	v_perm_b32 v8, v9, v8, s1
	v_pk_fma_f16 v8, v8, s36, v102 op_sel_hi:[1,0,1]
	v_lshrrev_b32_e32 v102, 4, v93
	v_pk_fma_f16 v9, v92, s36, v105 op_sel_hi:[1,0,1]
	v_pk_fma_f16 v92, v94, s36, v104 op_sel_hi:[1,0,1]
	v_pk_fma_f16 v94, v95, s36, v103 op_sel_hi:[1,0,1]
	v_and_b32_e32 v95, 0x7070707, v93
	v_and_b32_e32 v102, 0x7070707, v102
	v_perm_b32 v95, s2, v205, v95
	v_perm_b32 v102, s2, v205, v102
	v_lshlrev_b32_e32 v103, 4, v93
	v_and_or_b32 v95, v103, s4, v95
	v_and_or_b32 v93, v93, s4, v102
	v_perm_b32 v102, v93, v95, s5
	v_perm_b32 v103, v93, v95, s33
	v_perm_b32 v104, v93, v95, s0
	v_perm_b32 v93, v93, v95, s1
	v_pk_fma_f16 v95, v102, s36, v101 op_sel_hi:[1,0,1]
	v_readlane_b32 s59, v120, 4
	v_lshrrev_b32_e32 v101, 4, v90
	v_pk_fma_f16 v100, v103, s36, v100 op_sel_hi:[1,0,1]
	v_pk_fma_f16 v99, v104, s36, v99 op_sel_hi:[1,0,1]
	v_pk_fma_f16 v7, v93, s36, v15 op_sel_hi:[1,0,1]
	v_and_b32_e32 v93, 0x7070707, v90
	v_and_b32_e32 v101, 0x7070707, v101
	v_perm_b32 v93, s2, v205, v93
	v_perm_b32 v101, s2, v205, v101
	v_lshlrev_b32_e32 v102, 4, v90
	v_and_or_b32 v93, v102, s4, v93
	v_and_or_b32 v90, v90, s4, v101
	v_perm_b32 v103, v90, v93, s0
	v_perm_b32 v101, v90, v93, s5
	v_perm_b32 v102, v90, v93, s33
	v_perm_b32 v90, v90, v93, s1
	v_pk_fma_f16 v93, v103, s59, v94 op_sel_hi:[1,0,1]
	v_lshrrev_b32_e32 v94, 4, v91
	v_pk_fma_f16 v8, v90, s59, v8 op_sel_hi:[1,0,1]
	v_and_b32_e32 v90, 0x7070707, v91
	v_and_b32_e32 v94, 0x7070707, v94
	v_pk_fma_f16 v9, v101, s59, v9 op_sel_hi:[1,0,1]
	v_perm_b32 v90, s2, v205, v90
	v_perm_b32 v94, s2, v205, v94
	v_lshlrev_b32_e32 v101, 4, v91
	v_and_or_b32 v90, v101, s4, v90
	v_and_or_b32 v91, v91, s4, v94
	v_pk_fma_f16 v92, v102, s59, v92 op_sel_hi:[1,0,1]
	v_perm_b32 v94, v91, v90, s5
	v_perm_b32 v102, v91, v90, s0
	v_perm_b32 v101, v91, v90, s33
	v_perm_b32 v90, v91, v90, s1
	v_pk_fma_f16 v91, v94, s59, v95 op_sel_hi:[1,0,1]
	v_pk_fma_f16 v95, v102, s59, v99 op_sel_hi:[1,0,1]
	v_readlane_b32 s60, v120, 8
	v_lshrrev_b32_e32 v99, 4, v88
	v_pk_fma_f16 v94, v101, s59, v100 op_sel_hi:[1,0,1]
	v_pk_fma_f16 v7, v90, s59, v7 op_sel_hi:[1,0,1]
	v_and_b32_e32 v90, 0x7070707, v88
	v_and_b32_e32 v99, 0x7070707, v99
	v_perm_b32 v90, s2, v205, v90
	v_perm_b32 v99, s2, v205, v99
	v_lshlrev_b32_e32 v100, 4, v88
	v_and_or_b32 v90, v100, s4, v90
	v_and_or_b32 v88, v88, s4, v99
	v_perm_b32 v100, v88, v90, s33
	v_perm_b32 v101, v88, v90, s0
	v_perm_b32 v99, v88, v90, s5
	v_perm_b32 v88, v88, v90, s1
	v_pk_fma_f16 v90, v100, s60, v92 op_sel_hi:[1,0,1]
	v_pk_fma_f16 v92, v101, s60, v93 op_sel_hi:[1,0,1]
	v_lshrrev_b32_e32 v93, 4, v89
	v_pk_fma_f16 v8, v88, s60, v8 op_sel_hi:[1,0,1]
	v_and_b32_e32 v88, 0x7070707, v89
	v_and_b32_e32 v93, 0x7070707, v93
	v_pk_fma_f16 v9, v99, s60, v9 op_sel_hi:[1,0,1]
	v_perm_b32 v88, s2, v205, v88
	v_perm_b32 v93, s2, v205, v93
	v_lshlrev_b32_e32 v99, 4, v89
	v_and_or_b32 v88, v99, s4, v88
	v_and_or_b32 v89, v89, s4, v93
	v_perm_b32 v93, v89, v88, s5
	v_perm_b32 v99, v89, v88, s33
	v_perm_b32 v100, v89, v88, s0
	v_perm_b32 v88, v89, v88, s1
	v_pk_fma_f16 v89, v93, s60, v91 op_sel_hi:[1,0,1]
	v_pk_fma_f16 v91, v99, s60, v94 op_sel_hi:[1,0,1]
	v_readlane_b32 s36, v120, 12
	v_lshrrev_b32_e32 v94, 4, v86
	v_pk_fma_f16 v93, v100, s60, v95 op_sel_hi:[1,0,1]
	v_pk_fma_f16 v7, v88, s60, v7 op_sel_hi:[1,0,1]
	v_and_b32_e32 v88, 0x7070707, v86
	v_and_b32_e32 v94, 0x7070707, v94
	v_perm_b32 v88, s2, v205, v88
	v_perm_b32 v94, s2, v205, v94
	v_lshlrev_b32_e32 v95, 4, v86
	v_and_or_b32 v88, v95, s4, v88
	v_and_or_b32 v86, v86, s4, v94
	v_perm_b32 v95, v86, v88, s33
	v_perm_b32 v99, v86, v88, s0
	v_perm_b32 v94, v86, v88, s5
	v_perm_b32 v86, v86, v88, s1
	v_pk_fma_f16 v88, v95, s36, v90 op_sel_hi:[1,0,1]
	v_pk_fma_f16 v90, v99, s36, v92 op_sel_hi:[1,0,1]
	v_lshrrev_b32_e32 v92, 4, v87
	v_pk_fma_f16 v8, v86, s36, v8 op_sel_hi:[1,0,1]
	v_and_b32_e32 v86, 0x7070707, v87
	v_and_b32_e32 v92, 0x7070707, v92
	v_pk_fma_f16 v9, v94, s36, v9 op_sel_hi:[1,0,1]
	v_perm_b32 v86, s2, v205, v86
	v_perm_b32 v92, s2, v205, v92
	v_lshlrev_b32_e32 v94, 4, v87
	v_and_or_b32 v86, v94, s4, v86
	v_and_or_b32 v87, v87, s4, v92
	v_perm_b32 v92, v87, v86, s5
	v_perm_b32 v94, v87, v86, s33
	v_perm_b32 v95, v87, v86, s0
	v_perm_b32 v86, v87, v86, s1
	v_pk_fma_f16 v87, v92, s36, v89 op_sel_hi:[1,0,1]
	v_readlane_b32 s59, v120, 16
	v_lshrrev_b32_e32 v92, 4, v84
	v_pk_fma_f16 v89, v94, s36, v91 op_sel_hi:[1,0,1]
	v_pk_fma_f16 v91, v95, s36, v93 op_sel_hi:[1,0,1]
	v_pk_fma_f16 v7, v86, s36, v7 op_sel_hi:[1,0,1]
	v_and_b32_e32 v86, 0x7070707, v84
	v_and_b32_e32 v92, 0x7070707, v92
	v_perm_b32 v86, s2, v205, v86
	v_perm_b32 v92, s2, v205, v92
	v_lshlrev_b32_e32 v93, 4, v84
	v_and_or_b32 v86, v93, s4, v86
	v_and_or_b32 v84, v84, s4, v92
	v_perm_b32 v93, v84, v86, s33
	v_perm_b32 v94, v84, v86, s0
	v_perm_b32 v92, v84, v86, s5
	v_perm_b32 v84, v84, v86, s1
	v_pk_fma_f16 v86, v93, s59, v88 op_sel_hi:[1,0,1]
	v_pk_fma_f16 v88, v94, s59, v90 op_sel_hi:[1,0,1]
	v_lshrrev_b32_e32 v90, 4, v85
	v_pk_fma_f16 v8, v84, s59, v8 op_sel_hi:[1,0,1]
	v_and_b32_e32 v84, 0x7070707, v85
	v_and_b32_e32 v90, 0x7070707, v90
	v_pk_fma_f16 v9, v92, s59, v9 op_sel_hi:[1,0,1]
	v_perm_b32 v84, s2, v205, v84
	v_perm_b32 v90, s2, v205, v90
	v_lshlrev_b32_e32 v92, 4, v85
	v_and_or_b32 v84, v92, s4, v84
	v_and_or_b32 v85, v85, s4, v90
	v_perm_b32 v90, v85, v84, s5
	v_perm_b32 v92, v85, v84, s33
	v_perm_b32 v93, v85, v84, s0
	v_perm_b32 v84, v85, v84, s1
	v_pk_fma_f16 v85, v90, s59, v87 op_sel_hi:[1,0,1]
	v_readlane_b32 s60, v120, 20
	v_lshrrev_b32_e32 v90, 4, v82
	v_pk_fma_f16 v87, v92, s59, v89 op_sel_hi:[1,0,1]
	v_pk_fma_f16 v89, v93, s59, v91 op_sel_hi:[1,0,1]
	v_pk_fma_f16 v7, v84, s59, v7 op_sel_hi:[1,0,1]
	v_and_b32_e32 v84, 0x7070707, v82
	v_and_b32_e32 v90, 0x7070707, v90
	v_perm_b32 v84, s2, v205, v84
	v_perm_b32 v90, s2, v205, v90
	v_lshlrev_b32_e32 v91, 4, v82
	v_and_or_b32 v84, v91, s4, v84
	v_and_or_b32 v82, v82, s4, v90
	v_perm_b32 v91, v82, v84, s33
	v_perm_b32 v92, v82, v84, s0
	v_perm_b32 v90, v82, v84, s5
	v_perm_b32 v82, v82, v84, s1
	v_pk_fma_f16 v84, v91, s60, v86 op_sel_hi:[1,0,1]
	v_pk_fma_f16 v86, v92, s60, v88 op_sel_hi:[1,0,1]
	v_lshrrev_b32_e32 v88, 4, v83
	v_pk_fma_f16 v8, v82, s60, v8 op_sel_hi:[1,0,1]
	v_and_b32_e32 v82, 0x7070707, v83
	v_and_b32_e32 v88, 0x7070707, v88
	v_pk_fma_f16 v9, v90, s60, v9 op_sel_hi:[1,0,1]
	v_perm_b32 v82, s2, v205, v82
	v_perm_b32 v88, s2, v205, v88
	v_lshlrev_b32_e32 v90, 4, v83
	v_and_or_b32 v82, v90, s4, v82
	v_and_or_b32 v83, v83, s4, v88
	v_perm_b32 v88, v83, v82, s5
	v_perm_b32 v90, v83, v82, s33
	v_perm_b32 v91, v83, v82, s0
	v_perm_b32 v82, v83, v82, s1
	v_pk_fma_f16 v83, v88, s60, v85 op_sel_hi:[1,0,1]
	v_readlane_b32 s36, v120, 24
	v_lshrrev_b32_e32 v88, 4, v80
	v_pk_fma_f16 v85, v90, s60, v87 op_sel_hi:[1,0,1]
	v_pk_fma_f16 v87, v91, s60, v89 op_sel_hi:[1,0,1]
	v_pk_fma_f16 v7, v82, s60, v7 op_sel_hi:[1,0,1]
	v_and_b32_e32 v82, 0x7070707, v80
	v_and_b32_e32 v88, 0x7070707, v88
	v_perm_b32 v82, s2, v205, v82
	v_perm_b32 v88, s2, v205, v88
	v_lshlrev_b32_e32 v89, 4, v80
	v_and_or_b32 v82, v89, s4, v82
	v_and_or_b32 v80, v80, s4, v88
	v_perm_b32 v89, v80, v82, s33
	v_perm_b32 v90, v80, v82, s0
	v_perm_b32 v88, v80, v82, s5
	v_perm_b32 v80, v80, v82, s1
	v_pk_fma_f16 v82, v89, s36, v84 op_sel_hi:[1,0,1]
	v_pk_fma_f16 v84, v90, s36, v86 op_sel_hi:[1,0,1]
	v_lshrrev_b32_e32 v86, 4, v81
	v_pk_fma_f16 v8, v80, s36, v8 op_sel_hi:[1,0,1]
	v_and_b32_e32 v80, 0x7070707, v81
	v_and_b32_e32 v86, 0x7070707, v86
	v_pk_fma_f16 v9, v88, s36, v9 op_sel_hi:[1,0,1]
	v_perm_b32 v80, s2, v205, v80
	v_perm_b32 v86, s2, v205, v86
	v_lshlrev_b32_e32 v88, 4, v81
	v_and_or_b32 v80, v88, s4, v80
	v_and_or_b32 v81, v81, s4, v86
	v_perm_b32 v86, v81, v80, s5
	v_perm_b32 v88, v81, v80, s33
	v_perm_b32 v89, v81, v80, s0
	v_perm_b32 v80, v81, v80, s1
	v_pk_fma_f16 v81, v86, s36, v83 op_sel_hi:[1,0,1]
	v_readlane_b32 s59, v120, 28
	v_lshrrev_b32_e32 v86, 4, v78
	v_pk_fma_f16 v83, v88, s36, v85 op_sel_hi:[1,0,1]
	v_pk_fma_f16 v85, v89, s36, v87 op_sel_hi:[1,0,1]
	v_pk_fma_f16 v7, v80, s36, v7 op_sel_hi:[1,0,1]
	v_and_b32_e32 v80, 0x7070707, v78
	v_and_b32_e32 v86, 0x7070707, v86
	v_perm_b32 v80, s2, v205, v80
	v_perm_b32 v86, s2, v205, v86
	v_lshlrev_b32_e32 v87, 4, v78
	v_and_or_b32 v80, v87, s4, v80
	v_and_or_b32 v78, v78, s4, v86
	v_perm_b32 v87, v78, v80, s33
	v_perm_b32 v88, v78, v80, s0
	v_perm_b32 v86, v78, v80, s5
	v_perm_b32 v78, v78, v80, s1
	v_pk_fma_f16 v80, v87, s59, v82 op_sel_hi:[1,0,1]
	v_pk_fma_f16 v82, v88, s59, v84 op_sel_hi:[1,0,1]
	v_lshrrev_b32_e32 v84, 4, v79
	v_pk_fma_f16 v8, v78, s59, v8 op_sel_hi:[1,0,1]
	v_and_b32_e32 v78, 0x7070707, v79
	v_and_b32_e32 v84, 0x7070707, v84
	v_pk_fma_f16 v9, v86, s59, v9 op_sel_hi:[1,0,1]
	v_perm_b32 v78, s2, v205, v78
	v_perm_b32 v84, s2, v205, v84
	v_lshlrev_b32_e32 v86, 4, v79
	v_and_or_b32 v78, v86, s4, v78
	v_and_or_b32 v79, v79, s4, v84
	v_perm_b32 v84, v79, v78, s5
	v_perm_b32 v86, v79, v78, s33
	v_perm_b32 v87, v79, v78, s0
	v_perm_b32 v78, v79, v78, s1
	v_pk_fma_f16 v79, v84, s59, v81 op_sel_hi:[1,0,1]
	v_readlane_b32 s60, v120, 32
	v_lshrrev_b32_e32 v84, 4, v76
	v_pk_fma_f16 v81, v86, s59, v83 op_sel_hi:[1,0,1]
	v_pk_fma_f16 v83, v87, s59, v85 op_sel_hi:[1,0,1]
	v_pk_fma_f16 v7, v78, s59, v7 op_sel_hi:[1,0,1]
	v_and_b32_e32 v78, 0x7070707, v76
	v_and_b32_e32 v84, 0x7070707, v84
	v_perm_b32 v78, s2, v205, v78
	v_perm_b32 v84, s2, v205, v84
	v_lshlrev_b32_e32 v85, 4, v76
	v_and_or_b32 v78, v85, s4, v78
	v_and_or_b32 v76, v76, s4, v84
	v_perm_b32 v85, v76, v78, s33
	v_perm_b32 v86, v76, v78, s0
	v_perm_b32 v84, v76, v78, s5
	v_perm_b32 v76, v76, v78, s1
	v_pk_fma_f16 v78, v85, s60, v80 op_sel_hi:[1,0,1]
	v_pk_fma_f16 v80, v86, s60, v82 op_sel_hi:[1,0,1]
	v_lshrrev_b32_e32 v82, 4, v77
	v_pk_fma_f16 v8, v76, s60, v8 op_sel_hi:[1,0,1]
	v_and_b32_e32 v76, 0x7070707, v77
	v_and_b32_e32 v82, 0x7070707, v82
	v_pk_fma_f16 v9, v84, s60, v9 op_sel_hi:[1,0,1]
	v_perm_b32 v76, s2, v205, v76
	v_perm_b32 v82, s2, v205, v82
	v_lshlrev_b32_e32 v84, 4, v77
	v_and_or_b32 v76, v84, s4, v76
	v_and_or_b32 v77, v77, s4, v82
	v_perm_b32 v82, v77, v76, s5
	v_perm_b32 v84, v77, v76, s33
	v_perm_b32 v85, v77, v76, s0
	v_perm_b32 v76, v77, v76, s1
	v_pk_fma_f16 v77, v82, s60, v79 op_sel_hi:[1,0,1]
	v_readlane_b32 s36, v120, 36
	v_lshrrev_b32_e32 v82, 4, v70
	v_pk_fma_f16 v79, v84, s60, v81 op_sel_hi:[1,0,1]
	v_pk_fma_f16 v81, v85, s60, v83 op_sel_hi:[1,0,1]
	v_pk_fma_f16 v7, v76, s60, v7 op_sel_hi:[1,0,1]
	v_and_b32_e32 v76, 0x7070707, v70
	v_and_b32_e32 v82, 0x7070707, v82
	v_perm_b32 v76, s2, v205, v76
	v_perm_b32 v82, s2, v205, v82
	v_lshlrev_b32_e32 v83, 4, v70
	v_and_or_b32 v76, v83, s4, v76
	v_and_or_b32 v70, v70, s4, v82
	v_perm_b32 v83, v70, v76, s33
	v_perm_b32 v84, v70, v76, s0
	v_perm_b32 v82, v70, v76, s5
	v_perm_b32 v70, v70, v76, s1
	v_pk_fma_f16 v76, v83, s36, v78 op_sel_hi:[1,0,1]
	v_pk_fma_f16 v78, v84, s36, v80 op_sel_hi:[1,0,1]
	v_lshrrev_b32_e32 v80, 4, v71
	v_pk_fma_f16 v8, v70, s36, v8 op_sel_hi:[1,0,1]
	v_and_b32_e32 v70, 0x7070707, v71
	v_and_b32_e32 v80, 0x7070707, v80
	v_pk_fma_f16 v9, v82, s36, v9 op_sel_hi:[1,0,1]
	v_perm_b32 v70, s2, v205, v70
	v_perm_b32 v80, s2, v205, v80
	v_lshlrev_b32_e32 v82, 4, v71
	v_and_or_b32 v70, v82, s4, v70
	v_and_or_b32 v71, v71, s4, v80
	v_perm_b32 v80, v71, v70, s5
	v_perm_b32 v82, v71, v70, s33
	v_perm_b32 v83, v71, v70, s0
	v_perm_b32 v70, v71, v70, s1
	v_pk_fma_f16 v71, v80, s36, v77 op_sel_hi:[1,0,1]
	v_readlane_b32 s59, v120, 40
	v_lshrrev_b32_e32 v80, 4, v66
	v_pk_fma_f16 v77, v82, s36, v79 op_sel_hi:[1,0,1]
	v_pk_fma_f16 v79, v83, s36, v81 op_sel_hi:[1,0,1]
	v_pk_fma_f16 v7, v70, s36, v7 op_sel_hi:[1,0,1]
	v_and_b32_e32 v70, 0x7070707, v66
	v_and_b32_e32 v80, 0x7070707, v80
	v_perm_b32 v70, s2, v205, v70
	v_perm_b32 v80, s2, v205, v80
	v_lshlrev_b32_e32 v81, 4, v66
	v_and_or_b32 v70, v81, s4, v70
	v_and_or_b32 v66, v66, s4, v80
	v_perm_b32 v81, v66, v70, s33
	v_perm_b32 v82, v66, v70, s0
	v_perm_b32 v80, v66, v70, s5
	v_perm_b32 v66, v66, v70, s1
	v_pk_fma_f16 v70, v81, s59, v76 op_sel_hi:[1,0,1]
	v_pk_fma_f16 v76, v82, s59, v78 op_sel_hi:[1,0,1]
	v_lshrrev_b32_e32 v78, 4, v67
	v_pk_fma_f16 v8, v66, s59, v8 op_sel_hi:[1,0,1]
	v_and_b32_e32 v66, 0x7070707, v67
	v_and_b32_e32 v78, 0x7070707, v78
	v_pk_fma_f16 v9, v80, s59, v9 op_sel_hi:[1,0,1]
	v_perm_b32 v66, s2, v205, v66
	v_perm_b32 v78, s2, v205, v78
	v_lshlrev_b32_e32 v80, 4, v67
	v_and_or_b32 v66, v80, s4, v66
	v_and_or_b32 v67, v67, s4, v78
	v_perm_b32 v78, v67, v66, s5
	v_perm_b32 v80, v67, v66, s33
	v_perm_b32 v81, v67, v66, s0
	v_perm_b32 v66, v67, v66, s1
	v_pk_fma_f16 v67, v78, s59, v71 op_sel_hi:[1,0,1]
	v_readlane_b32 s60, v120, 44
	v_lshrrev_b32_e32 v78, 4, v72
	v_pk_fma_f16 v71, v80, s59, v77 op_sel_hi:[1,0,1]
	v_pk_fma_f16 v77, v81, s59, v79 op_sel_hi:[1,0,1]
	v_pk_fma_f16 v7, v66, s59, v7 op_sel_hi:[1,0,1]
	v_and_b32_e32 v66, 0x7070707, v72
	v_and_b32_e32 v78, 0x7070707, v78
	v_perm_b32 v66, s2, v205, v66
	v_perm_b32 v78, s2, v205, v78
	v_lshlrev_b32_e32 v79, 4, v72
	v_and_or_b32 v66, v79, s4, v66
	v_and_or_b32 v72, v72, s4, v78
	v_perm_b32 v80, v72, v66, s0
	v_perm_b32 v78, v72, v66, s5
	v_perm_b32 v79, v72, v66, s33
	v_perm_b32 v66, v72, v66, s1
	v_pk_fma_f16 v72, v80, s60, v76 op_sel_hi:[1,0,1]
	v_lshrrev_b32_e32 v76, 4, v73
	v_pk_fma_f16 v8, v66, s60, v8 op_sel_hi:[1,0,1]
	v_and_b32_e32 v66, 0x7070707, v73
	v_and_b32_e32 v76, 0x7070707, v76
	v_pk_fma_f16 v9, v78, s60, v9 op_sel_hi:[1,0,1]
	v_perm_b32 v66, s2, v205, v66
	v_perm_b32 v76, s2, v205, v76
	v_lshlrev_b32_e32 v78, 4, v73
	v_and_or_b32 v66, v78, s4, v66
	v_and_or_b32 v73, v73, s4, v76
	v_perm_b32 v76, v73, v66, s5
	v_pk_fma_f16 v70, v79, s60, v70 op_sel_hi:[1,0,1]
	v_perm_b32 v78, v73, v66, s33
	v_perm_b32 v79, v73, v66, s0
	v_perm_b32 v66, v73, v66, s1
	v_pk_fma_f16 v67, v76, s60, v67 op_sel_hi:[1,0,1]
	v_readlane_b32 s36, v120, 48
	v_lshrrev_b32_e32 v76, 4, v68
	v_pk_fma_f16 v71, v78, s60, v71 op_sel_hi:[1,0,1]
	v_pk_fma_f16 v73, v79, s60, v77 op_sel_hi:[1,0,1]
	v_pk_fma_f16 v7, v66, s60, v7 op_sel_hi:[1,0,1]
	v_and_b32_e32 v66, 0x7070707, v68
	v_and_b32_e32 v76, 0x7070707, v76
	v_perm_b32 v66, s2, v205, v66
	v_perm_b32 v76, s2, v205, v76
	v_lshlrev_b32_e32 v77, 4, v68
	v_and_or_b32 v66, v77, s4, v66
	v_and_or_b32 v68, v68, s4, v76
	v_perm_b32 v77, v68, v66, s33
	v_perm_b32 v78, v68, v66, s0
	v_perm_b32 v76, v68, v66, s5
	v_perm_b32 v66, v68, v66, s1
	v_pk_fma_f16 v68, v77, s36, v70 op_sel_hi:[1,0,1]
	v_pk_fma_f16 v70, v78, s36, v72 op_sel_hi:[1,0,1]
	v_lshrrev_b32_e32 v72, 4, v69
	v_pk_fma_f16 v8, v66, s36, v8 op_sel_hi:[1,0,1]
	v_and_b32_e32 v66, 0x7070707, v69
	v_and_b32_e32 v72, 0x7070707, v72
	v_pk_fma_f16 v9, v76, s36, v9 op_sel_hi:[1,0,1]
	v_perm_b32 v66, s2, v205, v66
	v_perm_b32 v72, s2, v205, v72
	v_lshlrev_b32_e32 v76, 4, v69
	v_and_or_b32 v66, v76, s4, v66
	v_and_or_b32 v69, v69, s4, v72
	v_perm_b32 v72, v69, v66, s5
	v_perm_b32 v76, v69, v66, s33
	v_perm_b32 v77, v69, v66, s0
	v_perm_b32 v66, v69, v66, s1
	v_pk_fma_f16 v67, v72, s36, v67 op_sel_hi:[1,0,1]
	v_readlane_b32 s59, v120, 52
	v_lshrrev_b32_e32 v72, 4, v64
	v_pk_fma_f16 v69, v76, s36, v71 op_sel_hi:[1,0,1]
	v_pk_fma_f16 v71, v77, s36, v73 op_sel_hi:[1,0,1]
	v_pk_fma_f16 v7, v66, s36, v7 op_sel_hi:[1,0,1]
	v_and_b32_e32 v66, 0x7070707, v64
	v_and_b32_e32 v72, 0x7070707, v72
	v_perm_b32 v66, s2, v205, v66
	v_perm_b32 v72, s2, v205, v72
	v_lshlrev_b32_e32 v73, 4, v64
	v_and_or_b32 v66, v73, s4, v66
	v_and_or_b32 v64, v64, s4, v72
	v_perm_b32 v73, v64, v66, s33
	v_perm_b32 v76, v64, v66, s0
	v_perm_b32 v72, v64, v66, s5
	v_perm_b32 v64, v64, v66, s1
	v_pk_fma_f16 v66, v73, s59, v68 op_sel_hi:[1,0,1]
	v_pk_fma_f16 v68, v76, s59, v70 op_sel_hi:[1,0,1]
	v_lshrrev_b32_e32 v70, 4, v65
	v_pk_fma_f16 v8, v64, s59, v8 op_sel_hi:[1,0,1]
	v_and_b32_e32 v64, 0x7070707, v65
	v_and_b32_e32 v70, 0x7070707, v70
	v_pk_fma_f16 v9, v72, s59, v9 op_sel_hi:[1,0,1]
	v_perm_b32 v64, s2, v205, v64
	v_perm_b32 v70, s2, v205, v70
	v_lshlrev_b32_e32 v72, 4, v65
	v_and_or_b32 v64, v72, s4, v64
	v_and_or_b32 v65, v65, s4, v70
	v_perm_b32 v70, v65, v64, s5
	v_perm_b32 v72, v65, v64, s33
	v_perm_b32 v73, v65, v64, s0
	v_perm_b32 v64, v65, v64, s1
	v_pk_fma_f16 v65, v70, s59, v67 op_sel_hi:[1,0,1]
	v_readlane_b32 s60, v120, 56
	v_lshrrev_b32_e32 v70, 4, v62
	v_pk_fma_f16 v67, v72, s59, v69 op_sel_hi:[1,0,1]
	v_pk_fma_f16 v69, v73, s59, v71 op_sel_hi:[1,0,1]
	v_pk_fma_f16 v7, v64, s59, v7 op_sel_hi:[1,0,1]
	v_and_b32_e32 v64, 0x7070707, v62
	v_and_b32_e32 v70, 0x7070707, v70
	v_perm_b32 v64, s2, v205, v64
	v_perm_b32 v70, s2, v205, v70
	v_lshlrev_b32_e32 v71, 4, v62
	v_and_or_b32 v64, v71, s4, v64
	v_and_or_b32 v62, v62, s4, v70
	v_perm_b32 v71, v62, v64, s33
	v_perm_b32 v72, v62, v64, s0
	v_perm_b32 v70, v62, v64, s5
	v_perm_b32 v62, v62, v64, s1
	v_pk_fma_f16 v64, v71, s60, v66 op_sel_hi:[1,0,1]
	v_pk_fma_f16 v66, v72, s60, v68 op_sel_hi:[1,0,1]
	v_lshrrev_b32_e32 v68, 4, v63
	v_pk_fma_f16 v8, v62, s60, v8 op_sel_hi:[1,0,1]
	v_and_b32_e32 v62, 0x7070707, v63
	v_and_b32_e32 v68, 0x7070707, v68
	v_pk_fma_f16 v9, v70, s60, v9 op_sel_hi:[1,0,1]
	v_perm_b32 v62, s2, v205, v62
	v_perm_b32 v68, s2, v205, v68
	v_lshlrev_b32_e32 v70, 4, v63
	v_and_or_b32 v62, v70, s4, v62
	v_and_or_b32 v63, v63, s4, v68
	v_perm_b32 v68, v63, v62, s5
	v_perm_b32 v70, v63, v62, s33
	v_perm_b32 v71, v63, v62, s0
	v_perm_b32 v62, v63, v62, s1
	v_pk_fma_f16 v7, v62, s60, v7 op_sel_hi:[1,0,1]
	v_readlane_b32 s36, v120, 60
	v_lshrrev_b32_e32 v62, 4, v50
	v_pk_fma_f16 v63, v68, s60, v65 op_sel_hi:[1,0,1]
	v_pk_fma_f16 v65, v70, s60, v67 op_sel_hi:[1,0,1]
	v_pk_fma_f16 v67, v71, s60, v69 op_sel_hi:[1,0,1]
	v_and_b32_e32 v15, 0x7070707, v50
	v_and_b32_e32 v62, 0x7070707, v62
	v_perm_b32 v15, s2, v205, v15
	v_perm_b32 v62, s2, v205, v62
	v_lshlrev_b32_e32 v68, 4, v50
	v_and_or_b32 v15, v68, s4, v15
	v_and_or_b32 v50, v50, s4, v62
	v_perm_b32 v62, v50, v15, s5
	v_perm_b32 v68, v50, v15, s33
	v_perm_b32 v69, v50, v15, s0
	v_perm_b32 v15, v50, v15, s1
	v_pk_fma_f16 v105, v62, s36, v9 op_sel_hi:[1,0,1]
	v_lshrrev_b32_e32 v9, 4, v51
	v_pk_fma_f16 v102, v15, s36, v8 op_sel_hi:[1,0,1]
	v_and_b32_e32 v8, 0x7070707, v51
	v_and_b32_e32 v9, 0x7070707, v9
	v_perm_b32 v8, s2, v205, v8
	v_perm_b32 v9, s2, v205, v9
	v_lshlrev_b32_e32 v15, 4, v51
	v_and_or_b32 v8, v15, s4, v8
	v_and_or_b32 v9, v51, s4, v9
	v_perm_b32 v15, v9, v8, s5
	v_perm_b32 v50, v9, v8, s33
	v_perm_b32 v51, v9, v8, s0
	v_perm_b32 v8, v9, v8, s1
	v_pk_fma_f16 v104, v68, s36, v64 op_sel_hi:[1,0,1]
	v_pk_fma_f16 v103, v69, s36, v66 op_sel_hi:[1,0,1]
	v_pk_fma_f16 v101, v15, s36, v63 op_sel_hi:[1,0,1]
	v_pk_fma_f16 v100, v50, s36, v65 op_sel_hi:[1,0,1]
	v_pk_fma_f16 v99, v51, s36, v67 op_sel_hi:[1,0,1]
	v_pk_fma_f16 v15, v8, s36, v7 op_sel_hi:[1,0,1]
	v_lshl_add_u64 v[6:7], v[18:19], 0, s[10:11]
	global_load_dwordx2 v[92:93], v[6:7], off
	v_lshl_add_u64 v[6:7], v[18:19], 0, s[12:13]
	global_load_dwordx2 v[90:91], v[6:7], off
	v_lshl_add_u64 v[6:7], v[18:19], 0, s[14:15]
	global_load_dwordx2 v[88:89], v[6:7], off
	v_lshl_add_u64 v[6:7], v[18:19], 0, s[16:17]
	global_load_dwordx2 v[86:87], v[6:7], off
	v_lshl_add_u64 v[6:7], v[18:19], 0, s[18:19]
	global_load_dwordx2 v[84:85], v[6:7], off
	v_lshl_add_u64 v[6:7], v[18:19], 0, s[20:21]
	global_load_dwordx2 v[82:83], v[6:7], off
	v_lshl_add_u64 v[6:7], v[18:19], 0, s[22:23]
	global_load_dwordx2 v[80:81], v[6:7], off
	v_lshl_add_u64 v[6:7], v[18:19], 0, s[24:25]
	global_load_dwordx2 v[78:79], v[6:7], off
	v_lshl_add_u64 v[6:7], v[18:19], 0, s[26:27]
	global_load_dwordx2 v[76:77], v[6:7], off
	v_lshl_add_u64 v[6:7], v[18:19], 0, s[28:29]
	v_readlane_b32 s50, v96, 13
	global_load_dwordx2 v[70:71], v[6:7], off
	v_lshl_add_u64 v[6:7], v[18:19], 0, s[30:31]
	global_load_dwordx2 v[40:41], v[40:41], off
	v_lshl_add_u64 v[52:53], v[16:17], 0, s[34:35]
	s_lshl_b64 s[38:39], s[38:39], 9
	s_ashr_i32 s51, s50, 31
	v_readlane_b32 s52, v96, 14
	global_load_dwordx2 v[66:67], v[6:7], off
	v_lshl_add_u64 v[6:7], v[18:19], 0, s[34:35]
	global_load_dwordx2 v[60:61], v[52:53], off
	global_load_dwordx2 v[72:73], v[6:7], off
	v_lshl_add_u64 v[52:53], v[16:17], 0, s[38:39]
	s_lshl_b64 s[50:51], s[50:51], 9
	s_ashr_i32 s53, s52, 31
	v_readlane_b32 s54, v96, 15
	v_lshl_add_u64 v[6:7], v[18:19], 0, s[38:39]
	global_load_dwordx2 v[58:59], v[52:53], off
	global_load_dwordx2 v[68:69], v[6:7], off
	v_lshl_add_u64 v[52:53], v[16:17], 0, s[50:51]
	s_lshl_b64 s[52:53], s[52:53], 9
	s_ashr_i32 s55, s54, 31
	v_lshl_add_u64 v[6:7], v[18:19], 0, s[50:51]
	global_load_dwordx2 v[56:57], v[52:53], off
	global_load_dwordx2 v[64:65], v[6:7], off
	v_lshl_add_u64 v[52:53], v[16:17], 0, s[52:53]
	s_lshl_b64 s[54:55], s[54:55], 9
	v_lshl_add_u64 v[6:7], v[18:19], 0, s[52:53]
	global_load_dwordx2 v[54:55], v[52:53], off
	global_load_dwordx2 v[62:63], v[6:7], off
	v_lshl_add_u64 v[52:53], v[16:17], 0, s[54:55]
	v_lshl_add_u64 v[6:7], v[18:19], 0, s[54:55]
	global_load_dwordx2 v[52:53], v[52:53], off
	s_cmpk_eq_i32 s56, 0x90
	global_load_dwordx2 v[50:51], v[6:7], off
	s_cbranch_scc0 .LBB0_770
	v_lshl_add_u64 v[94:95], v[2:3], 2, v[44:45]
	v_mov_b32_e32 v106, v208
	v_mov_b32_e32 v107, v209
	v_mov_b32_e32 v108, v210
	v_mov_b32_e32 v109, v211
	v_mov_b32_e32 v8, v212
	v_mov_b32_e32 v9, v213
	v_mov_b32_e32 v10, v214
	v_mov_b32_e32 v11, v215
	v_mov_b32_e32 v4, v216
	v_mov_b32_e32 v5, v217
	v_mov_b32_e32 v6, v218
	v_mov_b32_e32 v7, v219
	v_mov_b32_e32 v0, v220
	v_mov_b32_e32 v1, v221
	v_mov_b32_e32 v2, v222
	v_mov_b32_e32 v3, v223
	v_cvt_f32_f16_sdwa v13, v105 dst_sel:DWORD dst_unused:UNUSED_PAD src0_sel:WORD_1
	v_cvt_f32_f16_e32 v12, v105
	s_mov_b32 s12, 0x800000
	v_readlane_b32 s10, v255, 5
	v_readlane_b32 s11, v255, 6
	v_pk_add_f32 v[0:1], v[0:1], v[12:13]
	v_cvt_f32_f16_sdwa v13, v104 dst_sel:DWORD dst_unused:UNUSED_PAD src0_sel:WORD_1
	v_cvt_f32_f16_e32 v12, v104
	v_lshl_add_u64 v[48:49], v[48:49], 0, s[10:11]
	v_pk_add_f32 v[2:3], v[2:3], v[12:13]
	v_cvt_f32_f16_sdwa v13, v103 dst_sel:DWORD dst_unused:UNUSED_PAD src0_sel:WORD_1
	v_cvt_f32_f16_e32 v12, v103
	global_store_dwordx4 v[94:95], v[0:3], off
	v_pk_add_f32 v[4:5], v[4:5], v[12:13]
	v_cvt_f32_f16_sdwa v13, v102 dst_sel:DWORD dst_unused:UNUSED_PAD src0_sel:WORD_1
	v_cvt_f32_f16_e32 v12, v102
	v_mov_b32_e32 v102, v1
	v_mov_b32_e32 v103, v5
	v_pk_mul_f32 v[102:103], v[102:103], v[102:103]
	v_pk_add_f32 v[6:7], v[6:7], v[12:13]
	v_mov_b32_e32 v12, v0
	v_mov_b32_e32 v13, v4
	v_pk_fma_f32 v[12:13], v[12:13], v[12:13], v[102:103]
	v_mov_b32_e32 v102, v2
	v_mov_b32_e32 v103, v6
	v_pk_fma_f32 v[12:13], v[102:103], v[102:103], v[12:13]
	v_mov_b32_e32 v102, v3
	v_mov_b32_e32 v103, v7
	v_pk_fma_f32 v[102:103], v[102:103], v[102:103], v[12:13]
	v_cvt_f32_f16_sdwa v13, v101 dst_sel:DWORD dst_unused:UNUSED_PAD src0_sel:WORD_1
	v_cvt_f32_f16_e32 v12, v101
	v_cvt_f32_f16_sdwa v101, v15 dst_sel:DWORD dst_unused:UNUSED_PAD src0_sel:WORD_1
	global_store_dwordx4 v[94:95], v[4:7], off offset:16
	v_pk_add_f32 v[8:9], v[8:9], v[12:13]
	v_cvt_f32_f16_sdwa v13, v100 dst_sel:DWORD dst_unused:UNUSED_PAD src0_sel:WORD_1
	v_cvt_f32_f16_e32 v12, v100
	v_cvt_f32_f16_e32 v100, v15
	v_pk_add_f32 v[10:11], v[10:11], v[12:13]
	v_cvt_f32_f16_sdwa v13, v99 dst_sel:DWORD dst_unused:UNUSED_PAD src0_sel:WORD_1
	v_cvt_f32_f16_e32 v12, v99
	v_pk_add_f32 v[14:15], v[108:109], v[100:101]
	v_mov_b32_e32 v100, v9
	global_store_dwordx4 v[94:95], v[8:11], off offset:32
	v_pk_add_f32 v[12:13], v[106:107], v[12:13]
	global_store_dwordx4 v[94:95], v[12:15], off offset:48
	v_mov_b32_e32 v101, v13
	v_mov_b32_e32 v94, v8
	v_mov_b32_e32 v95, v12
	v_pk_mul_f32 v[100:101], v[100:101], v[100:101]
	v_add_f32_e32 v99, v102, v103
	v_pk_fma_f32 v[94:95], v[94:95], v[94:95], v[100:101]
	v_mov_b32_e32 v100, v10
	v_mov_b32_e32 v101, v14
	v_pk_fma_f32 v[94:95], v[100:101], v[100:101], v[94:95]
	v_mov_b32_e32 v100, v11
	v_mov_b32_e32 v101, v15
	v_pk_fma_f32 v[94:95], v[100:101], v[100:101], v[94:95]
	global_load_dwordx4 v[100:103], v[46:47], off offset:48
	global_load_dwordx4 v[104:107], v[46:47], off offset:32
	global_load_dwordx4 v[108:111], v[46:47], off offset:16
	global_load_dwordx4 v[112:115], v[46:47], off
	v_add_f32_e32 v94, v99, v94
	v_add_f32_e32 v94, v94, v95
	v_mov_b32_e32 v95, v94
	s_nop 1
	v_permlane32_swap_b32 v95, v94
	s_waitcnt lgkmcnt(0)
	v_add_f32_e32 v94, v94, v95
	v_mov_b32_e32 v95, v94
	s_nop 1
	v_permlane16_swap_b32 v95, v94
	s_waitcnt lgkmcnt(0)
	v_add_f32_e32 v94, v94, v95
	s_nop 1
	v_mov_b32_dpp v95, v94 row_ror:8 row_mask:0xf bank_mask:0xf
	s_waitcnt lgkmcnt(0)
	v_add_f32_e32 v94, v94, v95
	s_nop 1
	v_mov_b32_dpp v95, v94 row_half_mirror row_mask:0xf bank_mask:0xf
	s_nop 1
	v_mov_b32_dpp v95, v95 quad_perm:[3,2,1,0] row_mask:0xf bank_mask:0xf
	s_waitcnt lgkmcnt(0)
	v_add_f32_e32 v94, v94, v95
	s_nop 1
	v_mov_b32_dpp v95, v94 quad_perm:[2,3,0,1] row_mask:0xf bank_mask:0xf
	s_waitcnt lgkmcnt(0)
	v_add_f32_e32 v94, v94, v95
	s_nop 1
	v_mov_b32_dpp v95, v94 quad_perm:[1,0,3,2] row_mask:0xf bank_mask:0xf
	s_waitcnt lgkmcnt(0)
	v_add_f32_e32 v94, v94, v95
	v_fmamk_f32 v94, v94, 0x3a800000, v191
	v_cmp_gt_f32_e32 vcc, s12, v94
	v_mul_f32_e32 v95, 0x4b800000, v94
	s_nop 0
	v_cndmask_b32_e32 v94, v94, v95, vcc
	v_rsq_f32_e32 v94, v94
	s_nop 0
	v_mul_f32_e32 v95, 0x45800000, v94
	v_cndmask_b32_e32 v94, v94, v95, vcc
	v_pk_mul_f32 v[0:1], v[0:1], v[94:95] op_sel_hi:[1,0]
	v_pk_mul_f32 v[2:3], v[2:3], v[94:95] op_sel_hi:[1,0]
	s_waitcnt vmcnt(0)
	v_pk_mul_f32 v[0:1], v[112:113], v[0:1]
	v_pk_mul_f32 v[2:3], v[114:115], v[2:3]
	v_cvt_pk_bf16_f32 v0, v0, v1
	v_cvt_pk_bf16_f32 v1, v2, v3
	v_pk_mul_f32 v[2:3], v[4:5], v[94:95] op_sel_hi:[1,0]
	v_pk_mul_f32 v[4:5], v[6:7], v[94:95] op_sel_hi:[1,0]
	v_pk_mul_f32 v[2:3], v[108:109], v[2:3]
	v_pk_mul_f32 v[4:5], v[110:111], v[4:5]
	v_cvt_pk_bf16_f32 v2, v2, v3
	v_cvt_pk_bf16_f32 v3, v4, v5
	v_pk_mul_f32 v[4:5], v[8:9], v[94:95] op_sel_hi:[1,0]
	v_pk_mul_f32 v[6:7], v[10:11], v[94:95] op_sel_hi:[1,0]
	v_pk_mul_f32 v[4:5], v[104:105], v[4:5]
	v_pk_mul_f32 v[6:7], v[6:7], v[106:107]
	v_cvt_pk_bf16_f32 v4, v4, v5
	v_cvt_pk_bf16_f32 v5, v6, v7
	v_pk_mul_f32 v[6:7], v[12:13], v[94:95] op_sel_hi:[1,0]
	v_pk_mul_f32 v[8:9], v[14:15], v[94:95] op_sel_hi:[1,0]
	v_pk_mul_f32 v[6:7], v[6:7], v[100:101]
	v_pk_mul_f32 v[8:9], v[8:9], v[102:103]
	v_cvt_pk_bf16_f32 v6, v6, v7
	v_cvt_pk_bf16_f32 v7, v8, v9
	global_store_dwordx4 v[74:75], v[0:3], off
	global_store_dwordx4 v[74:75], v[4:7], off offset:16
	s_nop 0
	v_mov_b32_e32 v0, v98
	s_andn2_b64 exec, exec, s[8:9]
	s_cbranch_execnz .LBB0_769
